# back-edge rotation of the 10 GEMM K-loops: loop-carried scalar block and head address block moved in front of the back-edge barrier, exit path with its own barrier copy
# baseline (speedup 1.0000x reference)
; #define PG8_STAGE(bufoff, gbase, voff) do { _Pragma("unroll") for (int _i = 0; _i < 2; ++_i) \
;         __builtin_amdgcn_global_load_lds((const unsigned*)((const char*)(gbase) + (voff)[_i]), (PG8_LAS unsigned*)(lds + (bufoff) + ldsw + _i * 8192), 16, 0, 0); } while (0)
; #define PG8_LDA(dst, b, h) do { _Pragma("unroll") for (int m = 0; m < 4; ++m) _Pragma("unroll") for (int k = 0; k < 2; ++k) dst[m][k] = *(const PG8_LAS bf16x8*)(lds + PG8_SA(b, h) + aoff + m * 2048 + k * 1024); } while (0)
; #define PG8_LDB(dst, b, h) do { _Pragma("unroll") for (int n = 0; n < 2; ++n) _Pragma("unroll") for (int k = 0; k < 2; ++k) dst[n][k] = *(const PG8_LAS bf16x8*)(lds + PG8_SB(b, h) + boff + n * 2048 + k * 1024); } while (0)
; #define PG8_WAIT_V8_UNLESS_FIRST(t) asm volatile("s_cmp_eq_u32 %0, 0\n\ts_cbranch_scc1 .Lpg8skip%=\n\ts_waitcnt vmcnt(8)\n.Lpg8skip%=:" :: "s"(t) : "scc", "memory")
; #define PG8_WAIT_L(n) asm volatile("s_waitcnt lgkmcnt(" #n ")" ::: "memory")
; #define PG8_BAR __builtin_amdgcn_s_barrier()
; #define PG8_SCHED __builtin_amdgcn_sched_barrier(0)
; template <class Epi, class Sched, bool ALIGN_EPI = false, bool SP2 = false, bool FP8 = false, bool ABLK = false>
; __device__ __forceinline__ void gemm_phase(PG8_LAS unsigned char* lds, const Gemm g, const Sched& S, const Epi& E) {
;     ...
;         for (int t = 0; t < nt; t += 2) {
;             const bool last = (t == nt - 2);
;             const char* a1 = cA + (size_t)(t + 1) * kstepA;
;             const char* a2 = last ? nA : cA + (size_t)(t + 2) * kstepA; const char* b2 = last ? nB : cB + (size_t)(t + 2) * kstep;
;             const char* a3 = a2 + kstepA; const char* b3 = b2 + kstep;
;             if (last && has_next) S.a_ready(nxt);
;             if constexpr (SP2) {
;             PG8_LDB(B0, 0, 0); PG8_LDB(B1, 0, 1); PG8_SCHED; PG8_LDA(At, 0, 0); PG8_STAGE(PG8_SA(1, 1), a1 + hstepA, voffA);
;             PG8_WAIT_V8_UNLESS_FIRST(t); PG8_WAIT_L(0); PG8_BAR; PG8_MMA(0, 0, At, B0); PG8_MMA(0, 1, At, B1); PG8_BAR; PG8_SCHED;
.Lrot0_body:
	ds_read_b128 v[132:135], v144
	ds_read_b128 v[136:139], v144 offset:1024
	ds_read_b128 v[140:143], v144 offset:2048
	ds_read_b128 v[144:147], v144 offset:3072
	ds_read_b128 v[148:151], v162
	ds_read_b128 v[168:171], v162 offset:1024
	ds_read_b128 v[172:175], v162 offset:2048
	ds_read_b128 v[176:179], v162 offset:3072
	s_add_i32 m0, s18, 0xc000
	ds_read_b128 v[180:183], v166
	ds_read_b128 v[184:187], v166 offset:1024
	ds_read_b128 v[188:191], v166 offset:2048
	ds_read_b128 v[192:195], v166 offset:3072
	ds_read_b128 v[208:211], v166 offset:4096
	ds_read_b128 v[212:215], v166 offset:5120
	ds_read_b128 v[216:219], v166 offset:6144
	ds_read_b128 v[220:223], v166 offset:7168
	global_load_lds_dwordx4 v158, s[60:61]
	s_add_i32 m0, s18, 0xe000
	s_nop 0
	global_load_lds_dwordx4 v160, s[60:61]
	s_cmp_eq_u32 s74, 0
	s_cbranch_scc1 .Lpg8skip0
	s_waitcnt vmcnt(8)

; #define PG8_STAGE(bufoff, gbase, voff) do { _Pragma("unroll") for (int _i = 0; _i < 2; ++_i) \
;         __builtin_amdgcn_global_load_lds((const unsigned*)((const char*)(gbase) + (voff)[_i]), (PG8_LAS unsigned*)(lds + (bufoff) + ldsw + _i * 8192), 16, 0, 0); } while (0)
; #define PG8_LDA(dst, b, h) do { _Pragma("unroll") for (int m = 0; m < 4; ++m) _Pragma("unroll") for (int k = 0; k < 2; ++k) dst[m][k] = *(const PG8_LAS bf16x8*)(lds + PG8_SA(b, h) + aoff + m * 2048 + k * 1024); } while (0)
; #define PG8_LDB(dst, b, h) do { _Pragma("unroll") for (int n = 0; n < 2; ++n) _Pragma("unroll") for (int k = 0; k < 2; ++k) dst[n][k] = *(const PG8_LAS bf16x8*)(lds + PG8_SB(b, h) + boff + n * 2048 + k * 1024); } while (0)
; #define PG8_WAIT_V(n) asm volatile("s_waitcnt vmcnt(" #n ")" ::: "memory")
; #define PG8_WAIT_V8_UNLESS_FIRST(t) asm volatile("s_cmp_eq_u32 %0, 0\n\ts_cbranch_scc1 .Lpg8skip%=\n\ts_waitcnt vmcnt(8)\n.Lpg8skip%=:" :: "s"(t) : "scc", "memory")
; #define PG8_WAIT_L(n) asm volatile("s_waitcnt lgkmcnt(" #n ")" ::: "memory")
; #define PG8_BAR __builtin_amdgcn_s_barrier()
; #define PG8_SCHED __builtin_amdgcn_sched_barrier(0)
; template <class Epi, class Sched, bool ALIGN_EPI = false, bool SP2 = false, bool FP8 = false, bool ABLK = false>
; __device__ __forceinline__ void gemm_phase(PG8_LAS unsigned char* lds, const Gemm g, const Sched& S, const Epi& E) {
;     ...
;             PG8_WAIT_V8_UNLESS_FIRST(t); PG8_WAIT_L(0); PG8_BAR; PG8_MMA(1, 0, At, B0); PG8_MMA(1, 1, At, B1); PG8_BAR; PG8_SCHED;
;             PG8_LDB(B0, 1, 0); PG8_LDB(B1, 1, 1); PG8_SCHED; PG8_LDA(At, 1, 0); PG8_STAGE(PG8_SA(0, 1), a2 + hstepA, voffA);
;             PG8_WAIT_V(8); PG8_WAIT_L(0); PG8_BAR; PG8_MMA(0, 0, At, B0); PG8_MMA(0, 1, At, B1); PG8_BAR; PG8_SCHED;
.Lpg8skip1:
	s_waitcnt lgkmcnt(0)
	s_barrier
	s_setprio 1
	s_waitcnt lgkmcnt(0)
	v_mfma_f32_16x16x32_bf16 v[64:67], v[132:135], v[180:183], v[64:67]
	v_mfma_f32_16x16x32_bf16 v[60:63], v[140:143], v[180:183], v[60:63]
	v_mfma_f32_16x16x32_bf16 v[48:51], v[132:135], v[188:191], v[48:51]
	v_mfma_f32_16x16x32_bf16 v[44:47], v[140:143], v[188:191], v[44:47]
	v_mfma_f32_16x16x32_bf16 v[32:35], v[132:135], v[208:211], v[32:35]
	v_mfma_f32_16x16x32_bf16 v[28:31], v[140:143], v[208:211], v[28:31]
	v_mfma_f32_16x16x32_bf16 v[16:19], v[132:135], v[216:219], v[16:19]
	v_mfma_f32_16x16x32_bf16 v[12:15], v[140:143], v[216:219], v[12:15]
	v_mfma_f32_16x16x32_bf16 v[64:67], v[136:139], v[184:187], v[64:67]
	v_mfma_f32_16x16x32_bf16 v[60:63], v[144:147], v[184:187], v[60:63]
	v_mfma_f32_16x16x32_bf16 v[48:51], v[136:139], v[192:195], v[48:51]
	v_mfma_f32_16x16x32_bf16 v[44:47], v[144:147], v[192:195], v[44:47]
	v_mfma_f32_16x16x32_bf16 v[32:35], v[136:139], v[212:215], v[32:35]
	v_mfma_f32_16x16x32_bf16 v[28:31], v[144:147], v[212:215], v[28:31]
	v_mfma_f32_16x16x32_bf16 v[16:19], v[136:139], v[220:223], v[16:19]
	v_mfma_f32_16x16x32_bf16 v[12:15], v[144:147], v[220:223], v[12:15]
	s_setprio 0
	s_setprio 1
	v_mfma_f32_16x16x32_bf16 v[56:59], v[148:151], v[180:183], v[56:59]
	v_mfma_f32_16x16x32_bf16 v[52:55], v[172:175], v[180:183], v[52:55]
	v_mfma_f32_16x16x32_bf16 v[40:43], v[148:151], v[188:191], v[40:43]
	v_mfma_f32_16x16x32_bf16 v[36:39], v[172:175], v[188:191], v[36:39]
	v_mfma_f32_16x16x32_bf16 v[24:27], v[148:151], v[208:211], v[24:27]
	v_mfma_f32_16x16x32_bf16 v[20:23], v[172:175], v[208:211], v[20:23]
	v_mfma_f32_16x16x32_bf16 v[8:11], v[148:151], v[216:219], v[8:11]
	v_mfma_f32_16x16x32_bf16 v[4:7], v[172:175], v[216:219], v[4:7]
	v_mfma_f32_16x16x32_bf16 v[56:59], v[168:171], v[184:187], v[56:59]
	v_mfma_f32_16x16x32_bf16 v[52:55], v[176:179], v[184:187], v[52:55]
	v_mfma_f32_16x16x32_bf16 v[40:43], v[168:171], v[192:195], v[40:43]
	v_mfma_f32_16x16x32_bf16 v[36:39], v[176:179], v[192:195], v[36:39]
	v_mfma_f32_16x16x32_bf16 v[24:27], v[168:171], v[212:215], v[24:27]
	v_mfma_f32_16x16x32_bf16 v[20:23], v[176:179], v[212:215], v[20:23]
	v_mfma_f32_16x16x32_bf16 v[8:11], v[168:171], v[220:223], v[8:11]
	v_mfma_f32_16x16x32_bf16 v[4:7], v[176:179], v[220:223], v[4:7]
	s_setprio 0
	s_barrier
	s_add_i32 s75, 0, 0x18000
	s_add_i32 s76, 0, 0x1c000
	v_add_u32_e32 v144, s75, v165
	v_add_u32_e32 v167, s76, v165
	ds_read_b128 v[132:135], v144
	ds_read_b128 v[136:139], v144 offset:1024
	ds_read_b128 v[140:143], v144 offset:2048
	ds_read_b128 v[144:147], v144 offset:3072
	ds_read_b128 v[148:151], v167
	ds_read_b128 v[168:171], v167 offset:1024
	ds_read_b128 v[172:175], v167 offset:2048
	ds_read_b128 v[176:179], v167 offset:3072
	s_add_u32 s64, s64, 0x40000
	s_addc_u32 s65, s65, 0
	s_mov_b32 m0, s20
	ds_read_b128 v[180:183], v166 offset:32768
	ds_read_b128 v[184:187], v166 offset:33792
	ds_read_b128 v[188:191], v166 offset:34816
	ds_read_b128 v[192:195], v166 offset:35840
	ds_read_b128 v[208:211], v166 offset:36864
	ds_read_b128 v[212:215], v166 offset:37888
	ds_read_b128 v[216:219], v166 offset:38912
	ds_read_b128 v[220:223], v166 offset:39936
	global_load_lds_dwordx4 v156, s[64:65]
	s_mov_b32 m0, s21
	s_nop 0
	global_load_lds_dwordx4 v154, s[64:65]
	s_waitcnt vmcnt(8)
	s_waitcnt lgkmcnt(0)
	s_barrier
	s_setprio 1
	s_waitcnt lgkmcnt(0)
	v_mfma_f32_16x16x32_bf16 v[128:131], v[132:135], v[180:183], v[128:131]
	v_mfma_f32_16x16x32_bf16 v[124:127], v[140:143], v[180:183], v[124:127]
	v_mfma_f32_16x16x32_bf16 v[112:115], v[132:135], v[188:191], v[112:115]
	v_mfma_f32_16x16x32_bf16 v[108:111], v[140:143], v[188:191], v[108:111]
	v_mfma_f32_16x16x32_bf16 v[96:99], v[132:135], v[208:211], v[96:99]
	v_mfma_f32_16x16x32_bf16 v[92:95], v[140:143], v[208:211], v[92:95]
	v_mfma_f32_16x16x32_bf16 v[80:83], v[132:135], v[216:219], v[80:83]
	v_mfma_f32_16x16x32_bf16 v[76:79], v[140:143], v[216:219], v[76:79]
	v_mfma_f32_16x16x32_bf16 v[128:131], v[136:139], v[184:187], v[128:131]
	v_mfma_f32_16x16x32_bf16 v[124:127], v[144:147], v[184:187], v[124:127]
	v_mfma_f32_16x16x32_bf16 v[112:115], v[136:139], v[192:195], v[112:115]
	v_mfma_f32_16x16x32_bf16 v[108:111], v[144:147], v[192:195], v[108:111]
	v_mfma_f32_16x16x32_bf16 v[96:99], v[136:139], v[212:215], v[96:99]
	v_mfma_f32_16x16x32_bf16 v[92:95], v[144:147], v[212:215], v[92:95]
	v_mfma_f32_16x16x32_bf16 v[80:83], v[136:139], v[220:223], v[80:83]
	v_mfma_f32_16x16x32_bf16 v[76:79], v[144:147], v[220:223], v[76:79]
	s_setprio 0
	s_setprio 1
	v_mfma_f32_16x16x32_bf16 v[120:123], v[148:151], v[180:183], v[120:123]
	v_mfma_f32_16x16x32_bf16 v[116:119], v[172:175], v[180:183], v[116:119]
	v_mfma_f32_16x16x32_bf16 v[104:107], v[148:151], v[188:191], v[104:107]
	v_mfma_f32_16x16x32_bf16 v[100:103], v[172:175], v[188:191], v[100:103]
	v_mfma_f32_16x16x32_bf16 v[88:91], v[148:151], v[208:211], v[88:91]
	v_mfma_f32_16x16x32_bf16 v[84:87], v[172:175], v[208:211], v[84:87]
	v_mfma_f32_16x16x32_bf16 v[72:75], v[148:151], v[216:219], v[72:75]
	v_mfma_f32_16x16x32_bf16 v[68:71], v[172:175], v[216:219], v[68:71]
	v_mfma_f32_16x16x32_bf16 v[120:123], v[168:171], v[184:187], v[120:123]
	v_mfma_f32_16x16x32_bf16 v[116:119], v[176:179], v[184:187], v[116:119]
	v_mfma_f32_16x16x32_bf16 v[104:107], v[168:171], v[192:195], v[104:107]
	v_mfma_f32_16x16x32_bf16 v[100:103], v[176:179], v[192:195], v[100:103]
	v_mfma_f32_16x16x32_bf16 v[88:91], v[168:171], v[212:215], v[88:91]
	v_mfma_f32_16x16x32_bf16 v[84:87], v[176:179], v[212:215], v[84:87]
	v_mfma_f32_16x16x32_bf16 v[72:75], v[168:171], v[220:223], v[72:75]
	v_mfma_f32_16x16x32_bf16 v[68:71], v[176:179], v[220:223], v[68:71]
	s_setprio 0
	s_barrier
; #define PG8_STAGE(bufoff, gbase, voff) do { _Pragma("unroll") for (int _i = 0; _i < 2; ++_i) \
;         __builtin_amdgcn_global_load_lds((const unsigned*)((const char*)(gbase) + (voff)[_i]), (PG8_LAS unsigned*)(lds + (bufoff) + ldsw + _i * 8192), 16, 0, 0); } while (0)
; #define PG8_WAIT_V(n) asm volatile("s_waitcnt vmcnt(" #n ")" ::: "memory")
; #define PG8_WAIT_L(n) asm volatile("s_waitcnt lgkmcnt(" #n ")" ::: "memory")
; #define PG8_BAR __builtin_amdgcn_s_barrier()
; template <class Epi, class Sched, bool ALIGN_EPI = false, bool SP2 = false, bool FP8 = false, bool ABLK = false>
; __device__ __forceinline__ void gemm_phase(PG8_LAS unsigned char* lds, const Gemm g, const Sched& S, const Epi& E) {
;     ...
;         for (int t = 0; t < nt; t += 2) {
;             const bool last = (t == nt - 2);
;             const char* a1 = cA + (size_t)(t + 1) * kstepA;
;             const char* a2 = last ? nA : cA + (size_t)(t + 2) * kstepA; const char* b2 = last ? nB : cB + (size_t)(t + 2) * kstep;
;             const char* a3 = a2 + kstepA; const char* b3 = b2 + kstep;
;             if (last && has_next) S.a_ready(nxt);
;             if constexpr (SP2) {
;             PG8_LDB(B0, 0, 0); PG8_LDB(B1, 0, 1); PG8_SCHED; PG8_LDA(At, 0, 0); PG8_STAGE(PG8_SA(1, 1), a1 + hstepA, voffA);
;             PG8_WAIT_V8_UNLESS_FIRST(t); PG8_WAIT_L(0); PG8_BAR; PG8_MMA(0, 0, At, B0); PG8_MMA(0, 1, At, B1); PG8_BAR; PG8_SCHED;
;             PG8_LDA(At, 0, 1); PG8_STAGE(PG8_SB(0, 0), b2, voffB); PG8_STAGE(PG8_SB(0, 1), b2 + hstep, voffB); PG8_STAGE(PG8_SA(0, 0), a2, voffA);
;             PG8_WAIT_V8_UNLESS_FIRST(t); PG8_WAIT_L(0); PG8_BAR; PG8_MMA(1, 0, At, B0); PG8_MMA(1, 1, At, B1); PG8_BAR; PG8_SCHED;
;             PG8_LDB(B0, 1, 0); PG8_LDB(B1, 1, 1); PG8_SCHED; PG8_LDA(At, 1, 0); PG8_STAGE(PG8_SA(0, 1), a2 + hstepA, voffA);
;             PG8_WAIT_V(8); PG8_WAIT_L(0); PG8_BAR; PG8_MMA(0, 0, At, B0); PG8_MMA(0, 1, At, B1); PG8_BAR; PG8_SCHED;
;             PG8_LDA(At, 1, 1); PG8_STAGE(PG8_SB(1, 0), b3, voffB); PG8_STAGE(PG8_SB(1, 1), b3 + hstep, voffB); PG8_STAGE(PG8_SA(1, 0), a3, voffA);
;             PG8_WAIT_V(8); PG8_WAIT_L(0); PG8_BAR; PG8_MMA(1, 0, At, B0); PG8_MMA(1, 1, At, B1); PG8_BAR; PG8_SCHED;
;     ...
;         if constexpr (SP2) PG8_WAIT_V(0);
;         if constexpr (FP8) asm volatile("s_nop 15\n\ts_nop 15" ::: "memory");
;         if constexpr (ALIGN_EPI) { if (wr == 0) PG8_BAR; }
	s_add_i32 s64, s75, s17
	v_lshl_add_u64 v[162:163], v[162:163], 0, s[34:35]
	s_mov_b32 m0, s64
	ds_read_b128 v[180:183], v166 offset:49152
	ds_read_b128 v[184:187], v166 offset:50176
	ds_read_b128 v[188:191], v166 offset:51200
	ds_read_b128 v[192:195], v166 offset:52224
	ds_read_b128 v[208:211], v166 offset:53248
	ds_read_b128 v[212:215], v166 offset:54272
	ds_read_b128 v[216:219], v166 offset:55296
	ds_read_b128 v[220:223], v166 offset:56320
	global_load_lds_dwordx4 v[162:163], off
	s_add_i32 m0, s64, 0x2000
	s_add_u32 s62, s62, 0x40080
	v_lshl_add_u64 v[162:163], v[224:225], 0, s[34:35]
	s_addc_u32 s63, s63, 0
	s_add_i32 s64, s76, s17
	global_load_lds_dwordx4 v[162:163], off
	s_mov_b32 m0, s64
	s_nop 0
	global_load_lds_dwordx4 v2, s[62:63]
	s_add_i32 m0, s64, 0x2000
	s_nop 0
	global_load_lds_dwordx4 v152, s[62:63]
	v_lshl_add_u64 v[162:163], v[228:229], 0, s[34:35]
	s_mov_b32 m0, s66
	s_nop 0
	global_load_lds_dwordx4 v[162:163], off
	v_lshl_add_u64 v[162:163], v[230:231], 0, s[34:35]
	s_mov_b32 m0, s67
	s_nop 0
	global_load_lds_dwordx4 v[162:163], off
	s_waitcnt vmcnt(8)
	s_waitcnt lgkmcnt(0)
	s_barrier
	s_setprio 1
	s_waitcnt lgkmcnt(0)
	v_mfma_f32_16x16x32_bf16 v[64:67], v[132:135], v[180:183], v[64:67]
	v_mfma_f32_16x16x32_bf16 v[60:63], v[140:143], v[180:183], v[60:63]
	v_mfma_f32_16x16x32_bf16 v[48:51], v[132:135], v[188:191], v[48:51]
	v_mfma_f32_16x16x32_bf16 v[44:47], v[140:143], v[188:191], v[44:47]
	v_mfma_f32_16x16x32_bf16 v[32:35], v[132:135], v[208:211], v[32:35]
	v_mfma_f32_16x16x32_bf16 v[28:31], v[140:143], v[208:211], v[28:31]
	v_mfma_f32_16x16x32_bf16 v[16:19], v[132:135], v[216:219], v[16:19]
	v_mfma_f32_16x16x32_bf16 v[12:15], v[140:143], v[216:219], v[12:15]
	v_mfma_f32_16x16x32_bf16 v[64:67], v[136:139], v[184:187], v[64:67]
	v_mfma_f32_16x16x32_bf16 v[60:63], v[144:147], v[184:187], v[60:63]
	v_mfma_f32_16x16x32_bf16 v[48:51], v[136:139], v[192:195], v[48:51]
	v_mfma_f32_16x16x32_bf16 v[44:47], v[144:147], v[192:195], v[44:47]
	v_mfma_f32_16x16x32_bf16 v[32:35], v[136:139], v[212:215], v[32:35]
	v_mfma_f32_16x16x32_bf16 v[28:31], v[144:147], v[212:215], v[28:31]
	v_mfma_f32_16x16x32_bf16 v[16:19], v[136:139], v[220:223], v[16:19]
	v_mfma_f32_16x16x32_bf16 v[12:15], v[144:147], v[220:223], v[12:15]
	s_setprio 0
	s_setprio 1
	v_mfma_f32_16x16x32_bf16 v[56:59], v[148:151], v[180:183], v[56:59]
	v_mfma_f32_16x16x32_bf16 v[52:55], v[172:175], v[180:183], v[52:55]
	v_mfma_f32_16x16x32_bf16 v[40:43], v[148:151], v[188:191], v[40:43]
	v_mfma_f32_16x16x32_bf16 v[36:39], v[172:175], v[188:191], v[36:39]
	v_mfma_f32_16x16x32_bf16 v[24:27], v[148:151], v[208:211], v[24:27]
	v_mfma_f32_16x16x32_bf16 v[20:23], v[172:175], v[208:211], v[20:23]
	v_mfma_f32_16x16x32_bf16 v[8:11], v[148:151], v[216:219], v[8:11]
	v_mfma_f32_16x16x32_bf16 v[4:7], v[172:175], v[216:219], v[4:7]
	v_mfma_f32_16x16x32_bf16 v[56:59], v[168:171], v[184:187], v[56:59]
	v_mfma_f32_16x16x32_bf16 v[52:55], v[176:179], v[184:187], v[52:55]
	v_mfma_f32_16x16x32_bf16 v[40:43], v[168:171], v[192:195], v[40:43]
	v_mfma_f32_16x16x32_bf16 v[36:39], v[176:179], v[192:195], v[36:39]
	v_mfma_f32_16x16x32_bf16 v[24:27], v[168:171], v[212:215], v[24:27]
	v_mfma_f32_16x16x32_bf16 v[20:23], v[176:179], v[212:215], v[20:23]
	v_mfma_f32_16x16x32_bf16 v[8:11], v[168:171], v[220:223], v[8:11]
	v_mfma_f32_16x16x32_bf16 v[4:7], v[176:179], v[220:223], v[4:7]
	s_setprio 0
	s_add_u32 s60, s60, 0x100
	s_addc_u32 s61, s61, 0
	s_add_u32 s72, s72, 0x100
	s_addc_u32 s73, s73, 0
	s_cmp_gt_u32 s74, 13
	s_mov_b32 s62, s74
	s_cbranch_scc1 .Lrot0_exit
	s_add_i32 s74, s62, 2
	s_add_u32 s63, s60, 0xfffc0080
	s_addc_u32 s64, s61, -1
	s_add_i32 s75, 0, 0x10000
	s_cmp_eq_u32 s62, 12
	s_cselect_b32 s65, s4, s64
	s_cselect_b32 s64, s5, s63
	s_cselect_b32 s63, s53, s73
	s_cselect_b32 s62, s55, s72
	s_add_i32 s81, 0, 0x14000
	v_add_u32_e32 v144, s75, v165
	v_add_u32_e32 v162, s81, v165
	s_barrier
	s_branch .Lrot0_body
.Lrot0_exit:
	s_barrier
	s_waitcnt vmcnt(0)
	s_and_b64 vcc, exec, s[50:51]
	s_cbranch_vccz .LBB0_434
	s_barrier

; #define PG8_STAGE(bufoff, gbase, voff) do { _Pragma("unroll") for (int _i = 0; _i < 2; ++_i) \
;         __builtin_amdgcn_global_load_lds((const unsigned*)((const char*)(gbase) + (voff)[_i]), (PG8_LAS unsigned*)(lds + (bufoff) + ldsw + _i * 8192), 16, 0, 0); } while (0)
; #define PG8_LDA(dst, b, h) do { _Pragma("unroll") for (int m = 0; m < 4; ++m) _Pragma("unroll") for (int k = 0; k < 2; ++k) dst[m][k] = *(const PG8_LAS bf16x8*)(lds + PG8_SA(b, h) + aoff + m * 2048 + k * 1024); } while (0)
; #define PG8_LDB(dst, b, h) do { _Pragma("unroll") for (int n = 0; n < 2; ++n) _Pragma("unroll") for (int k = 0; k < 2; ++k) dst[n][k] = *(const PG8_LAS bf16x8*)(lds + PG8_SB(b, h) + boff + n * 2048 + k * 1024); } while (0)
; #define PG8_WAIT_V8_UNLESS_FIRST(t) asm volatile("s_cmp_eq_u32 %0, 0\n\ts_cbranch_scc1 .Lpg8skip%=\n\ts_waitcnt vmcnt(8)\n.Lpg8skip%=:" :: "s"(t) : "scc", "memory")
; #define PG8_WAIT_L(n) asm volatile("s_waitcnt lgkmcnt(" #n ")" ::: "memory")
; #define PG8_BAR __builtin_amdgcn_s_barrier()
; #define PG8_SCHED __builtin_amdgcn_sched_barrier(0)
; template <class Epi, class Sched, bool ALIGN_EPI = false, bool SP2 = false, bool FP8 = false, bool ABLK = false>
; __device__ __forceinline__ void gemm_phase(PG8_LAS unsigned char* lds, const Gemm g, const Sched& S, const Epi& E) {
;     ...
;             PG8_LDB(B0, 0, 0); PG8_LDB(B1, 0, 1); PG8_SCHED; PG8_LDA(At, 0, 0); PG8_STAGE(PG8_SA(1, 1), a1 + hstepA, voffA);
;             PG8_WAIT_V8_UNLESS_FIRST(t); PG8_WAIT_L(0); PG8_BAR; PG8_MMA(0, 0, At, B0); PG8_MMA(0, 1, At, B1); PG8_BAR; PG8_SCHED;
.Lrot1_body:
	ds_read_b128 v[28:31], v4
	ds_read_b128 v[32:35], v4 offset:1024
	ds_read_b128 v[20:23], v4 offset:2048
	ds_read_b128 v[24:27], v4 offset:3072
	ds_read_b128 v[12:15], v8
	ds_read_b128 v[16:19], v8 offset:1024
	s_waitcnt lgkmcnt(0)
	ds_read_b128 v[4:7], v8 offset:2048
	ds_read_b128 v[8:11], v8 offset:3072
	v_lshl_add_u64 v[178:179], v[174:175], 0, s[56:57]
	s_add_i32 m0, s18, 0xc000
	ds_read_b128 v[186:189], v184
	ds_read_b128 v[190:193], v184 offset:1024
	ds_read_b128 v[208:211], v184 offset:2048
	ds_read_b128 v[212:215], v184 offset:3072
	ds_read_b128 v[216:219], v184 offset:4096
	ds_read_b128 v[220:223], v184 offset:5120
	ds_read_b128 v[228:231], v184 offset:6144
	ds_read_b128 v[232:235], v184 offset:7168
	global_load_lds_dwordx4 v[178:179], off
	v_lshl_add_u64 v[178:179], v[176:177], 0, s[56:57]
	s_add_i32 m0, s18, 0xe000
	s_nop 0
	global_load_lds_dwordx4 v[178:179], off
	s_cmp_eq_u32 s71, 0
	s_cbranch_scc1 .Lpg8skip2
	s_waitcnt vmcnt(8)

; #define PG8_STAGE(bufoff, gbase, voff) do { _Pragma("unroll") for (int _i = 0; _i < 2; ++_i) \
;         __builtin_amdgcn_global_load_lds((const unsigned*)((const char*)(gbase) + (voff)[_i]), (PG8_LAS unsigned*)(lds + (bufoff) + ldsw + _i * 8192), 16, 0, 0); } while (0)
; #define PG8_LDA(dst, b, h) do { _Pragma("unroll") for (int m = 0; m < 4; ++m) _Pragma("unroll") for (int k = 0; k < 2; ++k) dst[m][k] = *(const PG8_LAS bf16x8*)(lds + PG8_SA(b, h) + aoff + m * 2048 + k * 1024); } while (0)
; #define PG8_LDB(dst, b, h) do { _Pragma("unroll") for (int n = 0; n < 2; ++n) _Pragma("unroll") for (int k = 0; k < 2; ++k) dst[n][k] = *(const PG8_LAS bf16x8*)(lds + PG8_SB(b, h) + boff + n * 2048 + k * 1024); } while (0)
; #define PG8_WAIT_V(n) asm volatile("s_waitcnt vmcnt(" #n ")" ::: "memory")
; #define PG8_WAIT_V8_UNLESS_FIRST(t) asm volatile("s_cmp_eq_u32 %0, 0\n\ts_cbranch_scc1 .Lpg8skip%=\n\ts_waitcnt vmcnt(8)\n.Lpg8skip%=:" :: "s"(t) : "scc", "memory")
; #define PG8_WAIT_L(n) asm volatile("s_waitcnt lgkmcnt(" #n ")" ::: "memory")
; #define PG8_BAR __builtin_amdgcn_s_barrier()
; #define PG8_SCHED __builtin_amdgcn_sched_barrier(0)
; template <class Epi, class Sched, bool ALIGN_EPI = false, bool SP2 = false, bool FP8 = false, bool ABLK = false>
; __device__ __forceinline__ void gemm_phase(PG8_LAS unsigned char* lds, const Gemm g, const Sched& S, const Epi& E) {
;     ...
;             PG8_WAIT_V8_UNLESS_FIRST(t); PG8_WAIT_L(0); PG8_BAR; PG8_MMA(1, 0, At, B0); PG8_MMA(1, 1, At, B1); PG8_BAR; PG8_SCHED;
;             PG8_LDB(B0, 1, 0); PG8_LDB(B1, 1, 1); PG8_SCHED; PG8_LDA(At, 1, 0); PG8_STAGE(PG8_SA(0, 1), a2 + hstepA, voffA);
;             PG8_WAIT_V(8); PG8_WAIT_L(0); PG8_BAR; PG8_MMA(0, 0, At, B0); PG8_MMA(0, 1, At, B1); PG8_BAR; PG8_SCHED;
.Lpg8skip3:
	s_waitcnt lgkmcnt(0)
	s_barrier
	s_setprio 1
	s_waitcnt lgkmcnt(0)
	v_mfma_scale_f32_16x16x128_f8f6f4 v[96:99], v[28:35], v[186:193], v[96:99], v245, v245 op_sel_hi:[0,0,0]
	v_mfma_scale_f32_16x16x128_f8f6f4 v[92:95], v[20:27], v[186:193], v[92:95], v245, v245 op_sel_hi:[0,0,0]
	v_mfma_scale_f32_16x16x128_f8f6f4 v[80:83], v[28:35], v[208:215], v[80:83], v245, v245 op_sel_hi:[0,0,0]
	v_mfma_scale_f32_16x16x128_f8f6f4 v[76:79], v[20:27], v[208:215], v[76:79], v245, v245 op_sel_hi:[0,0,0]
	v_mfma_scale_f32_16x16x128_f8f6f4 v[64:67], v[28:35], v[216:223], v[64:67], v245, v245 op_sel_hi:[0,0,0]
	v_mfma_scale_f32_16x16x128_f8f6f4 v[60:63], v[20:27], v[216:223], v[60:63], v245, v245 op_sel_hi:[0,0,0]
	v_mfma_scale_f32_16x16x128_f8f6f4 v[48:51], v[28:35], v[228:235], v[48:51], v245, v245 op_sel_hi:[0,0,0]
	v_mfma_scale_f32_16x16x128_f8f6f4 v[44:47], v[20:27], v[228:235], v[44:47], v245, v245 op_sel_hi:[0,0,0]
	s_setprio 0
	s_setprio 1
	v_mfma_scale_f32_16x16x128_f8f6f4 v[88:91], v[12:19], v[186:193], v[88:91], v245, v245 op_sel_hi:[0,0,0]
	v_mfma_scale_f32_16x16x128_f8f6f4 v[84:87], v[4:11], v[186:193], v[84:87], v245, v245 op_sel_hi:[0,0,0]
	v_mfma_scale_f32_16x16x128_f8f6f4 v[72:75], v[12:19], v[208:215], v[72:75], v245, v245 op_sel_hi:[0,0,0]
	v_mfma_scale_f32_16x16x128_f8f6f4 v[68:71], v[4:11], v[208:215], v[68:71], v245, v245 op_sel_hi:[0,0,0]
	v_mfma_scale_f32_16x16x128_f8f6f4 v[56:59], v[12:19], v[216:223], v[56:59], v245, v245 op_sel_hi:[0,0,0]
	v_mfma_scale_f32_16x16x128_f8f6f4 v[52:55], v[4:11], v[216:223], v[52:55], v245, v245 op_sel_hi:[0,0,0]
	v_mfma_scale_f32_16x16x128_f8f6f4 v[40:43], v[12:19], v[228:235], v[40:43], v245, v245 op_sel_hi:[0,0,0]
	v_mfma_scale_f32_16x16x128_f8f6f4 v[36:39], v[4:11], v[228:235], v[36:39], v245, v245 op_sel_hi:[0,0,0]
	s_setprio 0
	s_barrier
	s_add_i32 s62, 0, 0x18000
	s_add_i32 s63, 0, 0x1c000
	v_add_u32_e32 v16, s62, v183
	v_add_u32_e32 v32, s63, v183
	ds_read_b128 v[4:7], v16
	ds_read_b128 v[8:11], v16 offset:1024
	ds_read_b128 v[12:15], v16 offset:2048
	ds_read_b128 v[16:19], v16 offset:3072
	ds_read_b128 v[20:23], v32
	ds_read_b128 v[24:27], v32 offset:1024
	ds_read_b128 v[28:31], v32 offset:2048
	ds_read_b128 v[32:35], v32 offset:3072
	s_mov_b32 m0, s20
	v_lshl_add_u64 v[194:195], v[194:195], 0, s[24:25]
	ds_read_b128 v[186:189], v184 offset:32768
	ds_read_b128 v[190:193], v184 offset:33792
	ds_read_b128 v[208:211], v184 offset:34816
	ds_read_b128 v[212:215], v184 offset:35840
	ds_read_b128 v[216:219], v184 offset:36864
	ds_read_b128 v[220:223], v184 offset:37888
	ds_read_b128 v[228:231], v184 offset:38912
	ds_read_b128 v[232:235], v184 offset:39936
	global_load_lds_dwordx4 v[194:195], off
	v_lshl_add_u64 v[194:195], v[224:225], 0, s[24:25]
	s_mov_b32 m0, s21
	s_nop 0
	global_load_lds_dwordx4 v[194:195], off
	s_waitcnt vmcnt(8)
	s_waitcnt lgkmcnt(0)
	s_barrier
	s_setprio 1
	s_waitcnt lgkmcnt(0)
	v_mfma_scale_f32_16x16x128_f8f6f4 v[160:163], v[4:11], v[186:193], v[160:163], v245, v245 op_sel_hi:[0,0,0]
	v_mfma_scale_f32_16x16x128_f8f6f4 v[156:159], v[12:19], v[186:193], v[156:159], v245, v245 op_sel_hi:[0,0,0]
	v_mfma_scale_f32_16x16x128_f8f6f4 v[144:147], v[4:11], v[208:215], v[144:147], v245, v245 op_sel_hi:[0,0,0]
	v_mfma_scale_f32_16x16x128_f8f6f4 v[140:143], v[12:19], v[208:215], v[140:143], v245, v245 op_sel_hi:[0,0,0]
	v_mfma_scale_f32_16x16x128_f8f6f4 v[128:131], v[4:11], v[216:223], v[128:131], v245, v245 op_sel_hi:[0,0,0]
	v_mfma_scale_f32_16x16x128_f8f6f4 v[124:127], v[12:19], v[216:223], v[124:127], v245, v245 op_sel_hi:[0,0,0]
	v_mfma_scale_f32_16x16x128_f8f6f4 v[112:115], v[4:11], v[228:235], v[112:115], v245, v245 op_sel_hi:[0,0,0]
	v_mfma_scale_f32_16x16x128_f8f6f4 v[108:111], v[12:19], v[228:235], v[108:111], v245, v245 op_sel_hi:[0,0,0]
	s_setprio 0
	s_setprio 1
	v_mfma_scale_f32_16x16x128_f8f6f4 v[152:155], v[20:27], v[186:193], v[152:155], v245, v245 op_sel_hi:[0,0,0]
	v_mfma_scale_f32_16x16x128_f8f6f4 v[148:151], v[28:35], v[186:193], v[148:151], v245, v245 op_sel_hi:[0,0,0]
	v_mfma_scale_f32_16x16x128_f8f6f4 v[136:139], v[20:27], v[208:215], v[136:139], v245, v245 op_sel_hi:[0,0,0]
	v_mfma_scale_f32_16x16x128_f8f6f4 v[132:135], v[28:35], v[208:215], v[132:135], v245, v245 op_sel_hi:[0,0,0]
	v_mfma_scale_f32_16x16x128_f8f6f4 v[120:123], v[20:27], v[216:223], v[120:123], v245, v245 op_sel_hi:[0,0,0]
	v_mfma_scale_f32_16x16x128_f8f6f4 v[116:119], v[28:35], v[216:223], v[116:119], v245, v245 op_sel_hi:[0,0,0]
	v_mfma_scale_f32_16x16x128_f8f6f4 v[104:107], v[20:27], v[228:235], v[104:107], v245, v245 op_sel_hi:[0,0,0]
	v_mfma_scale_f32_16x16x128_f8f6f4 v[100:103], v[28:35], v[228:235], v[100:103], v245, v245 op_sel_hi:[0,0,0]
	s_setprio 0
	s_barrier
; #define PG8_STAGE(bufoff, gbase, voff) do { _Pragma("unroll") for (int _i = 0; _i < 2; ++_i) \
;         __builtin_amdgcn_global_load_lds((const unsigned*)((const char*)(gbase) + (voff)[_i]), (PG8_LAS unsigned*)(lds + (bufoff) + ldsw + _i * 8192), 16, 0, 0); } while (0)
; #define PG8_WAIT_V(n) asm volatile("s_waitcnt vmcnt(" #n ")" ::: "memory")
; #define PG8_WAIT_L(n) asm volatile("s_waitcnt lgkmcnt(" #n ")" ::: "memory")
; #define PG8_BAR __builtin_amdgcn_s_barrier()
; template <class Epi, class Sched, bool ALIGN_EPI = false, bool SP2 = false, bool FP8 = false, bool ABLK = false>
; __device__ __forceinline__ void gemm_phase(PG8_LAS unsigned char* lds, const Gemm g, const Sched& S, const Epi& E) {
;     ...
;         for (int t = 0; t < nt; t += 2) {
;             const bool last = (t == nt - 2);
;             const char* a1 = cA + (size_t)(t + 1) * kstepA;
;             const char* a2 = last ? nA : cA + (size_t)(t + 2) * kstepA; const char* b2 = last ? nB : cB + (size_t)(t + 2) * kstep;
;             const char* a3 = a2 + kstepA; const char* b3 = b2 + kstep;
;             if (last && has_next) S.a_ready(nxt);
;             if constexpr (SP2) {
;             PG8_LDB(B0, 0, 0); PG8_LDB(B1, 0, 1); PG8_SCHED; PG8_LDA(At, 0, 0); PG8_STAGE(PG8_SA(1, 1), a1 + hstepA, voffA);
;             PG8_WAIT_V8_UNLESS_FIRST(t); PG8_WAIT_L(0); PG8_BAR; PG8_MMA(0, 0, At, B0); PG8_MMA(0, 1, At, B1); PG8_BAR; PG8_SCHED;
;             PG8_LDA(At, 0, 1); PG8_STAGE(PG8_SB(0, 0), b2, voffB); PG8_STAGE(PG8_SB(0, 1), b2 + hstep, voffB); PG8_STAGE(PG8_SA(0, 0), a2, voffA);
;             PG8_WAIT_V8_UNLESS_FIRST(t); PG8_WAIT_L(0); PG8_BAR; PG8_MMA(1, 0, At, B0); PG8_MMA(1, 1, At, B1); PG8_BAR; PG8_SCHED;
;             PG8_LDB(B0, 1, 0); PG8_LDB(B1, 1, 1); PG8_SCHED; PG8_LDA(At, 1, 0); PG8_STAGE(PG8_SA(0, 1), a2 + hstepA, voffA);
;             PG8_WAIT_V(8); PG8_WAIT_L(0); PG8_BAR; PG8_MMA(0, 0, At, B0); PG8_MMA(0, 1, At, B1); PG8_BAR; PG8_SCHED;
;             PG8_LDA(At, 1, 1); PG8_STAGE(PG8_SB(1, 0), b3, voffB); PG8_STAGE(PG8_SB(1, 1), b3 + hstep, voffB); PG8_STAGE(PG8_SA(1, 0), a3, voffA);
;             PG8_WAIT_V(8); PG8_WAIT_L(0); PG8_BAR; PG8_MMA(1, 0, At, B0); PG8_MMA(1, 1, At, B1); PG8_BAR; PG8_SCHED;
;     ...
;         if constexpr (SP2) PG8_WAIT_V(0);
;         if constexpr (FP8) asm volatile("s_nop 15\n\ts_nop 15" ::: "memory");
;         if constexpr (ALIGN_EPI) { if (wr == 0) PG8_BAR; }
	s_add_i32 s62, s62, s17
	v_lshl_add_u64 v[178:179], v[178:179], 0, s[34:35]
	s_mov_b32 m0, s62
	ds_read_b128 v[186:189], v184 offset:49152
	ds_read_b128 v[190:193], v184 offset:50176
	ds_read_b128 v[208:211], v184 offset:51200
	ds_read_b128 v[212:215], v184 offset:52224
	ds_read_b128 v[216:219], v184 offset:53248
	ds_read_b128 v[220:223], v184 offset:54272
	ds_read_b128 v[228:231], v184 offset:55296
	ds_read_b128 v[232:235], v184 offset:56320
	global_load_lds_dwordx4 v[178:179], off
	s_add_i32 m0, s62, 0x2000
	s_add_u32 s60, s60, 0x58080
	v_lshl_add_u64 v[178:179], v[180:181], 0, s[34:35]
	s_addc_u32 s61, s61, 0
	s_add_i32 s62, s63, s17
	global_load_lds_dwordx4 v[178:179], off
	s_mov_b32 m0, s62
	s_nop 0
	global_load_lds_dwordx4 v2, s[60:61]
	s_add_i32 m0, s62, 0x2000
	s_nop 0
	global_load_lds_dwordx4 v164, s[60:61]
	s_mov_b32 m0, s64
	s_nop 0
	global_load_lds_dwordx4 v168, s[58:59]
	s_mov_b32 m0, s65
	s_nop 0
	global_load_lds_dwordx4 v166, s[58:59]
	s_waitcnt vmcnt(8)
	s_waitcnt lgkmcnt(0)
	s_barrier
	s_setprio 1
	s_waitcnt lgkmcnt(0)
	v_mfma_scale_f32_16x16x128_f8f6f4 v[96:99], v[4:11], v[186:193], v[96:99], v245, v245 op_sel_hi:[0,0,0]
	v_mfma_scale_f32_16x16x128_f8f6f4 v[92:95], v[12:19], v[186:193], v[92:95], v245, v245 op_sel_hi:[0,0,0]
	v_mfma_scale_f32_16x16x128_f8f6f4 v[80:83], v[4:11], v[208:215], v[80:83], v245, v245 op_sel_hi:[0,0,0]
	v_mfma_scale_f32_16x16x128_f8f6f4 v[76:79], v[12:19], v[208:215], v[76:79], v245, v245 op_sel_hi:[0,0,0]
	v_mfma_scale_f32_16x16x128_f8f6f4 v[64:67], v[4:11], v[216:223], v[64:67], v245, v245 op_sel_hi:[0,0,0]
	v_mfma_scale_f32_16x16x128_f8f6f4 v[60:63], v[12:19], v[216:223], v[60:63], v245, v245 op_sel_hi:[0,0,0]
	v_mfma_scale_f32_16x16x128_f8f6f4 v[48:51], v[4:11], v[228:235], v[48:51], v245, v245 op_sel_hi:[0,0,0]
	v_mfma_scale_f32_16x16x128_f8f6f4 v[44:47], v[12:19], v[228:235], v[44:47], v245, v245 op_sel_hi:[0,0,0]
	s_setprio 0
	s_setprio 1
	v_mfma_scale_f32_16x16x128_f8f6f4 v[88:91], v[20:27], v[186:193], v[88:91], v245, v245 op_sel_hi:[0,0,0]
	v_mfma_scale_f32_16x16x128_f8f6f4 v[84:87], v[28:35], v[186:193], v[84:87], v245, v245 op_sel_hi:[0,0,0]
	v_mfma_scale_f32_16x16x128_f8f6f4 v[72:75], v[20:27], v[208:215], v[72:75], v245, v245 op_sel_hi:[0,0,0]
	v_mfma_scale_f32_16x16x128_f8f6f4 v[68:71], v[28:35], v[208:215], v[68:71], v245, v245 op_sel_hi:[0,0,0]
	v_mfma_scale_f32_16x16x128_f8f6f4 v[56:59], v[20:27], v[216:223], v[56:59], v245, v245 op_sel_hi:[0,0,0]
	v_mfma_scale_f32_16x16x128_f8f6f4 v[52:55], v[28:35], v[216:223], v[52:55], v245, v245 op_sel_hi:[0,0,0]
	v_mfma_scale_f32_16x16x128_f8f6f4 v[40:43], v[20:27], v[228:235], v[40:43], v245, v245 op_sel_hi:[0,0,0]
	v_mfma_scale_f32_16x16x128_f8f6f4 v[36:39], v[28:35], v[228:235], v[36:39], v245, v245 op_sel_hi:[0,0,0]
	s_setprio 0
	s_add_u32 s4, s4, 0x100
	s_addc_u32 s5, s5, 0
	s_add_u32 s56, s56, 0x10000
	s_addc_u32 s57, s57, 0
	s_cmp_gt_u32 s71, 19
	s_cbranch_scc1 .Lrot1_exit
	s_add_i32 s71, s71, 2
	s_add_u32 s58, s54, s56
	s_addc_u32 s59, s55, s57
	s_add_u32 s58, s58, 0x10000
	s_addc_u32 s59, s59, 0
	s_cmp_eq_u32 s56, 0xa0000
	s_cselect_b32 s62, s42, s58
	s_cselect_b32 s63, s43, s59
	s_cselect_b32 s60, s52, s4
	s_cselect_b32 s61, s53, s5
	s_add_u32 s58, s62, 0x8000
	s_addc_u32 s59, s63, 0
	s_add_i32 s73, 0, 0x10000
	s_add_i32 s72, 0, 0x14000
	v_add_u32_e32 v4, s73, v183
	v_add_u32_e32 v8, s72, v183
	s_barrier
	s_branch .Lrot1_body
.Lrot1_exit:
	s_barrier
	s_waitcnt vmcnt(0)
	s_nop 15
	s_nop 15
	s_and_b64 vcc, exec, s[50:51]
	s_cbranch_vccz .LBB0_511
	s_barrier

; #define PG8_STAGE(bufoff, gbase, voff) do { _Pragma("unroll") for (int _i = 0; _i < 2; ++_i) \
;         __builtin_amdgcn_global_load_lds((const unsigned*)((const char*)(gbase) + (voff)[_i]), (PG8_LAS unsigned*)(lds + (bufoff) + ldsw + _i * 8192), 16, 0, 0); } while (0)
; #define PG8_LDA(dst, b, h) do { _Pragma("unroll") for (int m = 0; m < 4; ++m) _Pragma("unroll") for (int k = 0; k < 2; ++k) dst[m][k] = *(const PG8_LAS bf16x8*)(lds + PG8_SA(b, h) + aoff + m * 2048 + k * 1024); } while (0)
; #define PG8_LDB(dst, b, h) do { _Pragma("unroll") for (int n = 0; n < 2; ++n) _Pragma("unroll") for (int k = 0; k < 2; ++k) dst[n][k] = *(const PG8_LAS bf16x8*)(lds + PG8_SB(b, h) + boff + n * 2048 + k * 1024); } while (0)
; #define PG8_WAIT_V8_UNLESS_FIRST(t) asm volatile("s_cmp_eq_u32 %0, 0\n\ts_cbranch_scc1 .Lpg8skip%=\n\ts_waitcnt vmcnt(8)\n.Lpg8skip%=:" :: "s"(t) : "scc", "memory")
; #define PG8_WAIT_L(n) asm volatile("s_waitcnt lgkmcnt(" #n ")" ::: "memory")
; #define PG8_BAR __builtin_amdgcn_s_barrier()
; #define PG8_SCHED __builtin_amdgcn_sched_barrier(0)
; template <class Epi, class Sched, bool ALIGN_EPI = false, bool SP2 = false, bool FP8 = false, bool ABLK = false>
; __device__ __forceinline__ void gemm_phase(PG8_LAS unsigned char* lds, const Gemm g, const Sched& S, const Epi& E) {
;     ...
;             PG8_LDB(B0, 0, 0); PG8_LDB(B1, 0, 1); PG8_SCHED; PG8_LDA(At, 0, 0); PG8_STAGE(PG8_SA(1, 1), a1 + hstepA, voffA);
;             PG8_WAIT_V8_UNLESS_FIRST(t); PG8_WAIT_L(0); PG8_BAR; PG8_MMA(0, 0, At, B0); PG8_MMA(0, 1, At, B1); PG8_BAR; PG8_SCHED;
.Lrot2_body:
	ds_read_b128 v[132:135], v144
	ds_read_b128 v[136:139], v144 offset:1024
	ds_read_b128 v[140:143], v144 offset:2048
	ds_read_b128 v[144:147], v144 offset:3072
	ds_read_b128 v[148:151], v160
	ds_read_b128 v[152:155], v160 offset:1024
	ds_read_b128 v[156:159], v160 offset:2048
	ds_read_b128 v[160:163], v160 offset:3072
	s_add_i32 m0, s8, 0xc000
	ds_read_b128 v[164:167], v195
	ds_read_b128 v[168:171], v195 offset:1024
	ds_read_b128 v[182:185], v195 offset:2048
	ds_read_b128 v[208:211], v195 offset:3072
	ds_read_b128 v[212:215], v195 offset:4096
	ds_read_b128 v[216:219], v195 offset:5120
	ds_read_b128 v[220:223], v195 offset:6144
	ds_read_b128 v[228:231], v195 offset:7168
	global_load_lds_dwordx4 v178, s[42:43]
	s_add_i32 m0, s8, 0xe000
	s_nop 0
	global_load_lds_dwordx4 v180, s[42:43]
	s_cmp_eq_u32 s95, 0
	s_cbranch_scc1 .Lpg8skip4
	s_waitcnt vmcnt(8)

; #define PG8_STAGE(bufoff, gbase, voff) do { _Pragma("unroll") for (int _i = 0; _i < 2; ++_i) \
;         __builtin_amdgcn_global_load_lds((const unsigned*)((const char*)(gbase) + (voff)[_i]), (PG8_LAS unsigned*)(lds + (bufoff) + ldsw + _i * 8192), 16, 0, 0); } while (0)
; #define PG8_LDA(dst, b, h) do { _Pragma("unroll") for (int m = 0; m < 4; ++m) _Pragma("unroll") for (int k = 0; k < 2; ++k) dst[m][k] = *(const PG8_LAS bf16x8*)(lds + PG8_SA(b, h) + aoff + m * 2048 + k * 1024); } while (0)
; #define PG8_LDB(dst, b, h) do { _Pragma("unroll") for (int n = 0; n < 2; ++n) _Pragma("unroll") for (int k = 0; k < 2; ++k) dst[n][k] = *(const PG8_LAS bf16x8*)(lds + PG8_SB(b, h) + boff + n * 2048 + k * 1024); } while (0)
; #define PG8_WAIT_V(n) asm volatile("s_waitcnt vmcnt(" #n ")" ::: "memory")
; #define PG8_WAIT_V8_UNLESS_FIRST(t) asm volatile("s_cmp_eq_u32 %0, 0\n\ts_cbranch_scc1 .Lpg8skip%=\n\ts_waitcnt vmcnt(8)\n.Lpg8skip%=:" :: "s"(t) : "scc", "memory")
; #define PG8_WAIT_L(n) asm volatile("s_waitcnt lgkmcnt(" #n ")" ::: "memory")
; #define PG8_BAR __builtin_amdgcn_s_barrier()
; #define PG8_SCHED __builtin_amdgcn_sched_barrier(0)
; template <class Epi, class Sched, bool ALIGN_EPI = false, bool SP2 = false, bool FP8 = false, bool ABLK = false>
; __device__ __forceinline__ void gemm_phase(PG8_LAS unsigned char* lds, const Gemm g, const Sched& S, const Epi& E) {
;     ...
;             PG8_WAIT_V8_UNLESS_FIRST(t); PG8_WAIT_L(0); PG8_BAR; PG8_MMA(1, 0, At, B0); PG8_MMA(1, 1, At, B1); PG8_BAR; PG8_SCHED;
;             PG8_LDB(B0, 1, 0); PG8_LDB(B1, 1, 1); PG8_SCHED; PG8_LDA(At, 1, 0); PG8_STAGE(PG8_SA(0, 1), a2 + hstepA, voffA);
;             PG8_WAIT_V(8); PG8_WAIT_L(0); PG8_BAR; PG8_MMA(0, 0, At, B0); PG8_MMA(0, 1, At, B1); PG8_BAR; PG8_SCHED;
.Lpg8skip5:
	s_waitcnt lgkmcnt(0)
	s_barrier
	s_setprio 1
	s_waitcnt lgkmcnt(0)
	v_mfma_f32_16x16x32_bf16 v[64:67], v[132:135], v[164:167], v[64:67]
	v_mfma_f32_16x16x32_bf16 v[60:63], v[140:143], v[164:167], v[60:63]
	v_mfma_f32_16x16x32_bf16 v[48:51], v[132:135], v[182:185], v[48:51]
	v_mfma_f32_16x16x32_bf16 v[44:47], v[140:143], v[182:185], v[44:47]
	v_mfma_f32_16x16x32_bf16 v[32:35], v[132:135], v[212:215], v[32:35]
	v_mfma_f32_16x16x32_bf16 v[28:31], v[140:143], v[212:215], v[28:31]
	v_mfma_f32_16x16x32_bf16 v[16:19], v[132:135], v[220:223], v[16:19]
	v_mfma_f32_16x16x32_bf16 v[12:15], v[140:143], v[220:223], v[12:15]
	v_mfma_f32_16x16x32_bf16 v[64:67], v[136:139], v[168:171], v[64:67]
	v_mfma_f32_16x16x32_bf16 v[60:63], v[144:147], v[168:171], v[60:63]
	v_mfma_f32_16x16x32_bf16 v[48:51], v[136:139], v[208:211], v[48:51]
	v_mfma_f32_16x16x32_bf16 v[44:47], v[144:147], v[208:211], v[44:47]
	v_mfma_f32_16x16x32_bf16 v[32:35], v[136:139], v[216:219], v[32:35]
	v_mfma_f32_16x16x32_bf16 v[28:31], v[144:147], v[216:219], v[28:31]
	v_mfma_f32_16x16x32_bf16 v[16:19], v[136:139], v[228:231], v[16:19]
	v_mfma_f32_16x16x32_bf16 v[12:15], v[144:147], v[228:231], v[12:15]
	s_setprio 0
	s_setprio 1
	v_mfma_f32_16x16x32_bf16 v[56:59], v[148:151], v[164:167], v[56:59]
	v_mfma_f32_16x16x32_bf16 v[52:55], v[156:159], v[164:167], v[52:55]
	v_mfma_f32_16x16x32_bf16 v[40:43], v[148:151], v[182:185], v[40:43]
	v_mfma_f32_16x16x32_bf16 v[36:39], v[156:159], v[182:185], v[36:39]
	v_mfma_f32_16x16x32_bf16 v[24:27], v[148:151], v[212:215], v[24:27]
	v_mfma_f32_16x16x32_bf16 v[20:23], v[156:159], v[212:215], v[20:23]
	v_mfma_f32_16x16x32_bf16 v[8:11], v[148:151], v[220:223], v[8:11]
	v_mfma_f32_16x16x32_bf16 v[4:7], v[156:159], v[220:223], v[4:7]
	v_mfma_f32_16x16x32_bf16 v[56:59], v[152:155], v[168:171], v[56:59]
	v_mfma_f32_16x16x32_bf16 v[52:55], v[160:163], v[168:171], v[52:55]
	v_mfma_f32_16x16x32_bf16 v[40:43], v[152:155], v[208:211], v[40:43]
	v_mfma_f32_16x16x32_bf16 v[36:39], v[160:163], v[208:211], v[36:39]
	v_mfma_f32_16x16x32_bf16 v[24:27], v[152:155], v[216:219], v[24:27]
	v_mfma_f32_16x16x32_bf16 v[20:23], v[160:163], v[216:219], v[20:23]
	v_mfma_f32_16x16x32_bf16 v[8:11], v[152:155], v[228:231], v[8:11]
	v_mfma_f32_16x16x32_bf16 v[4:7], v[160:163], v[228:231], v[4:7]
	s_setprio 0
	s_barrier
	s_add_i32 s96, 0, 0x18000
	s_add_i32 s97, 0, 0x1c000
	v_add_u32_e32 v144, s96, v191
	v_add_u32_e32 v160, s97, v191
	ds_read_b128 v[132:135], v144
	ds_read_b128 v[136:139], v144 offset:1024
	ds_read_b128 v[140:143], v144 offset:2048
	ds_read_b128 v[144:147], v144 offset:3072
	ds_read_b128 v[148:151], v160
	ds_read_b128 v[152:155], v160 offset:1024
	ds_read_b128 v[156:159], v160 offset:2048
	ds_read_b128 v[160:163], v160 offset:3072
	s_add_u32 s90, s90, 0x40000
	s_addc_u32 s91, s91, 0
	s_mov_b32 m0, s17
	ds_read_b128 v[164:167], v195 offset:32768
	ds_read_b128 v[168:171], v195 offset:33792
	ds_read_b128 v[182:185], v195 offset:34816
	ds_read_b128 v[208:211], v195 offset:35840
	ds_read_b128 v[212:215], v195 offset:36864
	ds_read_b128 v[216:219], v195 offset:37888
	ds_read_b128 v[220:223], v195 offset:38912
	ds_read_b128 v[228:231], v195 offset:39936
	global_load_lds_dwordx4 v176, s[90:91]
	s_mov_b32 m0, s18
	s_nop 0
	global_load_lds_dwordx4 v174, s[90:91]
	s_waitcnt vmcnt(8)
	s_waitcnt lgkmcnt(0)
	s_barrier
	s_setprio 1
	s_waitcnt lgkmcnt(0)
	v_mfma_f32_16x16x32_bf16 v[128:131], v[132:135], v[164:167], v[128:131]
	v_mfma_f32_16x16x32_bf16 v[124:127], v[140:143], v[164:167], v[124:127]
	v_mfma_f32_16x16x32_bf16 v[112:115], v[132:135], v[182:185], v[112:115]
	v_mfma_f32_16x16x32_bf16 v[108:111], v[140:143], v[182:185], v[108:111]
	v_mfma_f32_16x16x32_bf16 v[96:99], v[132:135], v[212:215], v[96:99]
	v_mfma_f32_16x16x32_bf16 v[92:95], v[140:143], v[212:215], v[92:95]
	v_mfma_f32_16x16x32_bf16 v[80:83], v[132:135], v[220:223], v[80:83]
	v_mfma_f32_16x16x32_bf16 v[76:79], v[140:143], v[220:223], v[76:79]
	v_mfma_f32_16x16x32_bf16 v[128:131], v[136:139], v[168:171], v[128:131]
	v_mfma_f32_16x16x32_bf16 v[124:127], v[144:147], v[168:171], v[124:127]
	v_mfma_f32_16x16x32_bf16 v[112:115], v[136:139], v[208:211], v[112:115]
	v_mfma_f32_16x16x32_bf16 v[108:111], v[144:147], v[208:211], v[108:111]
	v_mfma_f32_16x16x32_bf16 v[96:99], v[136:139], v[216:219], v[96:99]
	v_mfma_f32_16x16x32_bf16 v[92:95], v[144:147], v[216:219], v[92:95]
	v_mfma_f32_16x16x32_bf16 v[80:83], v[136:139], v[228:231], v[80:83]
	v_mfma_f32_16x16x32_bf16 v[76:79], v[144:147], v[228:231], v[76:79]
	s_setprio 0
	s_setprio 1
	v_mfma_f32_16x16x32_bf16 v[120:123], v[148:151], v[164:167], v[120:123]
	v_mfma_f32_16x16x32_bf16 v[116:119], v[156:159], v[164:167], v[116:119]
	v_mfma_f32_16x16x32_bf16 v[104:107], v[148:151], v[182:185], v[104:107]
	v_mfma_f32_16x16x32_bf16 v[100:103], v[156:159], v[182:185], v[100:103]
	v_mfma_f32_16x16x32_bf16 v[88:91], v[148:151], v[212:215], v[88:91]
	v_mfma_f32_16x16x32_bf16 v[84:87], v[156:159], v[212:215], v[84:87]
	v_mfma_f32_16x16x32_bf16 v[72:75], v[148:151], v[220:223], v[72:75]
	v_mfma_f32_16x16x32_bf16 v[68:71], v[156:159], v[220:223], v[68:71]
	v_mfma_f32_16x16x32_bf16 v[120:123], v[152:155], v[168:171], v[120:123]
	v_mfma_f32_16x16x32_bf16 v[116:119], v[160:163], v[168:171], v[116:119]
	v_mfma_f32_16x16x32_bf16 v[104:107], v[152:155], v[208:211], v[104:107]
	v_mfma_f32_16x16x32_bf16 v[100:103], v[160:163], v[208:211], v[100:103]
	v_mfma_f32_16x16x32_bf16 v[88:91], v[152:155], v[216:219], v[88:91]
	v_mfma_f32_16x16x32_bf16 v[84:87], v[160:163], v[216:219], v[84:87]
	v_mfma_f32_16x16x32_bf16 v[72:75], v[152:155], v[228:231], v[72:75]
	v_mfma_f32_16x16x32_bf16 v[68:71], v[160:163], v[228:231], v[68:71]
	s_setprio 0
	s_barrier
; #define PG8_STAGE(bufoff, gbase, voff) do { _Pragma("unroll") for (int _i = 0; _i < 2; ++_i) \
;         __builtin_amdgcn_global_load_lds((const unsigned*)((const char*)(gbase) + (voff)[_i]), (PG8_LAS unsigned*)(lds + (bufoff) + ldsw + _i * 8192), 16, 0, 0); } while (0)
; #define PG8_WAIT_V(n) asm volatile("s_waitcnt vmcnt(" #n ")" ::: "memory")
; #define PG8_WAIT_L(n) asm volatile("s_waitcnt lgkmcnt(" #n ")" ::: "memory")
; #define PG8_BAR __builtin_amdgcn_s_barrier()
; template <class Epi, class Sched, bool ALIGN_EPI = false, bool SP2 = false, bool FP8 = false, bool ABLK = false>
; __device__ __forceinline__ void gemm_phase(PG8_LAS unsigned char* lds, const Gemm g, const Sched& S, const Epi& E) {
;     ...
;         for (int t = 0; t < nt; t += 2) {
;             const bool last = (t == nt - 2);
;             const char* a1 = cA + (size_t)(t + 1) * kstepA;
;             const char* a2 = last ? nA : cA + (size_t)(t + 2) * kstepA; const char* b2 = last ? nB : cB + (size_t)(t + 2) * kstep;
;             const char* a3 = a2 + kstepA; const char* b3 = b2 + kstep;
;             if (last && has_next) S.a_ready(nxt);
;             if constexpr (SP2) {
;             PG8_LDB(B0, 0, 0); PG8_LDB(B1, 0, 1); PG8_SCHED; PG8_LDA(At, 0, 0); PG8_STAGE(PG8_SA(1, 1), a1 + hstepA, voffA);
;             PG8_WAIT_V8_UNLESS_FIRST(t); PG8_WAIT_L(0); PG8_BAR; PG8_MMA(0, 0, At, B0); PG8_MMA(0, 1, At, B1); PG8_BAR; PG8_SCHED;
;             PG8_LDA(At, 0, 1); PG8_STAGE(PG8_SB(0, 0), b2, voffB); PG8_STAGE(PG8_SB(0, 1), b2 + hstep, voffB); PG8_STAGE(PG8_SA(0, 0), a2, voffA);
;             PG8_WAIT_V8_UNLESS_FIRST(t); PG8_WAIT_L(0); PG8_BAR; PG8_MMA(1, 0, At, B0); PG8_MMA(1, 1, At, B1); PG8_BAR; PG8_SCHED;
;             PG8_LDB(B0, 1, 0); PG8_LDB(B1, 1, 1); PG8_SCHED; PG8_LDA(At, 1, 0); PG8_STAGE(PG8_SA(0, 1), a2 + hstepA, voffA);
;             PG8_WAIT_V(8); PG8_WAIT_L(0); PG8_BAR; PG8_MMA(0, 0, At, B0); PG8_MMA(0, 1, At, B1); PG8_BAR; PG8_SCHED;
;             PG8_LDA(At, 1, 1); PG8_STAGE(PG8_SB(1, 0), b3, voffB); PG8_STAGE(PG8_SB(1, 1), b3 + hstep, voffB); PG8_STAGE(PG8_SA(1, 0), a3, voffA);
;             PG8_WAIT_V(8); PG8_WAIT_L(0); PG8_BAR; PG8_MMA(1, 0, At, B0); PG8_MMA(1, 1, At, B1); PG8_BAR; PG8_SCHED;
;     ...
;         if constexpr (SP2) PG8_WAIT_V(0);
;         if constexpr (FP8) asm volatile("s_nop 15\n\ts_nop 15" ::: "memory");
;         if constexpr (ALIGN_EPI) { if (wr == 0) PG8_BAR; }
	s_add_i32 s90, s96, s7
	v_lshl_add_u64 v[188:189], v[188:189], 0, s[34:35]
	s_mov_b32 m0, s90
	ds_read_b128 v[164:167], v195 offset:49152
	ds_read_b128 v[168:171], v195 offset:50176
	ds_read_b128 v[182:185], v195 offset:51200
	ds_read_b128 v[208:211], v195 offset:52224
	ds_read_b128 v[212:215], v195 offset:53248
	ds_read_b128 v[216:219], v195 offset:54272
	ds_read_b128 v[220:223], v195 offset:55296
	ds_read_b128 v[228:231], v195 offset:56320
	global_load_lds_dwordx4 v[188:189], off
	s_add_i32 m0, s90, 0x2000
	s_add_u32 s44, s44, 0x40080
	v_lshl_add_u64 v[188:189], v[192:193], 0, s[34:35]
	s_addc_u32 s45, s45, 0
	s_add_i32 s90, s97, s7
	global_load_lds_dwordx4 v[188:189], off
	s_mov_b32 m0, s90
	s_nop 0
	global_load_lds_dwordx4 v2, s[44:45]
	s_add_i32 m0, s90, 0x2000
	s_nop 0
	global_load_lds_dwordx4 v172, s[44:45]
	v_lshl_add_u64 v[188:189], v[224:225], 0, s[34:35]
	s_mov_b32 m0, s19
	s_nop 0
	global_load_lds_dwordx4 v[188:189], off
	v_lshl_add_u64 v[188:189], v[232:233], 0, s[34:35]
	s_mov_b32 m0, s20
	s_nop 0
	global_load_lds_dwordx4 v[188:189], off
	s_waitcnt vmcnt(8)
	s_waitcnt lgkmcnt(0)
	s_barrier
	s_setprio 1
	s_waitcnt lgkmcnt(0)
	v_mfma_f32_16x16x32_bf16 v[64:67], v[132:135], v[164:167], v[64:67]
	v_mfma_f32_16x16x32_bf16 v[60:63], v[140:143], v[164:167], v[60:63]
	v_mfma_f32_16x16x32_bf16 v[48:51], v[132:135], v[182:185], v[48:51]
	v_mfma_f32_16x16x32_bf16 v[44:47], v[140:143], v[182:185], v[44:47]
	v_mfma_f32_16x16x32_bf16 v[32:35], v[132:135], v[212:215], v[32:35]
	v_mfma_f32_16x16x32_bf16 v[28:31], v[140:143], v[212:215], v[28:31]
	v_mfma_f32_16x16x32_bf16 v[16:19], v[132:135], v[220:223], v[16:19]
	v_mfma_f32_16x16x32_bf16 v[12:15], v[140:143], v[220:223], v[12:15]
	v_mfma_f32_16x16x32_bf16 v[64:67], v[136:139], v[168:171], v[64:67]
	v_mfma_f32_16x16x32_bf16 v[60:63], v[144:147], v[168:171], v[60:63]
	v_mfma_f32_16x16x32_bf16 v[48:51], v[136:139], v[208:211], v[48:51]
	v_mfma_f32_16x16x32_bf16 v[44:47], v[144:147], v[208:211], v[44:47]
	v_mfma_f32_16x16x32_bf16 v[32:35], v[136:139], v[216:219], v[32:35]
	v_mfma_f32_16x16x32_bf16 v[28:31], v[144:147], v[216:219], v[28:31]
	v_mfma_f32_16x16x32_bf16 v[16:19], v[136:139], v[228:231], v[16:19]
	v_mfma_f32_16x16x32_bf16 v[12:15], v[144:147], v[228:231], v[12:15]
	s_setprio 0
	s_setprio 1
	v_mfma_f32_16x16x32_bf16 v[56:59], v[148:151], v[164:167], v[56:59]
	v_mfma_f32_16x16x32_bf16 v[52:55], v[156:159], v[164:167], v[52:55]
	v_mfma_f32_16x16x32_bf16 v[40:43], v[148:151], v[182:185], v[40:43]
	v_mfma_f32_16x16x32_bf16 v[36:39], v[156:159], v[182:185], v[36:39]
	v_mfma_f32_16x16x32_bf16 v[24:27], v[148:151], v[212:215], v[24:27]
	v_mfma_f32_16x16x32_bf16 v[20:23], v[156:159], v[212:215], v[20:23]
	v_mfma_f32_16x16x32_bf16 v[8:11], v[148:151], v[220:223], v[8:11]
	v_mfma_f32_16x16x32_bf16 v[4:7], v[156:159], v[220:223], v[4:7]
	v_mfma_f32_16x16x32_bf16 v[56:59], v[152:155], v[168:171], v[56:59]
	v_mfma_f32_16x16x32_bf16 v[52:55], v[160:163], v[168:171], v[52:55]
	v_mfma_f32_16x16x32_bf16 v[40:43], v[152:155], v[208:211], v[40:43]
	v_mfma_f32_16x16x32_bf16 v[36:39], v[160:163], v[208:211], v[36:39]
	v_mfma_f32_16x16x32_bf16 v[24:27], v[152:155], v[216:219], v[24:27]
	v_mfma_f32_16x16x32_bf16 v[20:23], v[160:163], v[216:219], v[20:23]
	v_mfma_f32_16x16x32_bf16 v[8:11], v[152:155], v[228:231], v[8:11]
	v_mfma_f32_16x16x32_bf16 v[4:7], v[160:163], v[228:231], v[4:7]
	s_setprio 0
	s_add_u32 s42, s42, 0x100
	s_addc_u32 s43, s43, 0
	s_add_u32 s92, s92, 0x100
	s_addc_u32 s94, s94, 0
	s_cmp_gt_u32 s95, 13
	s_mov_b32 s44, s95
	s_cbranch_scc1 .Lrot2_exit
	s_add_i32 s95, s44, 2
	s_add_u32 s45, s42, 0xfffc0080
	s_addc_u32 s90, s43, -1
	s_add_i32 s96, 0, 0x10000
	s_cmp_eq_u32 s44, 12
	s_cselect_b32 s91, s4, s90
	s_cselect_b32 s90, s5, s45
	s_cselect_b32 s45, s75, s94
	s_cselect_b32 s44, s77, s92
	s_add_i32 vcc_lo, 0, 0x14000
	v_add_u32_e32 v144, s96, v191
	v_add_u32_e32 v160, vcc_lo, v191
	s_barrier
	s_branch .Lrot2_body
.Lrot2_exit:
	s_barrier
	s_waitcnt vmcnt(0)
	s_and_b64 vcc, exec, s[64:65]
	s_cbranch_vccnz .LBB0_604
	s_cmpk_lt_i32 s73, 0xf4
	s_mov_b64 s[4:5], -1
	s_cbranch_scc1 .LBB0_605

; #define PG8_STAGE(bufoff, gbase, voff) do { _Pragma("unroll") for (int _i = 0; _i < 2; ++_i) \
;         __builtin_amdgcn_global_load_lds((const unsigned*)((const char*)(gbase) + (voff)[_i]), (PG8_LAS unsigned*)(lds + (bufoff) + ldsw + _i * 8192), 16, 0, 0); } while (0)
; #define PG8_LDA(dst, b, h) do { _Pragma("unroll") for (int m = 0; m < 4; ++m) _Pragma("unroll") for (int k = 0; k < 2; ++k) dst[m][k] = *(const PG8_LAS bf16x8*)(lds + PG8_SA(b, h) + aoff + m * 2048 + k * 1024); } while (0)
; #define PG8_LDB(dst, b, h) do { _Pragma("unroll") for (int n = 0; n < 2; ++n) _Pragma("unroll") for (int k = 0; k < 2; ++k) dst[n][k] = *(const PG8_LAS bf16x8*)(lds + PG8_SB(b, h) + boff + n * 2048 + k * 1024); } while (0)
; #define PG8_WAIT_V8_UNLESS_FIRST(t) asm volatile("s_cmp_eq_u32 %0, 0\n\ts_cbranch_scc1 .Lpg8skip%=\n\ts_waitcnt vmcnt(8)\n.Lpg8skip%=:" :: "s"(t) : "scc", "memory")
; #define PG8_WAIT_L(n) asm volatile("s_waitcnt lgkmcnt(" #n ")" ::: "memory")
; #define PG8_BAR __builtin_amdgcn_s_barrier()
; #define PG8_SCHED __builtin_amdgcn_sched_barrier(0)
; template <class Epi, class Sched, bool ALIGN_EPI = false, bool SP2 = false, bool FP8 = false, bool ABLK = false>
; __device__ __forceinline__ void gemm_phase(PG8_LAS unsigned char* lds, const Gemm g, const Sched& S, const Epi& E) {
;     ...
;             PG8_LDB(B0, 0, 0); PG8_LDB(B1, 0, 1); PG8_SCHED; PG8_LDA(At, 0, 0); PG8_STAGE(PG8_SA(1, 1), a1 + hstepA, voffA);
;             PG8_WAIT_V8_UNLESS_FIRST(t); PG8_WAIT_L(0); PG8_BAR; PG8_MMA(0, 0, At, B0); PG8_MMA(0, 1, At, B1); PG8_BAR; PG8_SCHED;
.Lrot3_body:
	ds_read_b128 v[124:127], v136
	ds_read_b128 v[128:131], v136 offset:1024
	ds_read_b128 v[132:135], v136 offset:2048
	ds_read_b128 v[136:139], v136 offset:3072
	ds_read_b128 v[140:143], v170
	ds_read_b128 v[144:147], v170 offset:1024
	ds_read_b128 v[156:159], v170 offset:2048
	ds_read_b128 v[170:173], v170 offset:3072
	s_add_i32 m0, s18, 0xc000
	ds_read_b128 v[174:177], v208
	ds_read_b128 v[178:181], v208 offset:1024
	ds_read_b128 v[182:185], v208 offset:2048
	ds_read_b128 v[186:189], v208 offset:3072
	ds_read_b128 v[190:193], v208 offset:4096
	ds_read_b128 v[210:213], v208 offset:5120
	ds_read_b128 v[214:217], v208 offset:6144
	ds_read_b128 v[218:221], v208 offset:7168
	global_load_lds_dwordx4 v166, s[42:43]
	s_add_i32 m0, s18, 0xe000
	s_nop 0
	global_load_lds_dwordx4 v168, s[42:43]
	s_cmp_eq_u32 s72, 0
	s_cbranch_scc1 .Lpg8skip6
	s_waitcnt vmcnt(8)

; #define PG8_STAGE(bufoff, gbase, voff) do { _Pragma("unroll") for (int _i = 0; _i < 2; ++_i) \
;         __builtin_amdgcn_global_load_lds((const unsigned*)((const char*)(gbase) + (voff)[_i]), (PG8_LAS unsigned*)(lds + (bufoff) + ldsw + _i * 8192), 16, 0, 0); } while (0)
; #define PG8_LDA(dst, b, h) do { _Pragma("unroll") for (int m = 0; m < 4; ++m) _Pragma("unroll") for (int k = 0; k < 2; ++k) dst[m][k] = *(const PG8_LAS bf16x8*)(lds + PG8_SA(b, h) + aoff + m * 2048 + k * 1024); } while (0)
; #define PG8_LDB(dst, b, h) do { _Pragma("unroll") for (int n = 0; n < 2; ++n) _Pragma("unroll") for (int k = 0; k < 2; ++k) dst[n][k] = *(const PG8_LAS bf16x8*)(lds + PG8_SB(b, h) + boff + n * 2048 + k * 1024); } while (0)
; #define PG8_WAIT_V(n) asm volatile("s_waitcnt vmcnt(" #n ")" ::: "memory")
; #define PG8_WAIT_V8_UNLESS_FIRST(t) asm volatile("s_cmp_eq_u32 %0, 0\n\ts_cbranch_scc1 .Lpg8skip%=\n\ts_waitcnt vmcnt(8)\n.Lpg8skip%=:" :: "s"(t) : "scc", "memory")
; #define PG8_WAIT_L(n) asm volatile("s_waitcnt lgkmcnt(" #n ")" ::: "memory")
; #define PG8_BAR __builtin_amdgcn_s_barrier()
; #define PG8_SCHED __builtin_amdgcn_sched_barrier(0)
; template <class Epi, class Sched, bool ALIGN_EPI = false, bool SP2 = false, bool FP8 = false, bool ABLK = false>
; __device__ __forceinline__ void gemm_phase(PG8_LAS unsigned char* lds, const Gemm g, const Sched& S, const Epi& E) {
;     ...
;             PG8_WAIT_V8_UNLESS_FIRST(t); PG8_WAIT_L(0); PG8_BAR; PG8_MMA(1, 0, At, B0); PG8_MMA(1, 1, At, B1); PG8_BAR; PG8_SCHED;
;             PG8_LDB(B0, 1, 0); PG8_LDB(B1, 1, 1); PG8_SCHED; PG8_LDA(At, 1, 0); PG8_STAGE(PG8_SA(0, 1), a2 + hstepA, voffA);
;             PG8_WAIT_V(8); PG8_WAIT_L(0); PG8_BAR; PG8_MMA(0, 0, At, B0); PG8_MMA(0, 1, At, B1); PG8_BAR; PG8_SCHED;
.Lpg8skip7:
	s_waitcnt lgkmcnt(0)
	s_barrier
	s_setprio 1
	s_waitcnt lgkmcnt(0)
	v_mfma_f32_16x16x32_bf16 v[64:67], v[124:127], v[174:177], v[64:67]
	v_mfma_f32_16x16x32_bf16 v[60:63], v[132:135], v[174:177], v[60:63]
	v_mfma_f32_16x16x32_bf16 v[48:51], v[124:127], v[182:185], v[48:51]
	v_mfma_f32_16x16x32_bf16 v[44:47], v[132:135], v[182:185], v[44:47]
	v_mfma_f32_16x16x32_bf16 v[32:35], v[124:127], v[190:193], v[32:35]
	v_mfma_f32_16x16x32_bf16 v[28:31], v[132:135], v[190:193], v[28:31]
	v_mfma_f32_16x16x32_bf16 v[16:19], v[124:127], v[214:217], v[16:19]
	v_mfma_f32_16x16x32_bf16 v[12:15], v[132:135], v[214:217], v[12:15]
	v_mfma_f32_16x16x32_bf16 v[64:67], v[128:131], v[178:181], v[64:67]
	v_mfma_f32_16x16x32_bf16 v[60:63], v[136:139], v[178:181], v[60:63]
	v_mfma_f32_16x16x32_bf16 v[48:51], v[128:131], v[186:189], v[48:51]
	v_mfma_f32_16x16x32_bf16 v[44:47], v[136:139], v[186:189], v[44:47]
	v_mfma_f32_16x16x32_bf16 v[32:35], v[128:131], v[210:213], v[32:35]
	v_mfma_f32_16x16x32_bf16 v[28:31], v[136:139], v[210:213], v[28:31]
	v_mfma_f32_16x16x32_bf16 v[16:19], v[128:131], v[218:221], v[16:19]
	v_mfma_f32_16x16x32_bf16 v[12:15], v[136:139], v[218:221], v[12:15]
	s_setprio 0
	s_setprio 1
	v_mfma_f32_16x16x32_bf16 v[56:59], v[140:143], v[174:177], v[56:59]
	v_mfma_f32_16x16x32_bf16 v[52:55], v[156:159], v[174:177], v[52:55]
	v_mfma_f32_16x16x32_bf16 v[40:43], v[140:143], v[182:185], v[40:43]
	v_mfma_f32_16x16x32_bf16 v[36:39], v[156:159], v[182:185], v[36:39]
	v_mfma_f32_16x16x32_bf16 v[24:27], v[140:143], v[190:193], v[24:27]
	v_mfma_f32_16x16x32_bf16 v[20:23], v[156:159], v[190:193], v[20:23]
	v_mfma_f32_16x16x32_bf16 v[8:11], v[140:143], v[214:217], v[8:11]
	v_mfma_f32_16x16x32_bf16 v[4:7], v[156:159], v[214:217], v[4:7]
	v_mfma_f32_16x16x32_bf16 v[56:59], v[144:147], v[178:181], v[56:59]
	v_mfma_f32_16x16x32_bf16 v[52:55], v[170:173], v[178:181], v[52:55]
	v_mfma_f32_16x16x32_bf16 v[40:43], v[144:147], v[186:189], v[40:43]
	v_mfma_f32_16x16x32_bf16 v[36:39], v[170:173], v[186:189], v[36:39]
	v_mfma_f32_16x16x32_bf16 v[24:27], v[144:147], v[210:213], v[24:27]
	v_mfma_f32_16x16x32_bf16 v[20:23], v[170:173], v[210:213], v[20:23]
	v_mfma_f32_16x16x32_bf16 v[8:11], v[144:147], v[218:221], v[8:11]
	v_mfma_f32_16x16x32_bf16 v[4:7], v[170:173], v[218:221], v[4:7]
	s_setprio 0
	s_barrier
	s_add_i32 s73, 0, 0x18000
	s_add_i32 s74, 0, 0x1c000
	v_add_u32_e32 v136, s73, v195
	v_add_u32_e32 v170, s74, v195
	ds_read_b128 v[124:127], v136
	ds_read_b128 v[128:131], v136 offset:1024
	ds_read_b128 v[132:135], v136 offset:2048
	ds_read_b128 v[136:139], v136 offset:3072
	ds_read_b128 v[140:143], v170
	ds_read_b128 v[144:147], v170 offset:1024
	ds_read_b128 v[156:159], v170 offset:2048
	ds_read_b128 v[170:173], v170 offset:3072
	s_add_u32 s62, s62, 0x40000
	s_addc_u32 s63, s63, 0
	s_mov_b32 m0, s20
	ds_read_b128 v[174:177], v208 offset:32768
	ds_read_b128 v[178:181], v208 offset:33792
	ds_read_b128 v[182:185], v208 offset:34816
	ds_read_b128 v[186:189], v208 offset:35840
	ds_read_b128 v[190:193], v208 offset:36864
	ds_read_b128 v[210:213], v208 offset:37888
	ds_read_b128 v[214:217], v208 offset:38912
	ds_read_b128 v[218:221], v208 offset:39936
	global_load_lds_dwordx4 v164, s[62:63]
	s_mov_b32 m0, s21
	s_nop 0
	global_load_lds_dwordx4 v162, s[62:63]
	s_waitcnt vmcnt(8)
	s_waitcnt lgkmcnt(0)
	s_barrier
	s_setprio 1
	s_waitcnt lgkmcnt(0)
	v_mfma_f32_16x16x32_bf16 v[152:155], v[124:127], v[174:177], v[152:155]
	v_mfma_f32_16x16x32_bf16 v[148:151], v[132:135], v[174:177], v[148:151]
	v_mfma_f32_16x16x32_bf16 v[112:115], v[124:127], v[182:185], v[112:115]
	v_mfma_f32_16x16x32_bf16 v[108:111], v[132:135], v[182:185], v[108:111]
	v_mfma_f32_16x16x32_bf16 v[96:99], v[124:127], v[190:193], v[96:99]
	v_mfma_f32_16x16x32_bf16 v[92:95], v[132:135], v[190:193], v[92:95]
	v_mfma_f32_16x16x32_bf16 v[80:83], v[124:127], v[214:217], v[80:83]
	v_mfma_f32_16x16x32_bf16 v[76:79], v[132:135], v[214:217], v[76:79]
	v_mfma_f32_16x16x32_bf16 v[152:155], v[128:131], v[178:181], v[152:155]
	v_mfma_f32_16x16x32_bf16 v[148:151], v[136:139], v[178:181], v[148:151]
	v_mfma_f32_16x16x32_bf16 v[112:115], v[128:131], v[186:189], v[112:115]
	v_mfma_f32_16x16x32_bf16 v[108:111], v[136:139], v[186:189], v[108:111]
	v_mfma_f32_16x16x32_bf16 v[96:99], v[128:131], v[210:213], v[96:99]
	v_mfma_f32_16x16x32_bf16 v[92:95], v[136:139], v[210:213], v[92:95]
	v_mfma_f32_16x16x32_bf16 v[80:83], v[128:131], v[218:221], v[80:83]
	v_mfma_f32_16x16x32_bf16 v[76:79], v[136:139], v[218:221], v[76:79]
	s_setprio 0
	s_setprio 1
	v_mfma_f32_16x16x32_bf16 v[120:123], v[140:143], v[174:177], v[120:123]
	v_mfma_f32_16x16x32_bf16 v[116:119], v[156:159], v[174:177], v[116:119]
	v_mfma_f32_16x16x32_bf16 v[104:107], v[140:143], v[182:185], v[104:107]
	v_mfma_f32_16x16x32_bf16 v[100:103], v[156:159], v[182:185], v[100:103]
	v_mfma_f32_16x16x32_bf16 v[88:91], v[140:143], v[190:193], v[88:91]
	v_mfma_f32_16x16x32_bf16 v[84:87], v[156:159], v[190:193], v[84:87]
	v_mfma_f32_16x16x32_bf16 v[72:75], v[140:143], v[214:217], v[72:75]
	v_mfma_f32_16x16x32_bf16 v[68:71], v[156:159], v[214:217], v[68:71]
	v_mfma_f32_16x16x32_bf16 v[120:123], v[144:147], v[178:181], v[120:123]
	v_mfma_f32_16x16x32_bf16 v[116:119], v[170:173], v[178:181], v[116:119]
	v_mfma_f32_16x16x32_bf16 v[104:107], v[144:147], v[186:189], v[104:107]
	v_mfma_f32_16x16x32_bf16 v[100:103], v[170:173], v[186:189], v[100:103]
	v_mfma_f32_16x16x32_bf16 v[88:91], v[144:147], v[210:213], v[88:91]
	v_mfma_f32_16x16x32_bf16 v[84:87], v[170:173], v[210:213], v[84:87]
	v_mfma_f32_16x16x32_bf16 v[72:75], v[144:147], v[218:221], v[72:75]
	v_mfma_f32_16x16x32_bf16 v[68:71], v[170:173], v[218:221], v[68:71]
	s_setprio 0
	s_barrier
; #define PG8_STAGE(bufoff, gbase, voff) do { _Pragma("unroll") for (int _i = 0; _i < 2; ++_i) \
;         __builtin_amdgcn_global_load_lds((const unsigned*)((const char*)(gbase) + (voff)[_i]), (PG8_LAS unsigned*)(lds + (bufoff) + ldsw + _i * 8192), 16, 0, 0); } while (0)
; #define PG8_LDA(dst, b, h) do { _Pragma("unroll") for (int m = 0; m < 4; ++m) _Pragma("unroll") for (int k = 0; k < 2; ++k) dst[m][k] = *(const PG8_LAS bf16x8*)(lds + PG8_SA(b, h) + aoff + m * 2048 + k * 1024); } while (0)
; #define PG8_WAIT_V(n) asm volatile("s_waitcnt vmcnt(" #n ")" ::: "memory")
; #define PG8_WAIT_L(n) asm volatile("s_waitcnt lgkmcnt(" #n ")" ::: "memory")
; template <class Epi, class Sched, bool ALIGN_EPI = false, bool SP2 = false, bool FP8 = false, bool ABLK = false>
; __device__ __forceinline__ void gemm_phase(PG8_LAS unsigned char* lds, const Gemm g, const Sched& S, const Epi& E) {
;     ...
;         for (int t = 0; t < nt; t += 2) {
;             const bool last = (t == nt - 2);
;             const char* a1 = cA + (size_t)(t + 1) * kstepA;
;             const char* a2 = last ? nA : cA + (size_t)(t + 2) * kstepA; const char* b2 = last ? nB : cB + (size_t)(t + 2) * kstep;
;             const char* a3 = a2 + kstepA; const char* b3 = b2 + kstep;
;             if (last && has_next) S.a_ready(nxt);
;             if constexpr (SP2) {
;             PG8_LDB(B0, 0, 0); PG8_LDB(B1, 0, 1); PG8_SCHED; PG8_LDA(At, 0, 0); PG8_STAGE(PG8_SA(1, 1), a1 + hstepA, voffA);
;             PG8_WAIT_V8_UNLESS_FIRST(t); PG8_WAIT_L(0); PG8_BAR; PG8_MMA(0, 0, At, B0); PG8_MMA(0, 1, At, B1); PG8_BAR; PG8_SCHED;
;             PG8_LDA(At, 0, 1); PG8_STAGE(PG8_SB(0, 0), b2, voffB); PG8_STAGE(PG8_SB(0, 1), b2 + hstep, voffB); PG8_STAGE(PG8_SA(0, 0), a2, voffA);
;             PG8_WAIT_V8_UNLESS_FIRST(t); PG8_WAIT_L(0); PG8_BAR; PG8_MMA(1, 0, At, B0); PG8_MMA(1, 1, At, B1); PG8_BAR; PG8_SCHED;
;             PG8_LDB(B0, 1, 0); PG8_LDB(B1, 1, 1); PG8_SCHED; PG8_LDA(At, 1, 0); PG8_STAGE(PG8_SA(0, 1), a2 + hstepA, voffA);
;             PG8_WAIT_V(8); PG8_WAIT_L(0); PG8_BAR; PG8_MMA(0, 0, At, B0); PG8_MMA(0, 1, At, B1); PG8_BAR; PG8_SCHED;
;             PG8_LDA(At, 1, 1); PG8_STAGE(PG8_SB(1, 0), b3, voffB); PG8_STAGE(PG8_SB(1, 1), b3 + hstep, voffB); PG8_STAGE(PG8_SA(1, 0), a3, voffA);
;             PG8_WAIT_V(8); PG8_WAIT_L(0); PG8_BAR; PG8_MMA(1, 0, At, B0); PG8_MMA(1, 1, At, B1); PG8_BAR; PG8_SCHED;
	s_add_i32 s62, s73, s17
	v_lshl_add_u64 v[204:205], v[204:205], 0, s[34:35]
	s_mov_b32 m0, s62
	ds_read_b128 v[174:177], v208 offset:49152
	ds_read_b128 v[178:181], v208 offset:50176
	ds_read_b128 v[182:185], v208 offset:51200
	ds_read_b128 v[186:189], v208 offset:52224
	ds_read_b128 v[190:193], v208 offset:53248
	ds_read_b128 v[210:213], v208 offset:54272
	ds_read_b128 v[214:217], v208 offset:55296
	ds_read_b128 v[218:221], v208 offset:56320
	global_load_lds_dwordx4 v[204:205], off
	s_add_i32 m0, s62, 0x2000
	s_add_u32 s60, s60, 0x40080
	v_lshl_add_u64 v[204:205], v[206:207], 0, s[34:35]
	s_addc_u32 s61, s61, 0
	s_add_i32 s62, s74, s17
	global_load_lds_dwordx4 v[204:205], off
	s_mov_b32 m0, s62
	s_nop 0
	global_load_lds_dwordx4 v2, s[60:61]
	s_add_i32 m0, s62, 0x2000
	s_nop 0
	global_load_lds_dwordx4 v160, s[60:61]
	v_lshl_add_u64 v[204:205], v[222:223], 0, s[34:35]
	s_mov_b32 m0, s65
	s_nop 0
	global_load_lds_dwordx4 v[204:205], off
	v_lshl_add_u64 v[204:205], v[224:225], 0, s[34:35]
	s_mov_b32 m0, s66
	s_nop 0
	global_load_lds_dwordx4 v[204:205], off
	s_waitcnt vmcnt(8)
	s_waitcnt lgkmcnt(0)
	s_barrier
	s_setprio 1
	s_waitcnt lgkmcnt(0)
	v_mfma_f32_16x16x32_bf16 v[64:67], v[124:127], v[174:177], v[64:67]
	v_mfma_f32_16x16x32_bf16 v[60:63], v[132:135], v[174:177], v[60:63]
	v_mfma_f32_16x16x32_bf16 v[48:51], v[124:127], v[182:185], v[48:51]
	v_mfma_f32_16x16x32_bf16 v[44:47], v[132:135], v[182:185], v[44:47]
	v_mfma_f32_16x16x32_bf16 v[32:35], v[124:127], v[190:193], v[32:35]
	v_mfma_f32_16x16x32_bf16 v[28:31], v[132:135], v[190:193], v[28:31]
	v_mfma_f32_16x16x32_bf16 v[16:19], v[124:127], v[214:217], v[16:19]
	v_mfma_f32_16x16x32_bf16 v[12:15], v[132:135], v[214:217], v[12:15]
	v_mfma_f32_16x16x32_bf16 v[64:67], v[128:131], v[178:181], v[64:67]
	v_mfma_f32_16x16x32_bf16 v[60:63], v[136:139], v[178:181], v[60:63]
	v_mfma_f32_16x16x32_bf16 v[48:51], v[128:131], v[186:189], v[48:51]
	v_mfma_f32_16x16x32_bf16 v[44:47], v[136:139], v[186:189], v[44:47]
	v_mfma_f32_16x16x32_bf16 v[32:35], v[128:131], v[210:213], v[32:35]
	v_mfma_f32_16x16x32_bf16 v[28:31], v[136:139], v[210:213], v[28:31]
	v_mfma_f32_16x16x32_bf16 v[16:19], v[128:131], v[218:221], v[16:19]
	v_mfma_f32_16x16x32_bf16 v[12:15], v[136:139], v[218:221], v[12:15]
	s_setprio 0
	s_setprio 1
	v_mfma_f32_16x16x32_bf16 v[56:59], v[140:143], v[174:177], v[56:59]
	v_mfma_f32_16x16x32_bf16 v[52:55], v[156:159], v[174:177], v[52:55]
	v_mfma_f32_16x16x32_bf16 v[40:43], v[140:143], v[182:185], v[40:43]
	v_mfma_f32_16x16x32_bf16 v[36:39], v[156:159], v[182:185], v[36:39]
	v_mfma_f32_16x16x32_bf16 v[24:27], v[140:143], v[190:193], v[24:27]
	v_mfma_f32_16x16x32_bf16 v[20:23], v[156:159], v[190:193], v[20:23]
	v_mfma_f32_16x16x32_bf16 v[8:11], v[140:143], v[214:217], v[8:11]
	v_mfma_f32_16x16x32_bf16 v[4:7], v[156:159], v[214:217], v[4:7]
	v_mfma_f32_16x16x32_bf16 v[56:59], v[144:147], v[178:181], v[56:59]
	v_mfma_f32_16x16x32_bf16 v[52:55], v[170:173], v[178:181], v[52:55]
	v_mfma_f32_16x16x32_bf16 v[40:43], v[144:147], v[186:189], v[40:43]
	v_mfma_f32_16x16x32_bf16 v[36:39], v[170:173], v[186:189], v[36:39]
	v_mfma_f32_16x16x32_bf16 v[24:27], v[144:147], v[210:213], v[24:27]
	v_mfma_f32_16x16x32_bf16 v[20:23], v[170:173], v[210:213], v[20:23]
	v_mfma_f32_16x16x32_bf16 v[8:11], v[144:147], v[218:221], v[8:11]
	v_mfma_f32_16x16x32_bf16 v[4:7], v[170:173], v[218:221], v[4:7]
	s_setprio 0
	s_add_u32 s42, s42, 0x100
	s_addc_u32 s43, s43, 0
	s_add_u32 s70, s70, 0x100
	s_addc_u32 s71, s71, 0
	s_cmp_gt_u32 s72, 13
	s_mov_b32 s60, s72
	s_cbranch_scc1 .Lrot3_exit
	s_add_i32 s72, s60, 2
	s_add_u32 s61, s42, 0xfffc0080
	s_addc_u32 s62, s43, -1
	s_add_i32 s73, 0, 0x10000
	s_cmp_eq_u32 s60, 12
	s_cselect_b32 s63, s4, s62
	s_cselect_b32 s62, s5, s61
	s_cselect_b32 s61, s53, s71
	s_cselect_b32 s60, s55, s70
	s_add_i32 s76, 0, 0x14000
	v_add_u32_e32 v136, s73, v195
	v_add_u32_e32 v170, s76, v195
	s_barrier
	s_branch .Lrot3_body

; #define PG8_STAGE(bufoff, gbase, voff) do { _Pragma("unroll") for (int _i = 0; _i < 2; ++_i) \
;         __builtin_amdgcn_global_load_lds((const unsigned*)((const char*)(gbase) + (voff)[_i]), (PG8_LAS unsigned*)(lds + (bufoff) + ldsw + _i * 8192), 16, 0, 0); } while (0)
; #define PG8_LDA(dst, b, h) do { _Pragma("unroll") for (int m = 0; m < 4; ++m) _Pragma("unroll") for (int k = 0; k < 2; ++k) dst[m][k] = *(const PG8_LAS bf16x8*)(lds + PG8_SA(b, h) + aoff + m * 2048 + k * 1024); } while (0)
; #define PG8_LDB(dst, b, h) do { _Pragma("unroll") for (int n = 0; n < 2; ++n) _Pragma("unroll") for (int k = 0; k < 2; ++k) dst[n][k] = *(const PG8_LAS bf16x8*)(lds + PG8_SB(b, h) + boff + n * 2048 + k * 1024); } while (0)
; #define PG8_WAIT_V8_UNLESS_FIRST(t) asm volatile("s_cmp_eq_u32 %0, 0\n\ts_cbranch_scc1 .Lpg8skip%=\n\ts_waitcnt vmcnt(8)\n.Lpg8skip%=:" :: "s"(t) : "scc", "memory")
; #define PG8_WAIT_L(n) asm volatile("s_waitcnt lgkmcnt(" #n ")" ::: "memory")
; #define PG8_BAR __builtin_amdgcn_s_barrier()
; #define PG8_SCHED __builtin_amdgcn_sched_barrier(0)
; template <class Epi, class Sched, bool ALIGN_EPI = false, bool SP2 = false, bool FP8 = false, bool ABLK = false>
; __device__ __forceinline__ void gemm_phase(PG8_LAS unsigned char* lds, const Gemm g, const Sched& S, const Epi& E) {
;     ...
;             PG8_LDB(B0, 0, 0); PG8_LDB(B1, 0, 1); PG8_SCHED; PG8_LDA(At, 0, 0); PG8_STAGE(PG8_SA(1, 1), a1 + hstepA, voffA);
;             PG8_WAIT_V8_UNLESS_FIRST(t); PG8_WAIT_L(0); PG8_BAR; PG8_MMA(0, 0, At, B0); PG8_MMA(0, 1, At, B1); PG8_BAR; PG8_SCHED;
.Lrot4_body:
	ds_read_b128 v[28:31], v4
	ds_read_b128 v[32:35], v4 offset:1024
	ds_read_b128 v[20:23], v4 offset:2048
	ds_read_b128 v[24:27], v4 offset:3072
	ds_read_b128 v[12:15], v8
	ds_read_b128 v[16:19], v8 offset:1024
	ds_read_b128 v[4:7], v8 offset:2048
	ds_read_b128 v[8:11], v8 offset:3072
	s_add_i32 m0, s18, 0xc000
	ds_read_b128 v[174:177], v184
	ds_read_b128 v[178:181], v184 offset:1024
	ds_read_b128 v[186:189], v184 offset:2048
	ds_read_b128 v[190:193], v184 offset:3072
	ds_read_b128 v[208:211], v184 offset:4096
	ds_read_b128 v[212:215], v184 offset:5120
	ds_read_b128 v[216:219], v184 offset:6144
	ds_read_b128 v[220:223], v184 offset:7168
	global_load_lds_dwordx4 v170, s[56:57]
	s_add_i32 m0, s18, 0xe000
	s_nop 0
	global_load_lds_dwordx4 v172, s[56:57]
	s_cmp_eq_u32 s69, 0
	s_cbranch_scc1 .Lpg8skip8
	s_waitcnt vmcnt(8)

; #define PG8_STAGE(bufoff, gbase, voff) do { _Pragma("unroll") for (int _i = 0; _i < 2; ++_i) \
;         __builtin_amdgcn_global_load_lds((const unsigned*)((const char*)(gbase) + (voff)[_i]), (PG8_LAS unsigned*)(lds + (bufoff) + ldsw + _i * 8192), 16, 0, 0); } while (0)
; #define PG8_LDA(dst, b, h) do { _Pragma("unroll") for (int m = 0; m < 4; ++m) _Pragma("unroll") for (int k = 0; k < 2; ++k) dst[m][k] = *(const PG8_LAS bf16x8*)(lds + PG8_SA(b, h) + aoff + m * 2048 + k * 1024); } while (0)
; #define PG8_LDB(dst, b, h) do { _Pragma("unroll") for (int n = 0; n < 2; ++n) _Pragma("unroll") for (int k = 0; k < 2; ++k) dst[n][k] = *(const PG8_LAS bf16x8*)(lds + PG8_SB(b, h) + boff + n * 2048 + k * 1024); } while (0)
; #define PG8_WAIT_V(n) asm volatile("s_waitcnt vmcnt(" #n ")" ::: "memory")
; #define PG8_WAIT_V8_UNLESS_FIRST(t) asm volatile("s_cmp_eq_u32 %0, 0\n\ts_cbranch_scc1 .Lpg8skip%=\n\ts_waitcnt vmcnt(8)\n.Lpg8skip%=:" :: "s"(t) : "scc", "memory")
; #define PG8_WAIT_L(n) asm volatile("s_waitcnt lgkmcnt(" #n ")" ::: "memory")
; #define PG8_BAR __builtin_amdgcn_s_barrier()
; #define PG8_SCHED __builtin_amdgcn_sched_barrier(0)
; template <class Epi, class Sched, bool ALIGN_EPI = false, bool SP2 = false, bool FP8 = false, bool ABLK = false>
; __device__ __forceinline__ void gemm_phase(PG8_LAS unsigned char* lds, const Gemm g, const Sched& S, const Epi& E) {
;     ...
;             PG8_WAIT_V8_UNLESS_FIRST(t); PG8_WAIT_L(0); PG8_BAR; PG8_MMA(1, 0, At, B0); PG8_MMA(1, 1, At, B1); PG8_BAR; PG8_SCHED;
;             PG8_LDB(B0, 1, 0); PG8_LDB(B1, 1, 1); PG8_SCHED; PG8_LDA(At, 1, 0); PG8_STAGE(PG8_SA(0, 1), a2 + hstepA, voffA);
;             PG8_WAIT_V(8); PG8_WAIT_L(0); PG8_BAR; PG8_MMA(0, 0, At, B0); PG8_MMA(0, 1, At, B1); PG8_BAR; PG8_SCHED;
.Lpg8skip9:
	s_waitcnt lgkmcnt(0)
	s_barrier
	s_setprio 1
	s_waitcnt lgkmcnt(0)
	v_mfma_scale_f32_16x16x128_f8f6f4 v[96:99], v[28:35], v[186:193], v[96:99], v245, v245 op_sel_hi:[0,0,0]
	v_mfma_scale_f32_16x16x128_f8f6f4 v[92:95], v[20:27], v[186:193], v[92:95], v245, v245 op_sel_hi:[0,0,0]
	v_mfma_scale_f32_16x16x128_f8f6f4 v[80:83], v[28:35], v[208:215], v[80:83], v245, v245 op_sel_hi:[0,0,0]
	v_mfma_scale_f32_16x16x128_f8f6f4 v[76:79], v[20:27], v[208:215], v[76:79], v245, v245 op_sel_hi:[0,0,0]
	v_mfma_scale_f32_16x16x128_f8f6f4 v[64:67], v[28:35], v[216:223], v[64:67], v245, v245 op_sel_hi:[0,0,0]
	v_mfma_scale_f32_16x16x128_f8f6f4 v[60:63], v[20:27], v[216:223], v[60:63], v245, v245 op_sel_hi:[0,0,0]
	v_mfma_scale_f32_16x16x128_f8f6f4 v[48:51], v[28:35], v[228:235], v[48:51], v245, v245 op_sel_hi:[0,0,0]
	v_mfma_scale_f32_16x16x128_f8f6f4 v[44:47], v[20:27], v[228:235], v[44:47], v245, v245 op_sel_hi:[0,0,0]
	s_setprio 0
	s_setprio 1
	v_mfma_scale_f32_16x16x128_f8f6f4 v[88:91], v[12:19], v[186:193], v[88:91], v245, v245 op_sel_hi:[0,0,0]
	v_mfma_scale_f32_16x16x128_f8f6f4 v[84:87], v[4:11], v[186:193], v[84:87], v245, v245 op_sel_hi:[0,0,0]
	v_mfma_scale_f32_16x16x128_f8f6f4 v[72:75], v[12:19], v[208:215], v[72:75], v245, v245 op_sel_hi:[0,0,0]
	v_mfma_scale_f32_16x16x128_f8f6f4 v[68:71], v[4:11], v[208:215], v[68:71], v245, v245 op_sel_hi:[0,0,0]
	v_mfma_scale_f32_16x16x128_f8f6f4 v[56:59], v[12:19], v[216:223], v[56:59], v245, v245 op_sel_hi:[0,0,0]
	v_mfma_scale_f32_16x16x128_f8f6f4 v[52:55], v[4:11], v[216:223], v[52:55], v245, v245 op_sel_hi:[0,0,0]
	v_mfma_scale_f32_16x16x128_f8f6f4 v[40:43], v[12:19], v[228:235], v[40:43], v245, v245 op_sel_hi:[0,0,0]
	v_mfma_scale_f32_16x16x128_f8f6f4 v[36:39], v[4:11], v[228:235], v[36:39], v245, v245 op_sel_hi:[0,0,0]
	s_setprio 0
	s_barrier
	s_add_i32 s70, 0, 0x18000
	s_add_i32 s71, 0, 0x1c000
	v_add_u32_e32 v16, s70, v183
	v_add_u32_e32 v32, s71, v183
	ds_read_b128 v[4:7], v16
	ds_read_b128 v[8:11], v16 offset:1024
	ds_read_b128 v[12:15], v16 offset:2048
	ds_read_b128 v[16:19], v16 offset:3072
	ds_read_b128 v[20:23], v32
	ds_read_b128 v[24:27], v32 offset:1024
	ds_read_b128 v[28:31], v32 offset:2048
	ds_read_b128 v[32:35], v32 offset:3072
	s_add_u32 s60, s60, 0x20000
	s_addc_u32 s61, s61, 0
	s_mov_b32 m0, s20
	ds_read_b128 v[186:189], v184 offset:32768
	ds_read_b128 v[190:193], v184 offset:33792
	ds_read_b128 v[208:211], v184 offset:34816
	ds_read_b128 v[212:215], v184 offset:35840
	ds_read_b128 v[216:219], v184 offset:36864
	ds_read_b128 v[220:223], v184 offset:37888
	ds_read_b128 v[228:231], v184 offset:38912
	ds_read_b128 v[232:235], v184 offset:39936
	global_load_lds_dwordx4 v168, s[60:61]
	s_mov_b32 m0, s21
	s_nop 0
	global_load_lds_dwordx4 v166, s[60:61]
	s_waitcnt vmcnt(8)
	s_waitcnt lgkmcnt(0)
	s_barrier
	s_setprio 1
	s_waitcnt lgkmcnt(0)
	v_mfma_scale_f32_16x16x128_f8f6f4 v[160:163], v[4:11], v[186:193], v[160:163], v245, v245 op_sel_hi:[0,0,0]
	v_mfma_scale_f32_16x16x128_f8f6f4 v[156:159], v[12:19], v[186:193], v[156:159], v245, v245 op_sel_hi:[0,0,0]
	v_mfma_scale_f32_16x16x128_f8f6f4 v[144:147], v[4:11], v[208:215], v[144:147], v245, v245 op_sel_hi:[0,0,0]
	v_mfma_scale_f32_16x16x128_f8f6f4 v[140:143], v[12:19], v[208:215], v[140:143], v245, v245 op_sel_hi:[0,0,0]
	v_mfma_scale_f32_16x16x128_f8f6f4 v[128:131], v[4:11], v[216:223], v[128:131], v245, v245 op_sel_hi:[0,0,0]
	v_mfma_scale_f32_16x16x128_f8f6f4 v[124:127], v[12:19], v[216:223], v[124:127], v245, v245 op_sel_hi:[0,0,0]
	v_mfma_scale_f32_16x16x128_f8f6f4 v[112:115], v[4:11], v[228:235], v[112:115], v245, v245 op_sel_hi:[0,0,0]
	v_mfma_scale_f32_16x16x128_f8f6f4 v[108:111], v[12:19], v[228:235], v[108:111], v245, v245 op_sel_hi:[0,0,0]
	s_setprio 0
	s_setprio 1
	v_mfma_scale_f32_16x16x128_f8f6f4 v[152:155], v[20:27], v[186:193], v[152:155], v245, v245 op_sel_hi:[0,0,0]
	v_mfma_scale_f32_16x16x128_f8f6f4 v[148:151], v[28:35], v[186:193], v[148:151], v245, v245 op_sel_hi:[0,0,0]
	v_mfma_scale_f32_16x16x128_f8f6f4 v[136:139], v[20:27], v[208:215], v[136:139], v245, v245 op_sel_hi:[0,0,0]
	v_mfma_scale_f32_16x16x128_f8f6f4 v[132:135], v[28:35], v[208:215], v[132:135], v245, v245 op_sel_hi:[0,0,0]
	v_mfma_scale_f32_16x16x128_f8f6f4 v[120:123], v[20:27], v[216:223], v[120:123], v245, v245 op_sel_hi:[0,0,0]
	v_mfma_scale_f32_16x16x128_f8f6f4 v[116:119], v[28:35], v[216:223], v[116:119], v245, v245 op_sel_hi:[0,0,0]
	v_mfma_scale_f32_16x16x128_f8f6f4 v[104:107], v[20:27], v[228:235], v[104:107], v245, v245 op_sel_hi:[0,0,0]
	v_mfma_scale_f32_16x16x128_f8f6f4 v[100:103], v[28:35], v[228:235], v[100:103], v245, v245 op_sel_hi:[0,0,0]
	s_setprio 0
	s_barrier
; #define PG8_STAGE(bufoff, gbase, voff) do { _Pragma("unroll") for (int _i = 0; _i < 2; ++_i) \
;         __builtin_amdgcn_global_load_lds((const unsigned*)((const char*)(gbase) + (voff)[_i]), (PG8_LAS unsigned*)(lds + (bufoff) + ldsw + _i * 8192), 16, 0, 0); } while (0)
; #define PG8_WAIT_V(n) asm volatile("s_waitcnt vmcnt(" #n ")" ::: "memory")
; #define PG8_WAIT_L(n) asm volatile("s_waitcnt lgkmcnt(" #n ")" ::: "memory")
; #define PG8_BAR __builtin_amdgcn_s_barrier()
; template <class Epi, class Sched, bool ALIGN_EPI = false, bool SP2 = false, bool FP8 = false, bool ABLK = false>
; __device__ __forceinline__ void gemm_phase(PG8_LAS unsigned char* lds, const Gemm g, const Sched& S, const Epi& E) {
;     ...
;         for (int t = 0; t < nt; t += 2) {
;             const bool last = (t == nt - 2);
;             const char* a1 = cA + (size_t)(t + 1) * kstepA;
;             const char* a2 = last ? nA : cA + (size_t)(t + 2) * kstepA; const char* b2 = last ? nB : cB + (size_t)(t + 2) * kstep;
;             const char* a3 = a2 + kstepA; const char* b3 = b2 + kstep;
;             if (last && has_next) S.a_ready(nxt);
;             if constexpr (SP2) {
;             PG8_LDB(B0, 0, 0); PG8_LDB(B1, 0, 1); PG8_SCHED; PG8_LDA(At, 0, 0); PG8_STAGE(PG8_SA(1, 1), a1 + hstepA, voffA);
;             PG8_WAIT_V8_UNLESS_FIRST(t); PG8_WAIT_L(0); PG8_BAR; PG8_MMA(0, 0, At, B0); PG8_MMA(0, 1, At, B1); PG8_BAR; PG8_SCHED;
;             PG8_LDA(At, 0, 1); PG8_STAGE(PG8_SB(0, 0), b2, voffB); PG8_STAGE(PG8_SB(0, 1), b2 + hstep, voffB); PG8_STAGE(PG8_SA(0, 0), a2, voffA);
;             PG8_WAIT_V8_UNLESS_FIRST(t); PG8_WAIT_L(0); PG8_BAR; PG8_MMA(1, 0, At, B0); PG8_MMA(1, 1, At, B1); PG8_BAR; PG8_SCHED;
;             PG8_LDB(B0, 1, 0); PG8_LDB(B1, 1, 1); PG8_SCHED; PG8_LDA(At, 1, 0); PG8_STAGE(PG8_SA(0, 1), a2 + hstepA, voffA);
;             PG8_WAIT_V(8); PG8_WAIT_L(0); PG8_BAR; PG8_MMA(0, 0, At, B0); PG8_MMA(0, 1, At, B1); PG8_BAR; PG8_SCHED;
;             PG8_LDA(At, 1, 1); PG8_STAGE(PG8_SB(1, 0), b3, voffB); PG8_STAGE(PG8_SB(1, 1), b3 + hstep, voffB); PG8_STAGE(PG8_SA(1, 0), a3, voffA);
;             PG8_WAIT_V(8); PG8_WAIT_L(0); PG8_BAR; PG8_MMA(1, 0, At, B0); PG8_MMA(1, 1, At, B1); PG8_BAR; PG8_SCHED;
;     ...
;         if constexpr (SP2) PG8_WAIT_V(0);
;         if constexpr (FP8) asm volatile("s_nop 15\n\ts_nop 15" ::: "memory");
;         if constexpr (ALIGN_EPI) { if (wr == 0) PG8_BAR; }
	s_add_i32 s60, s70, s17
	v_lshl_add_u64 v[174:175], v[174:175], 0, s[34:35]
	s_mov_b32 m0, s60
	ds_read_b128 v[186:189], v184 offset:49152
	ds_read_b128 v[190:193], v184 offset:50176
	ds_read_b128 v[208:211], v184 offset:51200
	ds_read_b128 v[212:215], v184 offset:52224
	ds_read_b128 v[216:219], v184 offset:53248
	ds_read_b128 v[220:223], v184 offset:54272
	ds_read_b128 v[228:231], v184 offset:55296
	ds_read_b128 v[232:235], v184 offset:56320
	global_load_lds_dwordx4 v[174:175], off
	s_add_i32 m0, s60, 0x2000
	s_add_u32 s58, s58, 0x20080
	v_lshl_add_u64 v[174:175], v[176:177], 0, s[34:35]
	s_addc_u32 s59, s59, 0
	s_add_i32 s60, s71, s17
	global_load_lds_dwordx4 v[174:175], off
	s_mov_b32 m0, s60
	s_nop 0
	global_load_lds_dwordx4 v2, s[58:59]
	s_add_i32 m0, s60, 0x2000
	s_nop 0
	global_load_lds_dwordx4 v164, s[58:59]
	v_lshl_add_u64 v[174:175], v[178:179], 0, s[34:35]
	s_mov_b32 m0, s62
	s_nop 0
	global_load_lds_dwordx4 v[174:175], off
	v_lshl_add_u64 v[174:175], v[180:181], 0, s[34:35]
	s_mov_b32 m0, s63
	s_nop 0
	global_load_lds_dwordx4 v[174:175], off
	s_waitcnt vmcnt(8)
	s_waitcnt lgkmcnt(0)
	s_barrier
	s_setprio 1
	s_waitcnt lgkmcnt(0)
	v_mfma_scale_f32_16x16x128_f8f6f4 v[96:99], v[4:11], v[186:193], v[96:99], v245, v245 op_sel_hi:[0,0,0]
	v_mfma_scale_f32_16x16x128_f8f6f4 v[92:95], v[12:19], v[186:193], v[92:95], v245, v245 op_sel_hi:[0,0,0]
	v_mfma_scale_f32_16x16x128_f8f6f4 v[80:83], v[4:11], v[208:215], v[80:83], v245, v245 op_sel_hi:[0,0,0]
	v_mfma_scale_f32_16x16x128_f8f6f4 v[76:79], v[12:19], v[208:215], v[76:79], v245, v245 op_sel_hi:[0,0,0]
	v_mfma_scale_f32_16x16x128_f8f6f4 v[64:67], v[4:11], v[216:223], v[64:67], v245, v245 op_sel_hi:[0,0,0]
	v_mfma_scale_f32_16x16x128_f8f6f4 v[60:63], v[12:19], v[216:223], v[60:63], v245, v245 op_sel_hi:[0,0,0]
	v_mfma_scale_f32_16x16x128_f8f6f4 v[48:51], v[4:11], v[228:235], v[48:51], v245, v245 op_sel_hi:[0,0,0]
	v_mfma_scale_f32_16x16x128_f8f6f4 v[44:47], v[12:19], v[228:235], v[44:47], v245, v245 op_sel_hi:[0,0,0]
	s_setprio 0
	s_setprio 1
	v_mfma_scale_f32_16x16x128_f8f6f4 v[88:91], v[20:27], v[186:193], v[88:91], v245, v245 op_sel_hi:[0,0,0]
	v_mfma_scale_f32_16x16x128_f8f6f4 v[84:87], v[28:35], v[186:193], v[84:87], v245, v245 op_sel_hi:[0,0,0]
	v_mfma_scale_f32_16x16x128_f8f6f4 v[72:75], v[20:27], v[208:215], v[72:75], v245, v245 op_sel_hi:[0,0,0]
	v_mfma_scale_f32_16x16x128_f8f6f4 v[68:71], v[28:35], v[208:215], v[68:71], v245, v245 op_sel_hi:[0,0,0]
	v_mfma_scale_f32_16x16x128_f8f6f4 v[56:59], v[20:27], v[216:223], v[56:59], v245, v245 op_sel_hi:[0,0,0]
	v_mfma_scale_f32_16x16x128_f8f6f4 v[52:55], v[28:35], v[216:223], v[52:55], v245, v245 op_sel_hi:[0,0,0]
	v_mfma_scale_f32_16x16x128_f8f6f4 v[40:43], v[20:27], v[228:235], v[40:43], v245, v245 op_sel_hi:[0,0,0]
	v_mfma_scale_f32_16x16x128_f8f6f4 v[36:39], v[28:35], v[228:235], v[36:39], v245, v245 op_sel_hi:[0,0,0]
	s_setprio 0
	s_add_u32 s56, s56, 0x100
	s_addc_u32 s57, s57, 0
	s_add_u32 s67, s67, 0x100
	s_addc_u32 s68, s68, 0
	s_cmp_gt_u32 s69, 5
	s_mov_b32 s58, s69
	s_cbranch_scc1 .Lrot4_exit
	s_add_i32 s69, s58, 2
	s_add_u32 s59, s56, 0xfffe0080
	s_addc_u32 s60, s57, -1
	s_add_i32 s70, 0, 0x10000
	s_cmp_eq_u32 s58, 4
	s_cselect_b32 s61, s4, s60
	s_cselect_b32 s60, s5, s59
	s_cselect_b32 s59, s49, s68
	s_cselect_b32 s58, s51, s67
	s_add_i32 s71, 0, 0x14000
	v_add_u32_e32 v4, s70, v183
	v_add_u32_e32 v8, s71, v183
	s_barrier
	s_branch .Lrot4_body
.Lrot4_exit:
	s_barrier
	s_waitcnt vmcnt(0)
	s_nop 15
	s_nop 15
	s_and_b64 vcc, exec, s[46:47]
	s_cbranch_vccz .LBB0_1501
	s_barrier

; #define PG8_STAGE(bufoff, gbase, voff) do { _Pragma("unroll") for (int _i = 0; _i < 2; ++_i) \
;         __builtin_amdgcn_global_load_lds((const unsigned*)((const char*)(gbase) + (voff)[_i]), (PG8_LAS unsigned*)(lds + (bufoff) + ldsw + _i * 8192), 16, 0, 0); } while (0)
; #define PG8_LDA(dst, b, h) do { _Pragma("unroll") for (int m = 0; m < 4; ++m) _Pragma("unroll") for (int k = 0; k < 2; ++k) dst[m][k] = *(const PG8_LAS bf16x8*)(lds + PG8_SA(b, h) + aoff + m * 2048 + k * 1024); } while (0)
; #define PG8_LDB(dst, b, h) do { _Pragma("unroll") for (int n = 0; n < 2; ++n) _Pragma("unroll") for (int k = 0; k < 2; ++k) dst[n][k] = *(const PG8_LAS bf16x8*)(lds + PG8_SB(b, h) + boff + n * 2048 + k * 1024); } while (0)
; #define PG8_WAIT_V8_UNLESS_FIRST(t) asm volatile("s_cmp_eq_u32 %0, 0\n\ts_cbranch_scc1 .Lpg8skip%=\n\ts_waitcnt vmcnt(8)\n.Lpg8skip%=:" :: "s"(t) : "scc", "memory")
; #define PG8_WAIT_L(n) asm volatile("s_waitcnt lgkmcnt(" #n ")" ::: "memory")
; #define PG8_BAR __builtin_amdgcn_s_barrier()
; #define PG8_SCHED __builtin_amdgcn_sched_barrier(0)
; template <class Epi, class Sched, bool ALIGN_EPI = false, bool SP2 = false, bool FP8 = false, bool ABLK = false>
; __device__ __forceinline__ void gemm_phase(PG8_LAS unsigned char* lds, const Gemm g, const Sched& S, const Epi& E) {
;     ...
;             PG8_LDB(B0, 0, 0); PG8_LDB(B1, 0, 1); PG8_SCHED; PG8_LDA(At, 0, 0); PG8_STAGE(PG8_SA(1, 1), a1 + hstepA, voffA);
;             PG8_WAIT_V8_UNLESS_FIRST(t); PG8_WAIT_L(0); PG8_BAR; PG8_MMA(0, 0, At, B0); PG8_MMA(0, 1, At, B1); PG8_BAR; PG8_SCHED;
.Lrot5_body:
	ds_read_b128 v[28:31], v4
	ds_read_b128 v[32:35], v4 offset:1024
	ds_read_b128 v[20:23], v4 offset:2048
	ds_read_b128 v[24:27], v4 offset:3072
	ds_read_b128 v[12:15], v8
	ds_read_b128 v[16:19], v8 offset:1024
	s_waitcnt lgkmcnt(0)
	ds_read_b128 v[4:7], v8 offset:2048
	ds_read_b128 v[8:11], v8 offset:3072
	s_add_i32 m0, s18, 0xc000
	ds_read_b128 v[174:177], v208
	ds_read_b128 v[178:181], v208 offset:1024
	ds_read_b128 v[182:185], v208 offset:2048
	ds_read_b128 v[186:189], v208 offset:3072
	ds_read_b128 v[210:213], v208 offset:4096
	ds_read_b128 v[214:217], v208 offset:5120
	ds_read_b128 v[218:221], v208 offset:6144
	ds_read_b128 v[222:225], v208 offset:7168
	global_load_lds_dwordx4 v170, s[42:43]
	s_add_i32 m0, s18, 0xe000
	s_nop 0
	global_load_lds_dwordx4 v172, s[42:43]
	s_cmp_eq_u32 s72, 0
	s_cbranch_scc1 .Lpg8skip10
	s_waitcnt vmcnt(8)

; #define PG8_STAGE(bufoff, gbase, voff) do { _Pragma("unroll") for (int _i = 0; _i < 2; ++_i) \
;         __builtin_amdgcn_global_load_lds((const unsigned*)((const char*)(gbase) + (voff)[_i]), (PG8_LAS unsigned*)(lds + (bufoff) + ldsw + _i * 8192), 16, 0, 0); } while (0)
; #define PG8_LDA(dst, b, h) do { _Pragma("unroll") for (int m = 0; m < 4; ++m) _Pragma("unroll") for (int k = 0; k < 2; ++k) dst[m][k] = *(const PG8_LAS bf16x8*)(lds + PG8_SA(b, h) + aoff + m * 2048 + k * 1024); } while (0)
; #define PG8_LDB(dst, b, h) do { _Pragma("unroll") for (int n = 0; n < 2; ++n) _Pragma("unroll") for (int k = 0; k < 2; ++k) dst[n][k] = *(const PG8_LAS bf16x8*)(lds + PG8_SB(b, h) + boff + n * 2048 + k * 1024); } while (0)
; #define PG8_WAIT_V(n) asm volatile("s_waitcnt vmcnt(" #n ")" ::: "memory")
; #define PG8_WAIT_V8_UNLESS_FIRST(t) asm volatile("s_cmp_eq_u32 %0, 0\n\ts_cbranch_scc1 .Lpg8skip%=\n\ts_waitcnt vmcnt(8)\n.Lpg8skip%=:" :: "s"(t) : "scc", "memory")
; #define PG8_WAIT_L(n) asm volatile("s_waitcnt lgkmcnt(" #n ")" ::: "memory")
; #define PG8_BAR __builtin_amdgcn_s_barrier()
; #define PG8_SCHED __builtin_amdgcn_sched_barrier(0)
; template <class Epi, class Sched, bool ALIGN_EPI = false, bool SP2 = false, bool FP8 = false, bool ABLK = false>
; __device__ __forceinline__ void gemm_phase(PG8_LAS unsigned char* lds, const Gemm g, const Sched& S, const Epi& E) {
;     ...
;             PG8_WAIT_V8_UNLESS_FIRST(t); PG8_WAIT_L(0); PG8_BAR; PG8_MMA(1, 0, At, B0); PG8_MMA(1, 1, At, B1); PG8_BAR; PG8_SCHED;
;             PG8_LDB(B0, 1, 0); PG8_LDB(B1, 1, 1); PG8_SCHED; PG8_LDA(At, 1, 0); PG8_STAGE(PG8_SA(0, 1), a2 + hstepA, voffA);
;             PG8_WAIT_V(8); PG8_WAIT_L(0); PG8_BAR; PG8_MMA(0, 0, At, B0); PG8_MMA(0, 1, At, B1); PG8_BAR; PG8_SCHED;
.Lpg8skip11:
	s_waitcnt lgkmcnt(0)
	s_barrier
	s_setprio 1
	s_waitcnt lgkmcnt(0)
	v_mfma_scale_f32_16x16x128_f8f6f4 v[96:99], v[28:35], v[182:189], v[96:99], v245, v245 op_sel_hi:[0,0,0]
	v_mfma_scale_f32_16x16x128_f8f6f4 v[92:95], v[20:27], v[182:189], v[92:95], v245, v245 op_sel_hi:[0,0,0]
	v_mfma_scale_f32_16x16x128_f8f6f4 v[80:83], v[28:35], v[210:217], v[80:83], v245, v245 op_sel_hi:[0,0,0]
	v_mfma_scale_f32_16x16x128_f8f6f4 v[76:79], v[20:27], v[210:217], v[76:79], v245, v245 op_sel_hi:[0,0,0]
	v_mfma_scale_f32_16x16x128_f8f6f4 v[64:67], v[28:35], v[218:225], v[64:67], v245, v245 op_sel_hi:[0,0,0]
	v_mfma_scale_f32_16x16x128_f8f6f4 v[60:63], v[20:27], v[218:225], v[60:63], v245, v245 op_sel_hi:[0,0,0]
	v_mfma_scale_f32_16x16x128_f8f6f4 v[48:51], v[28:35], v[228:235], v[48:51], v245, v245 op_sel_hi:[0,0,0]
	v_mfma_scale_f32_16x16x128_f8f6f4 v[44:47], v[20:27], v[228:235], v[44:47], v245, v245 op_sel_hi:[0,0,0]
	s_setprio 0
	s_setprio 1
	v_mfma_scale_f32_16x16x128_f8f6f4 v[88:91], v[12:19], v[182:189], v[88:91], v245, v245 op_sel_hi:[0,0,0]
	v_mfma_scale_f32_16x16x128_f8f6f4 v[84:87], v[4:11], v[182:189], v[84:87], v245, v245 op_sel_hi:[0,0,0]
	v_mfma_scale_f32_16x16x128_f8f6f4 v[72:75], v[12:19], v[210:217], v[72:75], v245, v245 op_sel_hi:[0,0,0]
	v_mfma_scale_f32_16x16x128_f8f6f4 v[68:71], v[4:11], v[210:217], v[68:71], v245, v245 op_sel_hi:[0,0,0]
	v_mfma_scale_f32_16x16x128_f8f6f4 v[56:59], v[12:19], v[218:225], v[56:59], v245, v245 op_sel_hi:[0,0,0]
	v_mfma_scale_f32_16x16x128_f8f6f4 v[52:55], v[4:11], v[218:225], v[52:55], v245, v245 op_sel_hi:[0,0,0]
	v_mfma_scale_f32_16x16x128_f8f6f4 v[40:43], v[12:19], v[228:235], v[40:43], v245, v245 op_sel_hi:[0,0,0]
	v_mfma_scale_f32_16x16x128_f8f6f4 v[36:39], v[4:11], v[228:235], v[36:39], v245, v245 op_sel_hi:[0,0,0]
	s_setprio 0
	s_barrier
	s_add_i32 s73, 0, 0x18000
	s_add_i32 s74, 0, 0x1c000
	v_add_u32_e32 v16, s73, v195
	v_add_u32_e32 v32, s74, v195
	ds_read_b128 v[4:7], v16
	ds_read_b128 v[8:11], v16 offset:1024
	ds_read_b128 v[12:15], v16 offset:2048
	ds_read_b128 v[16:19], v16 offset:3072
	ds_read_b128 v[20:23], v32
	ds_read_b128 v[24:27], v32 offset:1024
	ds_read_b128 v[28:31], v32 offset:2048
	ds_read_b128 v[32:35], v32 offset:3072
	s_add_u32 s62, s62, 0x20000
	s_addc_u32 s63, s63, 0
	s_mov_b32 m0, s20
	ds_read_b128 v[182:185], v208 offset:32768
	ds_read_b128 v[186:189], v208 offset:33792
	ds_read_b128 v[210:213], v208 offset:34816
	ds_read_b128 v[214:217], v208 offset:35840
	ds_read_b128 v[218:221], v208 offset:36864
	ds_read_b128 v[222:225], v208 offset:37888
	ds_read_b128 v[228:231], v208 offset:38912
	ds_read_b128 v[232:235], v208 offset:39936
	global_load_lds_dwordx4 v168, s[62:63]
	s_mov_b32 m0, s21
	s_nop 0
	global_load_lds_dwordx4 v166, s[62:63]
	s_waitcnt vmcnt(8)
	s_waitcnt lgkmcnt(0)
	s_barrier
	s_setprio 1
	s_waitcnt lgkmcnt(0)
	v_mfma_scale_f32_16x16x128_f8f6f4 v[160:163], v[4:11], v[182:189], v[160:163], v245, v245 op_sel_hi:[0,0,0]
	v_mfma_scale_f32_16x16x128_f8f6f4 v[156:159], v[12:19], v[182:189], v[156:159], v245, v245 op_sel_hi:[0,0,0]
	v_mfma_scale_f32_16x16x128_f8f6f4 v[144:147], v[4:11], v[210:217], v[144:147], v245, v245 op_sel_hi:[0,0,0]
	v_mfma_scale_f32_16x16x128_f8f6f4 v[140:143], v[12:19], v[210:217], v[140:143], v245, v245 op_sel_hi:[0,0,0]
	v_mfma_scale_f32_16x16x128_f8f6f4 v[128:131], v[4:11], v[218:225], v[128:131], v245, v245 op_sel_hi:[0,0,0]
	v_mfma_scale_f32_16x16x128_f8f6f4 v[124:127], v[12:19], v[218:225], v[124:127], v245, v245 op_sel_hi:[0,0,0]
	v_mfma_scale_f32_16x16x128_f8f6f4 v[112:115], v[4:11], v[228:235], v[112:115], v245, v245 op_sel_hi:[0,0,0]
	v_mfma_scale_f32_16x16x128_f8f6f4 v[108:111], v[12:19], v[228:235], v[108:111], v245, v245 op_sel_hi:[0,0,0]
	s_setprio 0
	s_setprio 1
	v_mfma_scale_f32_16x16x128_f8f6f4 v[152:155], v[20:27], v[182:189], v[152:155], v245, v245 op_sel_hi:[0,0,0]
	v_mfma_scale_f32_16x16x128_f8f6f4 v[148:151], v[28:35], v[182:189], v[148:151], v245, v245 op_sel_hi:[0,0,0]
	v_mfma_scale_f32_16x16x128_f8f6f4 v[136:139], v[20:27], v[210:217], v[136:139], v245, v245 op_sel_hi:[0,0,0]
	v_mfma_scale_f32_16x16x128_f8f6f4 v[132:135], v[28:35], v[210:217], v[132:135], v245, v245 op_sel_hi:[0,0,0]
	v_mfma_scale_f32_16x16x128_f8f6f4 v[120:123], v[20:27], v[218:225], v[120:123], v245, v245 op_sel_hi:[0,0,0]
	v_mfma_scale_f32_16x16x128_f8f6f4 v[116:119], v[28:35], v[218:225], v[116:119], v245, v245 op_sel_hi:[0,0,0]
	v_mfma_scale_f32_16x16x128_f8f6f4 v[104:107], v[20:27], v[228:235], v[104:107], v245, v245 op_sel_hi:[0,0,0]
	v_mfma_scale_f32_16x16x128_f8f6f4 v[100:103], v[28:35], v[228:235], v[100:103], v245, v245 op_sel_hi:[0,0,0]
	s_setprio 0
	s_barrier
; #define PG8_STAGE(bufoff, gbase, voff) do { _Pragma("unroll") for (int _i = 0; _i < 2; ++_i) \
;         __builtin_amdgcn_global_load_lds((const unsigned*)((const char*)(gbase) + (voff)[_i]), (PG8_LAS unsigned*)(lds + (bufoff) + ldsw + _i * 8192), 16, 0, 0); } while (0)
; #define PG8_LDA(dst, b, h) do { _Pragma("unroll") for (int m = 0; m < 4; ++m) _Pragma("unroll") for (int k = 0; k < 2; ++k) dst[m][k] = *(const PG8_LAS bf16x8*)(lds + PG8_SA(b, h) + aoff + m * 2048 + k * 1024); } while (0)
; #define PG8_WAIT_V(n) asm volatile("s_waitcnt vmcnt(" #n ")" ::: "memory")
; #define PG8_WAIT_L(n) asm volatile("s_waitcnt lgkmcnt(" #n ")" ::: "memory")
; template <class Epi, class Sched, bool ALIGN_EPI = false, bool SP2 = false, bool FP8 = false, bool ABLK = false>
; __device__ __forceinline__ void gemm_phase(PG8_LAS unsigned char* lds, const Gemm g, const Sched& S, const Epi& E) {
;     ...
;         for (int t = 0; t < nt; t += 2) {
;             const bool last = (t == nt - 2);
;             const char* a1 = cA + (size_t)(t + 1) * kstepA;
;             const char* a2 = last ? nA : cA + (size_t)(t + 2) * kstepA; const char* b2 = last ? nB : cB + (size_t)(t + 2) * kstep;
;             const char* a3 = a2 + kstepA; const char* b3 = b2 + kstep;
;             if (last && has_next) S.a_ready(nxt);
;             if constexpr (SP2) {
;             PG8_LDB(B0, 0, 0); PG8_LDB(B1, 0, 1); PG8_SCHED; PG8_LDA(At, 0, 0); PG8_STAGE(PG8_SA(1, 1), a1 + hstepA, voffA);
;             PG8_WAIT_V8_UNLESS_FIRST(t); PG8_WAIT_L(0); PG8_BAR; PG8_MMA(0, 0, At, B0); PG8_MMA(0, 1, At, B1); PG8_BAR; PG8_SCHED;
;             PG8_LDA(At, 0, 1); PG8_STAGE(PG8_SB(0, 0), b2, voffB); PG8_STAGE(PG8_SB(0, 1), b2 + hstep, voffB); PG8_STAGE(PG8_SA(0, 0), a2, voffA);
;             PG8_WAIT_V8_UNLESS_FIRST(t); PG8_WAIT_L(0); PG8_BAR; PG8_MMA(1, 0, At, B0); PG8_MMA(1, 1, At, B1); PG8_BAR; PG8_SCHED;
;             PG8_LDB(B0, 1, 0); PG8_LDB(B1, 1, 1); PG8_SCHED; PG8_LDA(At, 1, 0); PG8_STAGE(PG8_SA(0, 1), a2 + hstepA, voffA);
;             PG8_WAIT_V(8); PG8_WAIT_L(0); PG8_BAR; PG8_MMA(0, 0, At, B0); PG8_MMA(0, 1, At, B1); PG8_BAR; PG8_SCHED;
;             PG8_LDA(At, 1, 1); PG8_STAGE(PG8_SB(1, 0), b3, voffB); PG8_STAGE(PG8_SB(1, 1), b3 + hstep, voffB); PG8_STAGE(PG8_SA(1, 0), a3, voffA);
;             PG8_WAIT_V(8); PG8_WAIT_L(0); PG8_BAR; PG8_MMA(1, 0, At, B0); PG8_MMA(1, 1, At, B1); PG8_BAR; PG8_SCHED;
	s_add_i32 s62, s73, s17
	v_lshl_add_u64 v[174:175], v[174:175], 0, s[34:35]
	s_mov_b32 m0, s62
	ds_read_b128 v[182:185], v208 offset:49152
	ds_read_b128 v[186:189], v208 offset:50176
	ds_read_b128 v[210:213], v208 offset:51200
	ds_read_b128 v[214:217], v208 offset:52224
	ds_read_b128 v[218:221], v208 offset:53248
	ds_read_b128 v[222:225], v208 offset:54272
	ds_read_b128 v[228:231], v208 offset:55296
	ds_read_b128 v[232:235], v208 offset:56320
	global_load_lds_dwordx4 v[174:175], off
	s_add_i32 m0, s62, 0x2000
	s_add_u32 s60, s60, 0x20080
	v_lshl_add_u64 v[174:175], v[176:177], 0, s[34:35]
	s_addc_u32 s61, s61, 0
	s_add_i32 s62, s74, s17
	global_load_lds_dwordx4 v[174:175], off
	s_mov_b32 m0, s62
	s_nop 0
	global_load_lds_dwordx4 v2, s[60:61]
	s_add_i32 m0, s62, 0x2000
	s_nop 0
	global_load_lds_dwordx4 v164, s[60:61]
	v_lshl_add_u64 v[174:175], v[178:179], 0, s[34:35]
	s_mov_b32 m0, s65
	s_nop 0
	global_load_lds_dwordx4 v[174:175], off
	v_lshl_add_u64 v[174:175], v[180:181], 0, s[34:35]
	s_mov_b32 m0, s66
	s_nop 0
	global_load_lds_dwordx4 v[174:175], off
	s_waitcnt vmcnt(8)
	s_waitcnt lgkmcnt(0)
	s_barrier
	s_setprio 1
	s_waitcnt lgkmcnt(0)
	v_mfma_scale_f32_16x16x128_f8f6f4 v[96:99], v[4:11], v[182:189], v[96:99], v245, v245 op_sel_hi:[0,0,0]
	v_mfma_scale_f32_16x16x128_f8f6f4 v[92:95], v[12:19], v[182:189], v[92:95], v245, v245 op_sel_hi:[0,0,0]
	v_mfma_scale_f32_16x16x128_f8f6f4 v[80:83], v[4:11], v[210:217], v[80:83], v245, v245 op_sel_hi:[0,0,0]
	v_mfma_scale_f32_16x16x128_f8f6f4 v[76:79], v[12:19], v[210:217], v[76:79], v245, v245 op_sel_hi:[0,0,0]
	v_mfma_scale_f32_16x16x128_f8f6f4 v[64:67], v[4:11], v[218:225], v[64:67], v245, v245 op_sel_hi:[0,0,0]
	v_mfma_scale_f32_16x16x128_f8f6f4 v[60:63], v[12:19], v[218:225], v[60:63], v245, v245 op_sel_hi:[0,0,0]
	v_mfma_scale_f32_16x16x128_f8f6f4 v[48:51], v[4:11], v[228:235], v[48:51], v245, v245 op_sel_hi:[0,0,0]
	v_mfma_scale_f32_16x16x128_f8f6f4 v[44:47], v[12:19], v[228:235], v[44:47], v245, v245 op_sel_hi:[0,0,0]
	s_setprio 0
	s_setprio 1
	v_mfma_scale_f32_16x16x128_f8f6f4 v[88:91], v[20:27], v[182:189], v[88:91], v245, v245 op_sel_hi:[0,0,0]
	v_mfma_scale_f32_16x16x128_f8f6f4 v[84:87], v[28:35], v[182:189], v[84:87], v245, v245 op_sel_hi:[0,0,0]
	v_mfma_scale_f32_16x16x128_f8f6f4 v[72:75], v[20:27], v[210:217], v[72:75], v245, v245 op_sel_hi:[0,0,0]
	v_mfma_scale_f32_16x16x128_f8f6f4 v[68:71], v[28:35], v[210:217], v[68:71], v245, v245 op_sel_hi:[0,0,0]
	v_mfma_scale_f32_16x16x128_f8f6f4 v[56:59], v[20:27], v[218:225], v[56:59], v245, v245 op_sel_hi:[0,0,0]
	v_mfma_scale_f32_16x16x128_f8f6f4 v[52:55], v[28:35], v[218:225], v[52:55], v245, v245 op_sel_hi:[0,0,0]
	v_mfma_scale_f32_16x16x128_f8f6f4 v[40:43], v[20:27], v[228:235], v[40:43], v245, v245 op_sel_hi:[0,0,0]
	v_mfma_scale_f32_16x16x128_f8f6f4 v[36:39], v[28:35], v[228:235], v[36:39], v245, v245 op_sel_hi:[0,0,0]
	s_setprio 0
	s_add_u32 s42, s42, 0x100
	s_addc_u32 s43, s43, 0
	s_add_u32 s70, s70, 0x100
	s_addc_u32 s71, s71, 0
	s_cmp_gt_u32 s72, 5
	s_mov_b32 s60, s72
	s_cbranch_scc1 .Lrot5_exit
	s_add_i32 s72, s60, 2
	s_add_u32 s61, s42, 0xfffe0080
	s_addc_u32 s62, s43, -1
	s_add_i32 s73, 0, 0x10000
	s_cmp_eq_u32 s60, 4
	s_cselect_b32 s63, s4, s62
	s_cselect_b32 s62, s5, s61
	s_cselect_b32 s61, s53, s71
	s_cselect_b32 s60, s55, s70
	s_add_i32 s74, 0, 0x14000
	v_add_u32_e32 v4, s73, v195
	v_add_u32_e32 v8, s74, v195
	s_barrier
	s_branch .Lrot5_body

; #define PG8_STAGE(bufoff, gbase, voff) do { _Pragma("unroll") for (int _i = 0; _i < 2; ++_i) \
;         __builtin_amdgcn_global_load_lds((const unsigned*)((const char*)(gbase) + (voff)[_i]), (PG8_LAS unsigned*)(lds + (bufoff) + ldsw + _i * 8192), 16, 0, 0); } while (0)
; #define PG8_LDA(dst, b, h) do { _Pragma("unroll") for (int m = 0; m < 4; ++m) _Pragma("unroll") for (int k = 0; k < 2; ++k) dst[m][k] = *(const PG8_LAS bf16x8*)(lds + PG8_SA(b, h) + aoff + m * 2048 + k * 1024); } while (0)
; #define PG8_LDB(dst, b, h) do { _Pragma("unroll") for (int n = 0; n < 2; ++n) _Pragma("unroll") for (int k = 0; k < 2; ++k) dst[n][k] = *(const PG8_LAS bf16x8*)(lds + PG8_SB(b, h) + boff + n * 2048 + k * 1024); } while (0)
; #define PG8_WAIT_V8_UNLESS_FIRST(t) asm volatile("s_cmp_eq_u32 %0, 0\n\ts_cbranch_scc1 .Lpg8skip%=\n\ts_waitcnt vmcnt(8)\n.Lpg8skip%=:" :: "s"(t) : "scc", "memory")
; #define PG8_WAIT_L(n) asm volatile("s_waitcnt lgkmcnt(" #n ")" ::: "memory")
; #define PG8_BAR __builtin_amdgcn_s_barrier()
; #define PG8_SCHED __builtin_amdgcn_sched_barrier(0)
; template <class Epi, class Sched, bool ALIGN_EPI = false, bool SP2 = false, bool FP8 = false, bool ABLK = false>
; __device__ __forceinline__ void gemm_phase(PG8_LAS unsigned char* lds, const Gemm g, const Sched& S, const Epi& E) {
;     ...
;             PG8_LDB(B0, 0, 0); PG8_LDB(B1, 0, 1); PG8_SCHED; PG8_LDA(At, 0, 0); PG8_STAGE(PG8_SA(1, 1), a1 + hstepA, voffA);
;             PG8_WAIT_V8_UNLESS_FIRST(t); PG8_WAIT_L(0); PG8_BAR; PG8_MMA(0, 0, At, B0); PG8_MMA(0, 1, At, B1); PG8_BAR; PG8_SCHED;
.Lrot6_body:
	ds_read_b128 v[28:31], v4
	ds_read_b128 v[32:35], v4 offset:1024
	ds_read_b128 v[20:23], v4 offset:2048
	ds_read_b128 v[24:27], v4 offset:3072
	ds_read_b128 v[12:15], v8
	ds_read_b128 v[16:19], v8 offset:1024
	ds_read_b128 v[4:7], v8 offset:2048
	ds_read_b128 v[8:11], v8 offset:3072
	s_add_i32 m0, s20, 0xc000
	ds_read_b128 v[174:177], v184
	ds_read_b128 v[178:181], v184 offset:1024
	ds_read_b128 v[186:189], v184 offset:2048
	ds_read_b128 v[190:193], v184 offset:3072
	ds_read_b128 v[208:211], v184 offset:4096
	ds_read_b128 v[212:215], v184 offset:5120
	ds_read_b128 v[216:219], v184 offset:6144
	ds_read_b128 v[220:223], v184 offset:7168
	global_load_lds_dwordx4 v170, s[60:61]
	s_add_i32 m0, s20, 0xe000
	s_nop 0
	global_load_lds_dwordx4 v172, s[60:61]
	s_cmp_eq_u32 s75, 0
	s_cbranch_scc1 .Lpg8skip12
	s_waitcnt vmcnt(8)

; #define PG8_STAGE(bufoff, gbase, voff) do { _Pragma("unroll") for (int _i = 0; _i < 2; ++_i) \
;         __builtin_amdgcn_global_load_lds((const unsigned*)((const char*)(gbase) + (voff)[_i]), (PG8_LAS unsigned*)(lds + (bufoff) + ldsw + _i * 8192), 16, 0, 0); } while (0)
; #define PG8_LDA(dst, b, h) do { _Pragma("unroll") for (int m = 0; m < 4; ++m) _Pragma("unroll") for (int k = 0; k < 2; ++k) dst[m][k] = *(const PG8_LAS bf16x8*)(lds + PG8_SA(b, h) + aoff + m * 2048 + k * 1024); } while (0)
; #define PG8_LDB(dst, b, h) do { _Pragma("unroll") for (int n = 0; n < 2; ++n) _Pragma("unroll") for (int k = 0; k < 2; ++k) dst[n][k] = *(const PG8_LAS bf16x8*)(lds + PG8_SB(b, h) + boff + n * 2048 + k * 1024); } while (0)
; #define PG8_WAIT_V(n) asm volatile("s_waitcnt vmcnt(" #n ")" ::: "memory")
; #define PG8_WAIT_V8_UNLESS_FIRST(t) asm volatile("s_cmp_eq_u32 %0, 0\n\ts_cbranch_scc1 .Lpg8skip%=\n\ts_waitcnt vmcnt(8)\n.Lpg8skip%=:" :: "s"(t) : "scc", "memory")
; #define PG8_WAIT_L(n) asm volatile("s_waitcnt lgkmcnt(" #n ")" ::: "memory")
; #define PG8_BAR __builtin_amdgcn_s_barrier()
; #define PG8_SCHED __builtin_amdgcn_sched_barrier(0)
; template <class Epi, class Sched, bool ALIGN_EPI = false, bool SP2 = false, bool FP8 = false, bool ABLK = false>
; __device__ __forceinline__ void gemm_phase(PG8_LAS unsigned char* lds, const Gemm g, const Sched& S, const Epi& E) {
;     ...
;             PG8_WAIT_V8_UNLESS_FIRST(t); PG8_WAIT_L(0); PG8_BAR; PG8_MMA(1, 0, At, B0); PG8_MMA(1, 1, At, B1); PG8_BAR; PG8_SCHED;
;             PG8_LDB(B0, 1, 0); PG8_LDB(B1, 1, 1); PG8_SCHED; PG8_LDA(At, 1, 0); PG8_STAGE(PG8_SA(0, 1), a2 + hstepA, voffA);
;             PG8_WAIT_V(8); PG8_WAIT_L(0); PG8_BAR; PG8_MMA(0, 0, At, B0); PG8_MMA(0, 1, At, B1); PG8_BAR; PG8_SCHED;
.Lpg8skip13:
	s_waitcnt lgkmcnt(0)
	s_barrier
	s_setprio 1
	s_waitcnt lgkmcnt(0)
	v_mfma_scale_f32_16x16x128_f8f6f4 v[96:99], v[28:35], v[186:193], v[96:99], v245, v245 op_sel_hi:[0,0,0]
	v_mfma_scale_f32_16x16x128_f8f6f4 v[92:95], v[20:27], v[186:193], v[92:95], v245, v245 op_sel_hi:[0,0,0]
	v_mfma_scale_f32_16x16x128_f8f6f4 v[80:83], v[28:35], v[208:215], v[80:83], v245, v245 op_sel_hi:[0,0,0]
	v_mfma_scale_f32_16x16x128_f8f6f4 v[76:79], v[20:27], v[208:215], v[76:79], v245, v245 op_sel_hi:[0,0,0]
	v_mfma_scale_f32_16x16x128_f8f6f4 v[64:67], v[28:35], v[216:223], v[64:67], v245, v245 op_sel_hi:[0,0,0]
	v_mfma_scale_f32_16x16x128_f8f6f4 v[60:63], v[20:27], v[216:223], v[60:63], v245, v245 op_sel_hi:[0,0,0]
	v_mfma_scale_f32_16x16x128_f8f6f4 v[48:51], v[28:35], v[228:235], v[48:51], v245, v245 op_sel_hi:[0,0,0]
	v_mfma_scale_f32_16x16x128_f8f6f4 v[44:47], v[20:27], v[228:235], v[44:47], v245, v245 op_sel_hi:[0,0,0]
	s_setprio 0
	s_setprio 1
	v_mfma_scale_f32_16x16x128_f8f6f4 v[88:91], v[12:19], v[186:193], v[88:91], v245, v245 op_sel_hi:[0,0,0]
	v_mfma_scale_f32_16x16x128_f8f6f4 v[84:87], v[4:11], v[186:193], v[84:87], v245, v245 op_sel_hi:[0,0,0]
	v_mfma_scale_f32_16x16x128_f8f6f4 v[72:75], v[12:19], v[208:215], v[72:75], v245, v245 op_sel_hi:[0,0,0]
	v_mfma_scale_f32_16x16x128_f8f6f4 v[68:71], v[4:11], v[208:215], v[68:71], v245, v245 op_sel_hi:[0,0,0]
	v_mfma_scale_f32_16x16x128_f8f6f4 v[56:59], v[12:19], v[216:223], v[56:59], v245, v245 op_sel_hi:[0,0,0]
	v_mfma_scale_f32_16x16x128_f8f6f4 v[52:55], v[4:11], v[216:223], v[52:55], v245, v245 op_sel_hi:[0,0,0]
	v_mfma_scale_f32_16x16x128_f8f6f4 v[40:43], v[12:19], v[228:235], v[40:43], v245, v245 op_sel_hi:[0,0,0]
	v_mfma_scale_f32_16x16x128_f8f6f4 v[36:39], v[4:11], v[228:235], v[36:39], v245, v245 op_sel_hi:[0,0,0]
	s_setprio 0
	s_barrier
	s_add_i32 s76, 0, 0x18000
	s_add_i32 s77, 0, 0x1c000
	v_add_u32_e32 v16, s76, v183
	v_add_u32_e32 v32, s77, v183
	ds_read_b128 v[4:7], v16
	ds_read_b128 v[8:11], v16 offset:1024
	ds_read_b128 v[12:15], v16 offset:2048
	ds_read_b128 v[16:19], v16 offset:3072
	ds_read_b128 v[20:23], v32
	ds_read_b128 v[24:27], v32 offset:1024
	ds_read_b128 v[28:31], v32 offset:2048
	ds_read_b128 v[32:35], v32 offset:3072
	s_add_u32 s64, s64, 0x20000
	s_addc_u32 s65, s65, 0
	s_mov_b32 m0, s22
	ds_read_b128 v[186:189], v184 offset:32768
	ds_read_b128 v[190:193], v184 offset:33792
	ds_read_b128 v[208:211], v184 offset:34816
	ds_read_b128 v[212:215], v184 offset:35840
	ds_read_b128 v[216:219], v184 offset:36864
	ds_read_b128 v[220:223], v184 offset:37888
	ds_read_b128 v[228:231], v184 offset:38912
	ds_read_b128 v[232:235], v184 offset:39936
	global_load_lds_dwordx4 v168, s[64:65]
	s_mov_b32 m0, s23
	s_nop 0
	global_load_lds_dwordx4 v166, s[64:65]
	s_waitcnt vmcnt(8)
	s_waitcnt lgkmcnt(0)
	s_barrier
	s_setprio 1
	s_waitcnt lgkmcnt(0)
	v_mfma_scale_f32_16x16x128_f8f6f4 v[160:163], v[4:11], v[186:193], v[160:163], v245, v245 op_sel_hi:[0,0,0]
	v_mfma_scale_f32_16x16x128_f8f6f4 v[156:159], v[12:19], v[186:193], v[156:159], v245, v245 op_sel_hi:[0,0,0]
	v_mfma_scale_f32_16x16x128_f8f6f4 v[144:147], v[4:11], v[208:215], v[144:147], v245, v245 op_sel_hi:[0,0,0]
	v_mfma_scale_f32_16x16x128_f8f6f4 v[140:143], v[12:19], v[208:215], v[140:143], v245, v245 op_sel_hi:[0,0,0]
	v_mfma_scale_f32_16x16x128_f8f6f4 v[128:131], v[4:11], v[216:223], v[128:131], v245, v245 op_sel_hi:[0,0,0]
	v_mfma_scale_f32_16x16x128_f8f6f4 v[124:127], v[12:19], v[216:223], v[124:127], v245, v245 op_sel_hi:[0,0,0]
	v_mfma_scale_f32_16x16x128_f8f6f4 v[112:115], v[4:11], v[228:235], v[112:115], v245, v245 op_sel_hi:[0,0,0]
	v_mfma_scale_f32_16x16x128_f8f6f4 v[108:111], v[12:19], v[228:235], v[108:111], v245, v245 op_sel_hi:[0,0,0]
	s_setprio 0
	s_setprio 1
	v_mfma_scale_f32_16x16x128_f8f6f4 v[152:155], v[20:27], v[186:193], v[152:155], v245, v245 op_sel_hi:[0,0,0]
	v_mfma_scale_f32_16x16x128_f8f6f4 v[148:151], v[28:35], v[186:193], v[148:151], v245, v245 op_sel_hi:[0,0,0]
	v_mfma_scale_f32_16x16x128_f8f6f4 v[136:139], v[20:27], v[208:215], v[136:139], v245, v245 op_sel_hi:[0,0,0]
	v_mfma_scale_f32_16x16x128_f8f6f4 v[132:135], v[28:35], v[208:215], v[132:135], v245, v245 op_sel_hi:[0,0,0]
	v_mfma_scale_f32_16x16x128_f8f6f4 v[120:123], v[20:27], v[216:223], v[120:123], v245, v245 op_sel_hi:[0,0,0]
	v_mfma_scale_f32_16x16x128_f8f6f4 v[116:119], v[28:35], v[216:223], v[116:119], v245, v245 op_sel_hi:[0,0,0]
	v_mfma_scale_f32_16x16x128_f8f6f4 v[104:107], v[20:27], v[228:235], v[104:107], v245, v245 op_sel_hi:[0,0,0]
	v_mfma_scale_f32_16x16x128_f8f6f4 v[100:103], v[28:35], v[228:235], v[100:103], v245, v245 op_sel_hi:[0,0,0]
	s_setprio 0
	s_barrier
; #define PG8_STAGE(bufoff, gbase, voff) do { _Pragma("unroll") for (int _i = 0; _i < 2; ++_i) \
;         __builtin_amdgcn_global_load_lds((const unsigned*)((const char*)(gbase) + (voff)[_i]), (PG8_LAS unsigned*)(lds + (bufoff) + ldsw + _i * 8192), 16, 0, 0); } while (0)
; #define PG8_LDA(dst, b, h) do { _Pragma("unroll") for (int m = 0; m < 4; ++m) _Pragma("unroll") for (int k = 0; k < 2; ++k) dst[m][k] = *(const PG8_LAS bf16x8*)(lds + PG8_SA(b, h) + aoff + m * 2048 + k * 1024); } while (0)
; #define PG8_WAIT_V(n) asm volatile("s_waitcnt vmcnt(" #n ")" ::: "memory")
; #define PG8_WAIT_L(n) asm volatile("s_waitcnt lgkmcnt(" #n ")" ::: "memory")
; template <class Epi, class Sched, bool ALIGN_EPI = false, bool SP2 = false, bool FP8 = false, bool ABLK = false>
; __device__ __forceinline__ void gemm_phase(PG8_LAS unsigned char* lds, const Gemm g, const Sched& S, const Epi& E) {
;     ...
;         for (int t = 0; t < nt; t += 2) {
;             const bool last = (t == nt - 2);
;             const char* a1 = cA + (size_t)(t + 1) * kstepA;
;             const char* a2 = last ? nA : cA + (size_t)(t + 2) * kstepA; const char* b2 = last ? nB : cB + (size_t)(t + 2) * kstep;
;             const char* a3 = a2 + kstepA; const char* b3 = b2 + kstep;
;             if (last && has_next) S.a_ready(nxt);
;             if constexpr (SP2) {
;             PG8_LDB(B0, 0, 0); PG8_LDB(B1, 0, 1); PG8_SCHED; PG8_LDA(At, 0, 0); PG8_STAGE(PG8_SA(1, 1), a1 + hstepA, voffA);
;             PG8_WAIT_V8_UNLESS_FIRST(t); PG8_WAIT_L(0); PG8_BAR; PG8_MMA(0, 0, At, B0); PG8_MMA(0, 1, At, B1); PG8_BAR; PG8_SCHED;
;             PG8_LDA(At, 0, 1); PG8_STAGE(PG8_SB(0, 0), b2, voffB); PG8_STAGE(PG8_SB(0, 1), b2 + hstep, voffB); PG8_STAGE(PG8_SA(0, 0), a2, voffA);
;             PG8_WAIT_V8_UNLESS_FIRST(t); PG8_WAIT_L(0); PG8_BAR; PG8_MMA(1, 0, At, B0); PG8_MMA(1, 1, At, B1); PG8_BAR; PG8_SCHED;
;             PG8_LDB(B0, 1, 0); PG8_LDB(B1, 1, 1); PG8_SCHED; PG8_LDA(At, 1, 0); PG8_STAGE(PG8_SA(0, 1), a2 + hstepA, voffA);
;             PG8_WAIT_V(8); PG8_WAIT_L(0); PG8_BAR; PG8_MMA(0, 0, At, B0); PG8_MMA(0, 1, At, B1); PG8_BAR; PG8_SCHED;
;             PG8_LDA(At, 1, 1); PG8_STAGE(PG8_SB(1, 0), b3, voffB); PG8_STAGE(PG8_SB(1, 1), b3 + hstep, voffB); PG8_STAGE(PG8_SA(1, 0), a3, voffA);
;             PG8_WAIT_V(8); PG8_WAIT_L(0); PG8_BAR; PG8_MMA(1, 0, At, B0); PG8_MMA(1, 1, At, B1); PG8_BAR; PG8_SCHED;
	s_add_i32 s64, s76, s19
	v_lshl_add_u64 v[174:175], v[174:175], 0, s[34:35]
	s_mov_b32 m0, s64
	ds_read_b128 v[186:189], v184 offset:49152
	ds_read_b128 v[190:193], v184 offset:50176
	ds_read_b128 v[208:211], v184 offset:51200
	ds_read_b128 v[212:215], v184 offset:52224
	ds_read_b128 v[216:219], v184 offset:53248
	ds_read_b128 v[220:223], v184 offset:54272
	ds_read_b128 v[228:231], v184 offset:55296
	ds_read_b128 v[232:235], v184 offset:56320
	global_load_lds_dwordx4 v[174:175], off
	s_add_i32 m0, s64, 0x2000
	s_add_u32 s62, s62, 0x20080
	v_lshl_add_u64 v[174:175], v[176:177], 0, s[34:35]
	s_addc_u32 s63, s63, 0
	s_add_i32 s64, s77, s19
	global_load_lds_dwordx4 v[174:175], off
	s_mov_b32 m0, s64
	s_nop 0
	global_load_lds_dwordx4 v2, s[62:63]
	s_add_i32 m0, s64, 0x2000
	s_nop 0
	global_load_lds_dwordx4 v164, s[62:63]
	v_lshl_add_u64 v[174:175], v[178:179], 0, s[34:35]
	s_mov_b32 m0, s67
	s_nop 0
	global_load_lds_dwordx4 v[174:175], off
	v_lshl_add_u64 v[174:175], v[180:181], 0, s[34:35]
	s_mov_b32 m0, s68
	s_nop 0
	global_load_lds_dwordx4 v[174:175], off
	s_waitcnt vmcnt(8)
	s_waitcnt lgkmcnt(0)
	s_barrier
	s_setprio 1
	s_waitcnt lgkmcnt(0)
	v_mfma_scale_f32_16x16x128_f8f6f4 v[96:99], v[4:11], v[186:193], v[96:99], v245, v245 op_sel_hi:[0,0,0]
	v_mfma_scale_f32_16x16x128_f8f6f4 v[92:95], v[12:19], v[186:193], v[92:95], v245, v245 op_sel_hi:[0,0,0]
	v_mfma_scale_f32_16x16x128_f8f6f4 v[80:83], v[4:11], v[208:215], v[80:83], v245, v245 op_sel_hi:[0,0,0]
	v_mfma_scale_f32_16x16x128_f8f6f4 v[76:79], v[12:19], v[208:215], v[76:79], v245, v245 op_sel_hi:[0,0,0]
	v_mfma_scale_f32_16x16x128_f8f6f4 v[64:67], v[4:11], v[216:223], v[64:67], v245, v245 op_sel_hi:[0,0,0]
	v_mfma_scale_f32_16x16x128_f8f6f4 v[60:63], v[12:19], v[216:223], v[60:63], v245, v245 op_sel_hi:[0,0,0]
	v_mfma_scale_f32_16x16x128_f8f6f4 v[48:51], v[4:11], v[228:235], v[48:51], v245, v245 op_sel_hi:[0,0,0]
	v_mfma_scale_f32_16x16x128_f8f6f4 v[44:47], v[12:19], v[228:235], v[44:47], v245, v245 op_sel_hi:[0,0,0]
	s_setprio 0
	s_setprio 1
	v_mfma_scale_f32_16x16x128_f8f6f4 v[88:91], v[20:27], v[186:193], v[88:91], v245, v245 op_sel_hi:[0,0,0]
	v_mfma_scale_f32_16x16x128_f8f6f4 v[84:87], v[28:35], v[186:193], v[84:87], v245, v245 op_sel_hi:[0,0,0]
	v_mfma_scale_f32_16x16x128_f8f6f4 v[72:75], v[20:27], v[208:215], v[72:75], v245, v245 op_sel_hi:[0,0,0]
	v_mfma_scale_f32_16x16x128_f8f6f4 v[68:71], v[28:35], v[208:215], v[68:71], v245, v245 op_sel_hi:[0,0,0]
	v_mfma_scale_f32_16x16x128_f8f6f4 v[56:59], v[20:27], v[216:223], v[56:59], v245, v245 op_sel_hi:[0,0,0]
	v_mfma_scale_f32_16x16x128_f8f6f4 v[52:55], v[28:35], v[216:223], v[52:55], v245, v245 op_sel_hi:[0,0,0]
	v_mfma_scale_f32_16x16x128_f8f6f4 v[40:43], v[20:27], v[228:235], v[40:43], v245, v245 op_sel_hi:[0,0,0]
	v_mfma_scale_f32_16x16x128_f8f6f4 v[36:39], v[28:35], v[228:235], v[36:39], v245, v245 op_sel_hi:[0,0,0]
	s_setprio 0
	s_add_u32 s60, s60, 0x100
	s_addc_u32 s61, s61, 0
	s_add_u32 s73, s73, 0x100
	s_addc_u32 s74, s74, 0
	s_cmp_gt_u32 s75, 5
	s_mov_b32 s62, s75
	s_cbranch_scc1 .Lrot6_exit
	s_add_i32 s75, s62, 2
	s_add_u32 s63, s60, 0xfffe0080
	s_addc_u32 s64, s61, -1
	s_add_i32 s76, 0, 0x10000
	s_cmp_eq_u32 s62, 4
	s_cselect_b32 s65, s4, s64
	s_cselect_b32 s64, s5, s63
	s_cselect_b32 s63, s53, s74
	s_cselect_b32 s62, s55, s73
	s_add_i32 s77, 0, 0x14000
	v_add_u32_e32 v4, s76, v183
	v_add_u32_e32 v8, s77, v183
	s_barrier
	s_branch .Lrot6_body

; #define PG8_STAGE(bufoff, gbase, voff) do { _Pragma("unroll") for (int _i = 0; _i < 2; ++_i) \
;         __builtin_amdgcn_global_load_lds((const unsigned*)((const char*)(gbase) + (voff)[_i]), (PG8_LAS unsigned*)(lds + (bufoff) + ldsw + _i * 8192), 16, 0, 0); } while (0)
; #define PG8_LDA(dst, b, h) do { _Pragma("unroll") for (int m = 0; m < 4; ++m) _Pragma("unroll") for (int k = 0; k < 2; ++k) dst[m][k] = *(const PG8_LAS bf16x8*)(lds + PG8_SA(b, h) + aoff + m * 2048 + k * 1024); } while (0)
; #define PG8_LDB(dst, b, h) do { _Pragma("unroll") for (int n = 0; n < 2; ++n) _Pragma("unroll") for (int k = 0; k < 2; ++k) dst[n][k] = *(const PG8_LAS bf16x8*)(lds + PG8_SB(b, h) + boff + n * 2048 + k * 1024); } while (0)
; #define PG8_WAIT_V8_UNLESS_FIRST(t) asm volatile("s_cmp_eq_u32 %0, 0\n\ts_cbranch_scc1 .Lpg8skip%=\n\ts_waitcnt vmcnt(8)\n.Lpg8skip%=:" :: "s"(t) : "scc", "memory")
; #define PG8_WAIT_L(n) asm volatile("s_waitcnt lgkmcnt(" #n ")" ::: "memory")
; #define PG8_BAR __builtin_amdgcn_s_barrier()
; #define PG8_SCHED __builtin_amdgcn_sched_barrier(0)
; template <class Epi, class Sched, bool ALIGN_EPI = false, bool SP2 = false, bool FP8 = false, bool ABLK = false>
; __device__ __forceinline__ void gemm_phase(PG8_LAS unsigned char* lds, const Gemm g, const Sched& S, const Epi& E) {
;     ...
;             PG8_LDB(B0, 0, 0); PG8_LDB(B1, 0, 1); PG8_SCHED; PG8_LDA(At, 0, 0); PG8_STAGE(PG8_SA(1, 1), a1 + hstepA, voffA);
;             PG8_WAIT_V8_UNLESS_FIRST(t); PG8_WAIT_L(0); PG8_BAR; PG8_MMA(0, 0, At, B0); PG8_MMA(0, 1, At, B1); PG8_BAR; PG8_SCHED;
.Lrot7_body:
	ds_read_b128 v[28:31], v4
	ds_read_b128 v[32:35], v4 offset:1024
	ds_read_b128 v[20:23], v4 offset:2048
	ds_read_b128 v[24:27], v4 offset:3072
	ds_read_b128 v[12:15], v8
	ds_read_b128 v[16:19], v8 offset:1024
	ds_read_b128 v[4:7], v8 offset:2048
	ds_read_b128 v[8:11], v8 offset:3072
	s_add_i32 m0, s18, 0xc000
	ds_read_b128 v[174:177], v184
	ds_read_b128 v[178:181], v184 offset:1024
	ds_read_b128 v[186:189], v184 offset:2048
	ds_read_b128 v[190:193], v184 offset:3072
	ds_read_b128 v[208:211], v184 offset:4096
	ds_read_b128 v[212:215], v184 offset:5120
	ds_read_b128 v[216:219], v184 offset:6144
	ds_read_b128 v[220:223], v184 offset:7168
	global_load_lds_dwordx4 v170, s[56:57]
	s_add_i32 m0, s18, 0xe000
	s_nop 0
	global_load_lds_dwordx4 v172, s[56:57]
	s_cmp_eq_u32 s71, 0
	s_cbranch_scc1 .Lpg8skip14
	s_waitcnt vmcnt(8)

; #define PG8_STAGE(bufoff, gbase, voff) do { _Pragma("unroll") for (int _i = 0; _i < 2; ++_i) \
;         __builtin_amdgcn_global_load_lds((const unsigned*)((const char*)(gbase) + (voff)[_i]), (PG8_LAS unsigned*)(lds + (bufoff) + ldsw + _i * 8192), 16, 0, 0); } while (0)
; #define PG8_LDA(dst, b, h) do { _Pragma("unroll") for (int m = 0; m < 4; ++m) _Pragma("unroll") for (int k = 0; k < 2; ++k) dst[m][k] = *(const PG8_LAS bf16x8*)(lds + PG8_SA(b, h) + aoff + m * 2048 + k * 1024); } while (0)
; #define PG8_LDB(dst, b, h) do { _Pragma("unroll") for (int n = 0; n < 2; ++n) _Pragma("unroll") for (int k = 0; k < 2; ++k) dst[n][k] = *(const PG8_LAS bf16x8*)(lds + PG8_SB(b, h) + boff + n * 2048 + k * 1024); } while (0)
; #define PG8_WAIT_V(n) asm volatile("s_waitcnt vmcnt(" #n ")" ::: "memory")
; #define PG8_WAIT_V8_UNLESS_FIRST(t) asm volatile("s_cmp_eq_u32 %0, 0\n\ts_cbranch_scc1 .Lpg8skip%=\n\ts_waitcnt vmcnt(8)\n.Lpg8skip%=:" :: "s"(t) : "scc", "memory")
; #define PG8_WAIT_L(n) asm volatile("s_waitcnt lgkmcnt(" #n ")" ::: "memory")
; #define PG8_BAR __builtin_amdgcn_s_barrier()
; #define PG8_SCHED __builtin_amdgcn_sched_barrier(0)
; template <class Epi, class Sched, bool ALIGN_EPI = false, bool SP2 = false, bool FP8 = false, bool ABLK = false>
; __device__ __forceinline__ void gemm_phase(PG8_LAS unsigned char* lds, const Gemm g, const Sched& S, const Epi& E) {
;     ...
;             PG8_WAIT_V8_UNLESS_FIRST(t); PG8_WAIT_L(0); PG8_BAR; PG8_MMA(1, 0, At, B0); PG8_MMA(1, 1, At, B1); PG8_BAR; PG8_SCHED;
;             PG8_LDB(B0, 1, 0); PG8_LDB(B1, 1, 1); PG8_SCHED; PG8_LDA(At, 1, 0); PG8_STAGE(PG8_SA(0, 1), a2 + hstepA, voffA);
;             PG8_WAIT_V(8); PG8_WAIT_L(0); PG8_BAR; PG8_MMA(0, 0, At, B0); PG8_MMA(0, 1, At, B1); PG8_BAR; PG8_SCHED;
.Lpg8skip15:
	s_waitcnt lgkmcnt(0)
	s_barrier
	s_setprio 1
	s_waitcnt lgkmcnt(0)
	v_mfma_scale_f32_16x16x128_f8f6f4 v[96:99], v[28:35], v[186:193], v[96:99], v245, v245 op_sel_hi:[0,0,0]
	v_mfma_scale_f32_16x16x128_f8f6f4 v[92:95], v[20:27], v[186:193], v[92:95], v245, v245 op_sel_hi:[0,0,0]
	v_mfma_scale_f32_16x16x128_f8f6f4 v[80:83], v[28:35], v[208:215], v[80:83], v245, v245 op_sel_hi:[0,0,0]
	v_mfma_scale_f32_16x16x128_f8f6f4 v[76:79], v[20:27], v[208:215], v[76:79], v245, v245 op_sel_hi:[0,0,0]
	v_mfma_scale_f32_16x16x128_f8f6f4 v[64:67], v[28:35], v[216:223], v[64:67], v245, v245 op_sel_hi:[0,0,0]
	v_mfma_scale_f32_16x16x128_f8f6f4 v[60:63], v[20:27], v[216:223], v[60:63], v245, v245 op_sel_hi:[0,0,0]
	v_mfma_scale_f32_16x16x128_f8f6f4 v[48:51], v[28:35], v[228:235], v[48:51], v245, v245 op_sel_hi:[0,0,0]
	v_mfma_scale_f32_16x16x128_f8f6f4 v[44:47], v[20:27], v[228:235], v[44:47], v245, v245 op_sel_hi:[0,0,0]
	s_setprio 0
	s_setprio 1
	v_mfma_scale_f32_16x16x128_f8f6f4 v[88:91], v[12:19], v[186:193], v[88:91], v245, v245 op_sel_hi:[0,0,0]
	v_mfma_scale_f32_16x16x128_f8f6f4 v[84:87], v[4:11], v[186:193], v[84:87], v245, v245 op_sel_hi:[0,0,0]
	v_mfma_scale_f32_16x16x128_f8f6f4 v[72:75], v[12:19], v[208:215], v[72:75], v245, v245 op_sel_hi:[0,0,0]
	v_mfma_scale_f32_16x16x128_f8f6f4 v[68:71], v[4:11], v[208:215], v[68:71], v245, v245 op_sel_hi:[0,0,0]
	v_mfma_scale_f32_16x16x128_f8f6f4 v[56:59], v[12:19], v[216:223], v[56:59], v245, v245 op_sel_hi:[0,0,0]
	v_mfma_scale_f32_16x16x128_f8f6f4 v[52:55], v[4:11], v[216:223], v[52:55], v245, v245 op_sel_hi:[0,0,0]
	v_mfma_scale_f32_16x16x128_f8f6f4 v[40:43], v[12:19], v[228:235], v[40:43], v245, v245 op_sel_hi:[0,0,0]
	v_mfma_scale_f32_16x16x128_f8f6f4 v[36:39], v[4:11], v[228:235], v[36:39], v245, v245 op_sel_hi:[0,0,0]
	s_setprio 0
	s_barrier
	s_add_i32 s72, 0, 0x18000
	s_add_i32 s73, 0, 0x1c000
	v_add_u32_e32 v16, s72, v183
	v_add_u32_e32 v32, s73, v183
	ds_read_b128 v[4:7], v16
	ds_read_b128 v[8:11], v16 offset:1024
	ds_read_b128 v[12:15], v16 offset:2048
	ds_read_b128 v[16:19], v16 offset:3072
	ds_read_b128 v[20:23], v32
	ds_read_b128 v[24:27], v32 offset:1024
	ds_read_b128 v[28:31], v32 offset:2048
	ds_read_b128 v[32:35], v32 offset:3072
	s_add_u32 s60, s60, 0x20000
	s_addc_u32 s61, s61, 0
	s_mov_b32 m0, s20
	ds_read_b128 v[186:189], v184 offset:32768
	ds_read_b128 v[190:193], v184 offset:33792
	ds_read_b128 v[208:211], v184 offset:34816
	ds_read_b128 v[212:215], v184 offset:35840
	ds_read_b128 v[216:219], v184 offset:36864
	ds_read_b128 v[220:223], v184 offset:37888
	ds_read_b128 v[228:231], v184 offset:38912
	ds_read_b128 v[232:235], v184 offset:39936
	global_load_lds_dwordx4 v168, s[60:61]
	s_mov_b32 m0, s21
	s_nop 0
	global_load_lds_dwordx4 v166, s[60:61]
	s_waitcnt vmcnt(8)
	s_waitcnt lgkmcnt(0)
	s_barrier
	s_setprio 1
	s_waitcnt lgkmcnt(0)
	v_mfma_scale_f32_16x16x128_f8f6f4 v[160:163], v[4:11], v[186:193], v[160:163], v245, v245 op_sel_hi:[0,0,0]
	v_mfma_scale_f32_16x16x128_f8f6f4 v[156:159], v[12:19], v[186:193], v[156:159], v245, v245 op_sel_hi:[0,0,0]
	v_mfma_scale_f32_16x16x128_f8f6f4 v[144:147], v[4:11], v[208:215], v[144:147], v245, v245 op_sel_hi:[0,0,0]
	v_mfma_scale_f32_16x16x128_f8f6f4 v[140:143], v[12:19], v[208:215], v[140:143], v245, v245 op_sel_hi:[0,0,0]
	v_mfma_scale_f32_16x16x128_f8f6f4 v[128:131], v[4:11], v[216:223], v[128:131], v245, v245 op_sel_hi:[0,0,0]
	v_mfma_scale_f32_16x16x128_f8f6f4 v[124:127], v[12:19], v[216:223], v[124:127], v245, v245 op_sel_hi:[0,0,0]
	v_mfma_scale_f32_16x16x128_f8f6f4 v[112:115], v[4:11], v[228:235], v[112:115], v245, v245 op_sel_hi:[0,0,0]
	v_mfma_scale_f32_16x16x128_f8f6f4 v[108:111], v[12:19], v[228:235], v[108:111], v245, v245 op_sel_hi:[0,0,0]
	s_setprio 0
	s_setprio 1
	v_mfma_scale_f32_16x16x128_f8f6f4 v[152:155], v[20:27], v[186:193], v[152:155], v245, v245 op_sel_hi:[0,0,0]
	v_mfma_scale_f32_16x16x128_f8f6f4 v[148:151], v[28:35], v[186:193], v[148:151], v245, v245 op_sel_hi:[0,0,0]
	v_mfma_scale_f32_16x16x128_f8f6f4 v[136:139], v[20:27], v[208:215], v[136:139], v245, v245 op_sel_hi:[0,0,0]
	v_mfma_scale_f32_16x16x128_f8f6f4 v[132:135], v[28:35], v[208:215], v[132:135], v245, v245 op_sel_hi:[0,0,0]
	v_mfma_scale_f32_16x16x128_f8f6f4 v[120:123], v[20:27], v[216:223], v[120:123], v245, v245 op_sel_hi:[0,0,0]
	v_mfma_scale_f32_16x16x128_f8f6f4 v[116:119], v[28:35], v[216:223], v[116:119], v245, v245 op_sel_hi:[0,0,0]
	v_mfma_scale_f32_16x16x128_f8f6f4 v[104:107], v[20:27], v[228:235], v[104:107], v245, v245 op_sel_hi:[0,0,0]
	v_mfma_scale_f32_16x16x128_f8f6f4 v[100:103], v[28:35], v[228:235], v[100:103], v245, v245 op_sel_hi:[0,0,0]
	s_setprio 0
	s_barrier
; #define PG8_STAGE(bufoff, gbase, voff) do { _Pragma("unroll") for (int _i = 0; _i < 2; ++_i) \
;         __builtin_amdgcn_global_load_lds((const unsigned*)((const char*)(gbase) + (voff)[_i]), (PG8_LAS unsigned*)(lds + (bufoff) + ldsw + _i * 8192), 16, 0, 0); } while (0)
; #define PG8_LDA(dst, b, h) do { _Pragma("unroll") for (int m = 0; m < 4; ++m) _Pragma("unroll") for (int k = 0; k < 2; ++k) dst[m][k] = *(const PG8_LAS bf16x8*)(lds + PG8_SA(b, h) + aoff + m * 2048 + k * 1024); } while (0)
; #define PG8_WAIT_V(n) asm volatile("s_waitcnt vmcnt(" #n ")" ::: "memory")
; #define PG8_WAIT_L(n) asm volatile("s_waitcnt lgkmcnt(" #n ")" ::: "memory")
; template <class Epi, class Sched, bool ALIGN_EPI = false, bool SP2 = false, bool FP8 = false, bool ABLK = false>
; __device__ __forceinline__ void gemm_phase(PG8_LAS unsigned char* lds, const Gemm g, const Sched& S, const Epi& E) {
;     ...
;         for (int t = 0; t < nt; t += 2) {
;             const bool last = (t == nt - 2);
;             const char* a1 = cA + (size_t)(t + 1) * kstepA;
;             const char* a2 = last ? nA : cA + (size_t)(t + 2) * kstepA; const char* b2 = last ? nB : cB + (size_t)(t + 2) * kstep;
;             const char* a3 = a2 + kstepA; const char* b3 = b2 + kstep;
;             if (last && has_next) S.a_ready(nxt);
;             if constexpr (SP2) {
;             PG8_LDB(B0, 0, 0); PG8_LDB(B1, 0, 1); PG8_SCHED; PG8_LDA(At, 0, 0); PG8_STAGE(PG8_SA(1, 1), a1 + hstepA, voffA);
;             PG8_WAIT_V8_UNLESS_FIRST(t); PG8_WAIT_L(0); PG8_BAR; PG8_MMA(0, 0, At, B0); PG8_MMA(0, 1, At, B1); PG8_BAR; PG8_SCHED;
;             PG8_LDA(At, 0, 1); PG8_STAGE(PG8_SB(0, 0), b2, voffB); PG8_STAGE(PG8_SB(0, 1), b2 + hstep, voffB); PG8_STAGE(PG8_SA(0, 0), a2, voffA);
;             PG8_WAIT_V8_UNLESS_FIRST(t); PG8_WAIT_L(0); PG8_BAR; PG8_MMA(1, 0, At, B0); PG8_MMA(1, 1, At, B1); PG8_BAR; PG8_SCHED;
;             PG8_LDB(B0, 1, 0); PG8_LDB(B1, 1, 1); PG8_SCHED; PG8_LDA(At, 1, 0); PG8_STAGE(PG8_SA(0, 1), a2 + hstepA, voffA);
;             PG8_WAIT_V(8); PG8_WAIT_L(0); PG8_BAR; PG8_MMA(0, 0, At, B0); PG8_MMA(0, 1, At, B1); PG8_BAR; PG8_SCHED;
;             PG8_LDA(At, 1, 1); PG8_STAGE(PG8_SB(1, 0), b3, voffB); PG8_STAGE(PG8_SB(1, 1), b3 + hstep, voffB); PG8_STAGE(PG8_SA(1, 0), a3, voffA);
;             PG8_WAIT_V(8); PG8_WAIT_L(0); PG8_BAR; PG8_MMA(1, 0, At, B0); PG8_MMA(1, 1, At, B1); PG8_BAR; PG8_SCHED;
	s_add_i32 s60, s72, s17
	v_lshl_add_u64 v[174:175], v[174:175], 0, s[34:35]
	s_mov_b32 m0, s60
	ds_read_b128 v[186:189], v184 offset:49152
	ds_read_b128 v[190:193], v184 offset:50176
	ds_read_b128 v[208:211], v184 offset:51200
	ds_read_b128 v[212:215], v184 offset:52224
	ds_read_b128 v[216:219], v184 offset:53248
	ds_read_b128 v[220:223], v184 offset:54272
	ds_read_b128 v[228:231], v184 offset:55296
	ds_read_b128 v[232:235], v184 offset:56320
	global_load_lds_dwordx4 v[174:175], off
	s_add_i32 m0, s60, 0x2000
	s_add_u32 s58, s58, 0x20080
	v_lshl_add_u64 v[174:175], v[176:177], 0, s[34:35]
	s_addc_u32 s59, s59, 0
	s_add_i32 s60, s73, s17
	global_load_lds_dwordx4 v[174:175], off
	s_mov_b32 m0, s60
	s_nop 0
	global_load_lds_dwordx4 v2, s[58:59]
	s_add_i32 m0, s60, 0x2000
	s_nop 0
	global_load_lds_dwordx4 v164, s[58:59]
	v_lshl_add_u64 v[174:175], v[178:179], 0, s[34:35]
	s_mov_b32 m0, s63
	s_nop 0
	global_load_lds_dwordx4 v[174:175], off
	v_lshl_add_u64 v[174:175], v[180:181], 0, s[34:35]
	s_mov_b32 m0, s64
	s_nop 0
	global_load_lds_dwordx4 v[174:175], off
	s_waitcnt vmcnt(8)
	s_waitcnt lgkmcnt(0)
	s_barrier
	s_setprio 1
	s_waitcnt lgkmcnt(0)
	v_mfma_scale_f32_16x16x128_f8f6f4 v[96:99], v[4:11], v[186:193], v[96:99], v245, v245 op_sel_hi:[0,0,0]
	v_mfma_scale_f32_16x16x128_f8f6f4 v[92:95], v[12:19], v[186:193], v[92:95], v245, v245 op_sel_hi:[0,0,0]
	v_mfma_scale_f32_16x16x128_f8f6f4 v[80:83], v[4:11], v[208:215], v[80:83], v245, v245 op_sel_hi:[0,0,0]
	v_mfma_scale_f32_16x16x128_f8f6f4 v[76:79], v[12:19], v[208:215], v[76:79], v245, v245 op_sel_hi:[0,0,0]
	v_mfma_scale_f32_16x16x128_f8f6f4 v[64:67], v[4:11], v[216:223], v[64:67], v245, v245 op_sel_hi:[0,0,0]
	v_mfma_scale_f32_16x16x128_f8f6f4 v[60:63], v[12:19], v[216:223], v[60:63], v245, v245 op_sel_hi:[0,0,0]
	v_mfma_scale_f32_16x16x128_f8f6f4 v[48:51], v[4:11], v[228:235], v[48:51], v245, v245 op_sel_hi:[0,0,0]
	v_mfma_scale_f32_16x16x128_f8f6f4 v[44:47], v[12:19], v[228:235], v[44:47], v245, v245 op_sel_hi:[0,0,0]
	s_setprio 0
	s_setprio 1
	v_mfma_scale_f32_16x16x128_f8f6f4 v[88:91], v[20:27], v[186:193], v[88:91], v245, v245 op_sel_hi:[0,0,0]
	v_mfma_scale_f32_16x16x128_f8f6f4 v[84:87], v[28:35], v[186:193], v[84:87], v245, v245 op_sel_hi:[0,0,0]
	v_mfma_scale_f32_16x16x128_f8f6f4 v[72:75], v[20:27], v[208:215], v[72:75], v245, v245 op_sel_hi:[0,0,0]
	v_mfma_scale_f32_16x16x128_f8f6f4 v[68:71], v[28:35], v[208:215], v[68:71], v245, v245 op_sel_hi:[0,0,0]
	v_mfma_scale_f32_16x16x128_f8f6f4 v[56:59], v[20:27], v[216:223], v[56:59], v245, v245 op_sel_hi:[0,0,0]
	v_mfma_scale_f32_16x16x128_f8f6f4 v[52:55], v[28:35], v[216:223], v[52:55], v245, v245 op_sel_hi:[0,0,0]
	v_mfma_scale_f32_16x16x128_f8f6f4 v[40:43], v[20:27], v[228:235], v[40:43], v245, v245 op_sel_hi:[0,0,0]
	v_mfma_scale_f32_16x16x128_f8f6f4 v[36:39], v[28:35], v[228:235], v[36:39], v245, v245 op_sel_hi:[0,0,0]
	s_setprio 0
	s_add_u32 s56, s56, 0x100
	s_addc_u32 s57, s57, 0
	s_add_u32 s69, s69, 0x100
	s_addc_u32 s70, s70, 0
	s_cmp_gt_u32 s71, 5
	s_mov_b32 s58, s71
	s_cbranch_scc1 .Lrot7_exit
	s_add_i32 s71, s58, 2
	s_add_u32 s59, s56, 0xfffe0080
	s_addc_u32 s60, s57, -1
	s_add_i32 s72, 0, 0x10000
	s_cmp_eq_u32 s58, 4
	s_cselect_b32 s61, s4, s60
	s_cselect_b32 s60, s5, s59
	s_cselect_b32 s59, s49, s70
	s_cselect_b32 s58, s51, s69
	s_add_i32 s73, 0, 0x14000
	v_add_u32_e32 v4, s72, v183
	v_add_u32_e32 v8, s73, v183
	s_barrier
	s_branch .Lrot7_body

; #define PG8_STAGE(bufoff, gbase, voff) do { _Pragma("unroll") for (int _i = 0; _i < 2; ++_i) \
;         __builtin_amdgcn_global_load_lds((const unsigned*)((const char*)(gbase) + (voff)[_i]), (PG8_LAS unsigned*)(lds + (bufoff) + ldsw + _i * 8192), 16, 0, 0); } while (0)
; #define PG8_LDA(dst, b, h) do { _Pragma("unroll") for (int m = 0; m < 4; ++m) _Pragma("unroll") for (int k = 0; k < 2; ++k) dst[m][k] = *(const PG8_LAS bf16x8*)(lds + PG8_SA(b, h) + aoff + m * 2048 + k * 1024); } while (0)
; #define PG8_LDB(dst, b, h) do { _Pragma("unroll") for (int n = 0; n < 2; ++n) _Pragma("unroll") for (int k = 0; k < 2; ++k) dst[n][k] = *(const PG8_LAS bf16x8*)(lds + PG8_SB(b, h) + boff + n * 2048 + k * 1024); } while (0)
; #define PG8_WAIT_V8_UNLESS_FIRST(t) asm volatile("s_cmp_eq_u32 %0, 0\n\ts_cbranch_scc1 .Lpg8skip%=\n\ts_waitcnt vmcnt(8)\n.Lpg8skip%=:" :: "s"(t) : "scc", "memory")
; #define PG8_WAIT_L(n) asm volatile("s_waitcnt lgkmcnt(" #n ")" ::: "memory")
; #define PG8_BAR __builtin_amdgcn_s_barrier()
; #define PG8_SCHED __builtin_amdgcn_sched_barrier(0)
; template <class Epi, class Sched, bool ALIGN_EPI = false, bool SP2 = false, bool FP8 = false, bool ABLK = false>
; __device__ __forceinline__ void gemm_phase(PG8_LAS unsigned char* lds, const Gemm g, const Sched& S, const Epi& E) {
;     ...
;             PG8_LDB(B0, 0, 0); PG8_LDB(B1, 0, 1); PG8_SCHED; PG8_LDA(At, 0, 0); PG8_STAGE(PG8_SA(1, 1), a1 + hstepA, voffA);
;             PG8_WAIT_V8_UNLESS_FIRST(t); PG8_WAIT_L(0); PG8_BAR; PG8_MMA(0, 0, At, B0); PG8_MMA(0, 1, At, B1); PG8_BAR; PG8_SCHED;
.Lrot8_body:
	ds_read_b128 v[124:127], v144
	ds_read_b128 v[136:139], v144 offset:1024
	ds_read_b128 v[140:143], v144 offset:2048
	ds_read_b128 v[144:147], v144 offset:3072
	ds_read_b128 v[148:151], v166
	ds_read_b128 v[152:155], v166 offset:1024
	ds_read_b128 v[172:175], v166 offset:2048
	ds_read_b128 v[176:179], v166 offset:3072
	s_add_i32 m0, s20, 0xc000
	ds_read_b128 v[180:183], v170
	ds_read_b128 v[184:187], v170 offset:1024
	ds_read_b128 v[188:191], v170 offset:2048
	ds_read_b128 v[192:195], v170 offset:3072
	ds_read_b128 v[208:211], v170 offset:4096
	ds_read_b128 v[212:215], v170 offset:5120
	ds_read_b128 v[216:219], v170 offset:6144
	ds_read_b128 v[220:223], v170 offset:7168
	global_load_lds_dwordx4 v162, s[58:59]
	s_add_i32 m0, s20, 0xe000
	s_nop 0
	global_load_lds_dwordx4 v164, s[58:59]
	s_cmp_eq_u32 s73, 0
	s_cbranch_scc1 .Lpg8skip16
	s_waitcnt vmcnt(8)

; #define PG8_STAGE(bufoff, gbase, voff) do { _Pragma("unroll") for (int _i = 0; _i < 2; ++_i) \
;         __builtin_amdgcn_global_load_lds((const unsigned*)((const char*)(gbase) + (voff)[_i]), (PG8_LAS unsigned*)(lds + (bufoff) + ldsw + _i * 8192), 16, 0, 0); } while (0)
; #define PG8_LDA(dst, b, h) do { _Pragma("unroll") for (int m = 0; m < 4; ++m) _Pragma("unroll") for (int k = 0; k < 2; ++k) dst[m][k] = *(const PG8_LAS bf16x8*)(lds + PG8_SA(b, h) + aoff + m * 2048 + k * 1024); } while (0)
; #define PG8_LDB(dst, b, h) do { _Pragma("unroll") for (int n = 0; n < 2; ++n) _Pragma("unroll") for (int k = 0; k < 2; ++k) dst[n][k] = *(const PG8_LAS bf16x8*)(lds + PG8_SB(b, h) + boff + n * 2048 + k * 1024); } while (0)
; #define PG8_WAIT_V(n) asm volatile("s_waitcnt vmcnt(" #n ")" ::: "memory")
; #define PG8_WAIT_V8_UNLESS_FIRST(t) asm volatile("s_cmp_eq_u32 %0, 0\n\ts_cbranch_scc1 .Lpg8skip%=\n\ts_waitcnt vmcnt(8)\n.Lpg8skip%=:" :: "s"(t) : "scc", "memory")
; #define PG8_WAIT_L(n) asm volatile("s_waitcnt lgkmcnt(" #n ")" ::: "memory")
; #define PG8_BAR __builtin_amdgcn_s_barrier()
; #define PG8_SCHED __builtin_amdgcn_sched_barrier(0)
; template <class Epi, class Sched, bool ALIGN_EPI = false, bool SP2 = false, bool FP8 = false, bool ABLK = false>
; __device__ __forceinline__ void gemm_phase(PG8_LAS unsigned char* lds, const Gemm g, const Sched& S, const Epi& E) {
;     ...
;             PG8_WAIT_V8_UNLESS_FIRST(t); PG8_WAIT_L(0); PG8_BAR; PG8_MMA(1, 0, At, B0); PG8_MMA(1, 1, At, B1); PG8_BAR; PG8_SCHED;
;             PG8_LDB(B0, 1, 0); PG8_LDB(B1, 1, 1); PG8_SCHED; PG8_LDA(At, 1, 0); PG8_STAGE(PG8_SA(0, 1), a2 + hstepA, voffA);
;             PG8_WAIT_V(8); PG8_WAIT_L(0); PG8_BAR; PG8_MMA(0, 0, At, B0); PG8_MMA(0, 1, At, B1); PG8_BAR; PG8_SCHED;
.Lpg8skip17:
	s_waitcnt lgkmcnt(0)
	s_barrier
	s_setprio 1
	s_waitcnt lgkmcnt(0)
	v_mfma_f32_16x16x32_bf16 v[64:67], v[124:127], v[180:183], v[64:67]
	v_mfma_f32_16x16x32_bf16 v[56:59], v[140:143], v[180:183], v[56:59]
	v_mfma_f32_16x16x32_bf16 v[48:51], v[124:127], v[188:191], v[48:51]
	v_mfma_f32_16x16x32_bf16 v[40:43], v[140:143], v[188:191], v[40:43]
	v_mfma_f32_16x16x32_bf16 v[32:35], v[124:127], v[208:211], v[32:35]
	v_mfma_f32_16x16x32_bf16 v[24:27], v[140:143], v[208:211], v[24:27]
	v_mfma_f32_16x16x32_bf16 v[16:19], v[124:127], v[216:219], v[16:19]
	v_mfma_f32_16x16x32_bf16 v[8:11], v[140:143], v[216:219], v[8:11]
	v_mfma_f32_16x16x32_bf16 v[64:67], v[136:139], v[184:187], v[64:67]
	v_mfma_f32_16x16x32_bf16 v[56:59], v[144:147], v[184:187], v[56:59]
	v_mfma_f32_16x16x32_bf16 v[48:51], v[136:139], v[192:195], v[48:51]
	v_mfma_f32_16x16x32_bf16 v[40:43], v[144:147], v[192:195], v[40:43]
	v_mfma_f32_16x16x32_bf16 v[32:35], v[136:139], v[212:215], v[32:35]
	v_mfma_f32_16x16x32_bf16 v[24:27], v[144:147], v[212:215], v[24:27]
	v_mfma_f32_16x16x32_bf16 v[16:19], v[136:139], v[220:223], v[16:19]
	v_mfma_f32_16x16x32_bf16 v[8:11], v[144:147], v[220:223], v[8:11]
	s_setprio 0
	s_setprio 1
	v_mfma_f32_16x16x32_bf16 v[60:63], v[148:151], v[180:183], v[60:63]
	v_mfma_f32_16x16x32_bf16 v[52:55], v[172:175], v[180:183], v[52:55]
	v_mfma_f32_16x16x32_bf16 v[44:47], v[148:151], v[188:191], v[44:47]
	v_mfma_f32_16x16x32_bf16 v[36:39], v[172:175], v[188:191], v[36:39]
	v_mfma_f32_16x16x32_bf16 v[28:31], v[148:151], v[208:211], v[28:31]
	v_mfma_f32_16x16x32_bf16 v[20:23], v[172:175], v[208:211], v[20:23]
	v_mfma_f32_16x16x32_bf16 v[12:15], v[148:151], v[216:219], v[12:15]
	v_mfma_f32_16x16x32_bf16 v[4:7], v[172:175], v[216:219], v[4:7]
	v_mfma_f32_16x16x32_bf16 v[60:63], v[152:155], v[184:187], v[60:63]
	v_mfma_f32_16x16x32_bf16 v[52:55], v[176:179], v[184:187], v[52:55]
	v_mfma_f32_16x16x32_bf16 v[44:47], v[152:155], v[192:195], v[44:47]
	v_mfma_f32_16x16x32_bf16 v[36:39], v[176:179], v[192:195], v[36:39]
	v_mfma_f32_16x16x32_bf16 v[28:31], v[152:155], v[212:215], v[28:31]
	v_mfma_f32_16x16x32_bf16 v[20:23], v[176:179], v[212:215], v[20:23]
	v_mfma_f32_16x16x32_bf16 v[12:15], v[152:155], v[220:223], v[12:15]
	v_mfma_f32_16x16x32_bf16 v[4:7], v[176:179], v[220:223], v[4:7]
	s_setprio 0
	s_barrier
	s_add_i32 s74, 0, 0x18000
	s_add_i32 s75, 0, 0x1c000
	v_add_u32_e32 v144, s74, v169
	v_add_u32_e32 v171, s75, v169
	ds_read_b128 v[124:127], v144
	ds_read_b128 v[136:139], v144 offset:1024
	ds_read_b128 v[140:143], v144 offset:2048
	ds_read_b128 v[144:147], v144 offset:3072
	ds_read_b128 v[148:151], v171
	ds_read_b128 v[152:155], v171 offset:1024
	ds_read_b128 v[172:175], v171 offset:2048
	ds_read_b128 v[176:179], v171 offset:3072
	s_add_u32 s62, s62, 0x40000
	s_addc_u32 s63, s63, 0
	s_mov_b32 m0, s22
	ds_read_b128 v[180:183], v170 offset:32768
	ds_read_b128 v[184:187], v170 offset:33792
	ds_read_b128 v[188:191], v170 offset:34816
	ds_read_b128 v[192:195], v170 offset:35840
	ds_read_b128 v[208:211], v170 offset:36864
	ds_read_b128 v[212:215], v170 offset:37888
	ds_read_b128 v[216:219], v170 offset:38912
	ds_read_b128 v[220:223], v170 offset:39936
	global_load_lds_dwordx4 v160, s[62:63]
	s_mov_b32 m0, s23
	s_nop 0
	global_load_lds_dwordx4 v158, s[62:63]
	s_waitcnt vmcnt(8)
	s_waitcnt lgkmcnt(0)
	s_barrier
	s_setprio 1
	s_waitcnt lgkmcnt(0)
	v_mfma_f32_16x16x32_bf16 v[132:135], v[124:127], v[180:183], v[132:135]
	v_mfma_f32_16x16x32_bf16 v[128:131], v[140:143], v[180:183], v[128:131]
	v_mfma_f32_16x16x32_bf16 v[112:115], v[124:127], v[188:191], v[112:115]
	v_mfma_f32_16x16x32_bf16 v[104:107], v[140:143], v[188:191], v[104:107]
	v_mfma_f32_16x16x32_bf16 v[96:99], v[124:127], v[208:211], v[96:99]
	v_mfma_f32_16x16x32_bf16 v[88:91], v[140:143], v[208:211], v[88:91]
	v_mfma_f32_16x16x32_bf16 v[80:83], v[124:127], v[216:219], v[80:83]
	v_mfma_f32_16x16x32_bf16 v[72:75], v[140:143], v[216:219], v[72:75]
	v_mfma_f32_16x16x32_bf16 v[132:135], v[136:139], v[184:187], v[132:135]
	v_mfma_f32_16x16x32_bf16 v[128:131], v[144:147], v[184:187], v[128:131]
	v_mfma_f32_16x16x32_bf16 v[112:115], v[136:139], v[192:195], v[112:115]
	v_mfma_f32_16x16x32_bf16 v[104:107], v[144:147], v[192:195], v[104:107]
	v_mfma_f32_16x16x32_bf16 v[96:99], v[136:139], v[212:215], v[96:99]
	v_mfma_f32_16x16x32_bf16 v[88:91], v[144:147], v[212:215], v[88:91]
	v_mfma_f32_16x16x32_bf16 v[80:83], v[136:139], v[220:223], v[80:83]
	v_mfma_f32_16x16x32_bf16 v[72:75], v[144:147], v[220:223], v[72:75]
	s_setprio 0
	s_setprio 1
	v_mfma_f32_16x16x32_bf16 v[120:123], v[148:151], v[180:183], v[120:123]
	v_mfma_f32_16x16x32_bf16 v[116:119], v[172:175], v[180:183], v[116:119]
	v_mfma_f32_16x16x32_bf16 v[108:111], v[148:151], v[188:191], v[108:111]
	v_mfma_f32_16x16x32_bf16 v[100:103], v[172:175], v[188:191], v[100:103]
	v_mfma_f32_16x16x32_bf16 v[92:95], v[148:151], v[208:211], v[92:95]
	v_mfma_f32_16x16x32_bf16 v[84:87], v[172:175], v[208:211], v[84:87]
	v_mfma_f32_16x16x32_bf16 v[76:79], v[148:151], v[216:219], v[76:79]
	v_mfma_f32_16x16x32_bf16 v[68:71], v[172:175], v[216:219], v[68:71]
	v_mfma_f32_16x16x32_bf16 v[120:123], v[152:155], v[184:187], v[120:123]
	v_mfma_f32_16x16x32_bf16 v[116:119], v[176:179], v[184:187], v[116:119]
	v_mfma_f32_16x16x32_bf16 v[108:111], v[152:155], v[192:195], v[108:111]
	v_mfma_f32_16x16x32_bf16 v[100:103], v[176:179], v[192:195], v[100:103]
	v_mfma_f32_16x16x32_bf16 v[92:95], v[152:155], v[212:215], v[92:95]
	v_mfma_f32_16x16x32_bf16 v[84:87], v[176:179], v[212:215], v[84:87]
	v_mfma_f32_16x16x32_bf16 v[76:79], v[152:155], v[220:223], v[76:79]
	v_mfma_f32_16x16x32_bf16 v[68:71], v[176:179], v[220:223], v[68:71]
	s_setprio 0
	s_barrier
; #define PG8_STAGE(bufoff, gbase, voff) do { _Pragma("unroll") for (int _i = 0; _i < 2; ++_i) \
;         __builtin_amdgcn_global_load_lds((const unsigned*)((const char*)(gbase) + (voff)[_i]), (PG8_LAS unsigned*)(lds + (bufoff) + ldsw + _i * 8192), 16, 0, 0); } while (0)
; #define PG8_WAIT_V(n) asm volatile("s_waitcnt vmcnt(" #n ")" ::: "memory")
; #define PG8_WAIT_L(n) asm volatile("s_waitcnt lgkmcnt(" #n ")" ::: "memory")
; #define PG8_BAR __builtin_amdgcn_s_barrier()
; template <class Epi, class Sched, bool ALIGN_EPI = false, bool SP2 = false, bool FP8 = false, bool ABLK = false>
; __device__ __forceinline__ void gemm_phase(PG8_LAS unsigned char* lds, const Gemm g, const Sched& S, const Epi& E) {
;     ...
;         for (int t = 0; t < nt; t += 2) {
;             const bool last = (t == nt - 2);
;             const char* a1 = cA + (size_t)(t + 1) * kstepA;
;             const char* a2 = last ? nA : cA + (size_t)(t + 2) * kstepA; const char* b2 = last ? nB : cB + (size_t)(t + 2) * kstep;
;             const char* a3 = a2 + kstepA; const char* b3 = b2 + kstep;
;             if (last && has_next) S.a_ready(nxt);
;             if constexpr (SP2) {
;             PG8_LDB(B0, 0, 0); PG8_LDB(B1, 0, 1); PG8_SCHED; PG8_LDA(At, 0, 0); PG8_STAGE(PG8_SA(1, 1), a1 + hstepA, voffA);
;             PG8_WAIT_V8_UNLESS_FIRST(t); PG8_WAIT_L(0); PG8_BAR; PG8_MMA(0, 0, At, B0); PG8_MMA(0, 1, At, B1); PG8_BAR; PG8_SCHED;
;             PG8_LDA(At, 0, 1); PG8_STAGE(PG8_SB(0, 0), b2, voffB); PG8_STAGE(PG8_SB(0, 1), b2 + hstep, voffB); PG8_STAGE(PG8_SA(0, 0), a2, voffA);
;             PG8_WAIT_V8_UNLESS_FIRST(t); PG8_WAIT_L(0); PG8_BAR; PG8_MMA(1, 0, At, B0); PG8_MMA(1, 1, At, B1); PG8_BAR; PG8_SCHED;
;             PG8_LDB(B0, 1, 0); PG8_LDB(B1, 1, 1); PG8_SCHED; PG8_LDA(At, 1, 0); PG8_STAGE(PG8_SA(0, 1), a2 + hstepA, voffA);
;             PG8_WAIT_V(8); PG8_WAIT_L(0); PG8_BAR; PG8_MMA(0, 0, At, B0); PG8_MMA(0, 1, At, B1); PG8_BAR; PG8_SCHED;
;             PG8_LDA(At, 1, 1); PG8_STAGE(PG8_SB(1, 0), b3, voffB); PG8_STAGE(PG8_SB(1, 1), b3 + hstep, voffB); PG8_STAGE(PG8_SA(1, 0), a3, voffA);
;             PG8_WAIT_V(8); PG8_WAIT_L(0); PG8_BAR; PG8_MMA(1, 0, At, B0); PG8_MMA(1, 1, At, B1); PG8_BAR; PG8_SCHED;
;     ...
;         if constexpr (SP2) PG8_WAIT_V(0);
;         if constexpr (FP8) asm volatile("s_nop 15\n\ts_nop 15" ::: "memory");
;         if constexpr (ALIGN_EPI) { if (wr == 0) PG8_BAR; }
	s_add_i32 s62, s74, s19
	v_lshl_add_u64 v[166:167], v[166:167], 0, s[34:35]
	s_mov_b32 m0, s62
	ds_read_b128 v[180:183], v170 offset:49152
	ds_read_b128 v[184:187], v170 offset:50176
	ds_read_b128 v[188:191], v170 offset:51200
	ds_read_b128 v[192:195], v170 offset:52224
	ds_read_b128 v[208:211], v170 offset:53248
	ds_read_b128 v[212:215], v170 offset:54272
	ds_read_b128 v[216:219], v170 offset:55296
	ds_read_b128 v[220:223], v170 offset:56320
	global_load_lds_dwordx4 v[166:167], off
	s_add_i32 m0, s62, 0x2000
	s_add_u32 s60, s60, 0x40080
	v_lshl_add_u64 v[166:167], v[204:205], 0, s[34:35]
	s_addc_u32 s61, s61, 0
	s_add_i32 s62, s75, s19
	global_load_lds_dwordx4 v[166:167], off
	s_mov_b32 m0, s62
	s_nop 0
	global_load_lds_dwordx4 v2, s[60:61]
	s_add_i32 m0, s62, 0x2000
	s_nop 0
	global_load_lds_dwordx4 v156, s[60:61]
	v_lshl_add_u64 v[166:167], v[206:207], 0, s[34:35]
	s_mov_b32 m0, s65
	s_nop 0
	global_load_lds_dwordx4 v[166:167], off
	v_lshl_add_u64 v[166:167], v[224:225], 0, s[34:35]
	s_mov_b32 m0, s66
	s_nop 0
	global_load_lds_dwordx4 v[166:167], off
	s_waitcnt vmcnt(8)
	s_waitcnt lgkmcnt(0)
	s_barrier
	s_setprio 1
	s_waitcnt lgkmcnt(0)
	v_mfma_f32_16x16x32_bf16 v[64:67], v[124:127], v[180:183], v[64:67]
	v_mfma_f32_16x16x32_bf16 v[56:59], v[140:143], v[180:183], v[56:59]
	v_mfma_f32_16x16x32_bf16 v[48:51], v[124:127], v[188:191], v[48:51]
	v_mfma_f32_16x16x32_bf16 v[40:43], v[140:143], v[188:191], v[40:43]
	v_mfma_f32_16x16x32_bf16 v[32:35], v[124:127], v[208:211], v[32:35]
	v_mfma_f32_16x16x32_bf16 v[24:27], v[140:143], v[208:211], v[24:27]
	v_mfma_f32_16x16x32_bf16 v[16:19], v[124:127], v[216:219], v[16:19]
	v_mfma_f32_16x16x32_bf16 v[8:11], v[140:143], v[216:219], v[8:11]
	v_mfma_f32_16x16x32_bf16 v[64:67], v[136:139], v[184:187], v[64:67]
	v_mfma_f32_16x16x32_bf16 v[56:59], v[144:147], v[184:187], v[56:59]
	v_mfma_f32_16x16x32_bf16 v[48:51], v[136:139], v[192:195], v[48:51]
	v_mfma_f32_16x16x32_bf16 v[40:43], v[144:147], v[192:195], v[40:43]
	v_mfma_f32_16x16x32_bf16 v[32:35], v[136:139], v[212:215], v[32:35]
	v_mfma_f32_16x16x32_bf16 v[24:27], v[144:147], v[212:215], v[24:27]
	v_mfma_f32_16x16x32_bf16 v[16:19], v[136:139], v[220:223], v[16:19]
	v_mfma_f32_16x16x32_bf16 v[8:11], v[144:147], v[220:223], v[8:11]
	s_setprio 0
	s_setprio 1
	v_mfma_f32_16x16x32_bf16 v[60:63], v[148:151], v[180:183], v[60:63]
	v_mfma_f32_16x16x32_bf16 v[52:55], v[172:175], v[180:183], v[52:55]
	v_mfma_f32_16x16x32_bf16 v[44:47], v[148:151], v[188:191], v[44:47]
	v_mfma_f32_16x16x32_bf16 v[36:39], v[172:175], v[188:191], v[36:39]
	v_mfma_f32_16x16x32_bf16 v[28:31], v[148:151], v[208:211], v[28:31]
	v_mfma_f32_16x16x32_bf16 v[20:23], v[172:175], v[208:211], v[20:23]
	v_mfma_f32_16x16x32_bf16 v[12:15], v[148:151], v[216:219], v[12:15]
	v_mfma_f32_16x16x32_bf16 v[4:7], v[172:175], v[216:219], v[4:7]
	v_mfma_f32_16x16x32_bf16 v[60:63], v[152:155], v[184:187], v[60:63]
	v_mfma_f32_16x16x32_bf16 v[52:55], v[176:179], v[184:187], v[52:55]
	v_mfma_f32_16x16x32_bf16 v[44:47], v[152:155], v[192:195], v[44:47]
	v_mfma_f32_16x16x32_bf16 v[36:39], v[176:179], v[192:195], v[36:39]
	v_mfma_f32_16x16x32_bf16 v[28:31], v[152:155], v[212:215], v[28:31]
	v_mfma_f32_16x16x32_bf16 v[20:23], v[176:179], v[212:215], v[20:23]
	v_mfma_f32_16x16x32_bf16 v[12:15], v[152:155], v[220:223], v[12:15]
	v_mfma_f32_16x16x32_bf16 v[4:7], v[176:179], v[220:223], v[4:7]
	s_setprio 0
	s_add_u32 s58, s58, 0x100
	s_addc_u32 s59, s59, 0
	s_add_u32 s71, s71, 0x100
	s_addc_u32 s72, s72, 0
	s_cmp_gt_u32 s73, 13
	s_mov_b32 s60, s73
	s_cbranch_scc1 .Lrot8_exit
	s_add_i32 s73, s60, 2
	s_add_u32 s61, s58, 0xfffc0080
	s_addc_u32 s62, s59, -1
	s_add_i32 s74, 0, 0x10000
	s_cmp_eq_u32 s60, 12
	s_cselect_b32 s63, s4, s62
	s_cselect_b32 s62, s5, s61
	s_cselect_b32 s61, s51, s72
	s_cselect_b32 s60, s53, s71
	s_add_i32 s76, 0, 0x14000
	v_add_u32_e32 v144, s74, v169
	v_add_u32_e32 v166, s76, v169
	s_barrier
	s_branch .Lrot8_body
.Lrot8_exit:
	s_barrier
	s_waitcnt vmcnt(0)
	s_and_b64 vcc, exec, s[48:49]
	s_cbranch_vccz .LBB0_1712
	s_barrier

; #define PG8_STAGE(bufoff, gbase, voff) do { _Pragma("unroll") for (int _i = 0; _i < 2; ++_i) \
;         __builtin_amdgcn_global_load_lds((const unsigned*)((const char*)(gbase) + (voff)[_i]), (PG8_LAS unsigned*)(lds + (bufoff) + ldsw + _i * 8192), 16, 0, 0); } while (0)
; #define PG8_LDA(dst, b, h) do { _Pragma("unroll") for (int m = 0; m < 4; ++m) _Pragma("unroll") for (int k = 0; k < 2; ++k) dst[m][k] = *(const PG8_LAS bf16x8*)(lds + PG8_SA(b, h) + aoff + m * 2048 + k * 1024); } while (0)
; #define PG8_LDB(dst, b, h) do { _Pragma("unroll") for (int n = 0; n < 2; ++n) _Pragma("unroll") for (int k = 0; k < 2; ++k) dst[n][k] = *(const PG8_LAS bf16x8*)(lds + PG8_SB(b, h) + boff + n * 2048 + k * 1024); } while (0)
; #define PG8_WAIT_V8_UNLESS_FIRST(t) asm volatile("s_cmp_eq_u32 %0, 0\n\ts_cbranch_scc1 .Lpg8skip%=\n\ts_waitcnt vmcnt(8)\n.Lpg8skip%=:" :: "s"(t) : "scc", "memory")
; #define PG8_WAIT_L(n) asm volatile("s_waitcnt lgkmcnt(" #n ")" ::: "memory")
; #define PG8_BAR __builtin_amdgcn_s_barrier()
; #define PG8_SCHED __builtin_amdgcn_sched_barrier(0)
; template <class Epi, class Sched, bool ALIGN_EPI = false, bool SP2 = false, bool FP8 = false, bool ABLK = false>
; __device__ __forceinline__ void gemm_phase(PG8_LAS unsigned char* lds, const Gemm g, const Sched& S, const Epi& E) {
;     ...
;             PG8_LDB(B0, 0, 0); PG8_LDB(B1, 0, 1); PG8_SCHED; PG8_LDA(At, 0, 0); PG8_STAGE(PG8_SA(1, 1), a1 + hstepA, voffA);
;             PG8_WAIT_V8_UNLESS_FIRST(t); PG8_WAIT_L(0); PG8_BAR; PG8_MMA(0, 0, At, B0); PG8_MMA(0, 1, At, B1); PG8_BAR; PG8_SCHED;
.Lrot9_body:
	ds_read_b128 v[28:31], v4
	ds_read_b128 v[32:35], v4 offset:1024
	ds_read_b128 v[20:23], v4 offset:2048
	ds_read_b128 v[24:27], v4 offset:3072
	ds_read_b128 v[12:15], v8
	ds_read_b128 v[16:19], v8 offset:1024
	s_waitcnt lgkmcnt(0)
	ds_read_b128 v[4:7], v8 offset:2048
	ds_read_b128 v[8:11], v8 offset:3072
	v_lshl_add_u64 v[178:179], v[174:175], 0, s[54:55]
	s_add_i32 m0, s18, 0xc000
	ds_read_b128 v[186:189], v184
	ds_read_b128 v[190:193], v184 offset:1024
	ds_read_b128 v[208:211], v184 offset:2048
	ds_read_b128 v[212:215], v184 offset:3072
	ds_read_b128 v[216:219], v184 offset:4096
	ds_read_b128 v[220:223], v184 offset:5120
	ds_read_b128 v[228:231], v184 offset:6144
	ds_read_b128 v[232:235], v184 offset:7168
	global_load_lds_dwordx4 v[178:179], off
	v_lshl_add_u64 v[178:179], v[176:177], 0, s[54:55]
	s_add_i32 m0, s18, 0xe000
	s_nop 0
	global_load_lds_dwordx4 v[178:179], off
	s_cmp_eq_u32 s70, 0
	s_cbranch_scc1 .Lpg8skip18
	s_waitcnt vmcnt(8)

; #define PG8_STAGE(bufoff, gbase, voff) do { _Pragma("unroll") for (int _i = 0; _i < 2; ++_i) \
;         __builtin_amdgcn_global_load_lds((const unsigned*)((const char*)(gbase) + (voff)[_i]), (PG8_LAS unsigned*)(lds + (bufoff) + ldsw + _i * 8192), 16, 0, 0); } while (0)
; #define PG8_LDA(dst, b, h) do { _Pragma("unroll") for (int m = 0; m < 4; ++m) _Pragma("unroll") for (int k = 0; k < 2; ++k) dst[m][k] = *(const PG8_LAS bf16x8*)(lds + PG8_SA(b, h) + aoff + m * 2048 + k * 1024); } while (0)
; #define PG8_LDB(dst, b, h) do { _Pragma("unroll") for (int n = 0; n < 2; ++n) _Pragma("unroll") for (int k = 0; k < 2; ++k) dst[n][k] = *(const PG8_LAS bf16x8*)(lds + PG8_SB(b, h) + boff + n * 2048 + k * 1024); } while (0)
; #define PG8_WAIT_V(n) asm volatile("s_waitcnt vmcnt(" #n ")" ::: "memory")
; #define PG8_WAIT_V8_UNLESS_FIRST(t) asm volatile("s_cmp_eq_u32 %0, 0\n\ts_cbranch_scc1 .Lpg8skip%=\n\ts_waitcnt vmcnt(8)\n.Lpg8skip%=:" :: "s"(t) : "scc", "memory")
; #define PG8_WAIT_L(n) asm volatile("s_waitcnt lgkmcnt(" #n ")" ::: "memory")
; #define PG8_BAR __builtin_amdgcn_s_barrier()
; #define PG8_SCHED __builtin_amdgcn_sched_barrier(0)
; template <class Epi, class Sched, bool ALIGN_EPI = false, bool SP2 = false, bool FP8 = false, bool ABLK = false>
; __device__ __forceinline__ void gemm_phase(PG8_LAS unsigned char* lds, const Gemm g, const Sched& S, const Epi& E) {
;     ...
;             PG8_WAIT_V8_UNLESS_FIRST(t); PG8_WAIT_L(0); PG8_BAR; PG8_MMA(1, 0, At, B0); PG8_MMA(1, 1, At, B1); PG8_BAR; PG8_SCHED;
;             PG8_LDB(B0, 1, 0); PG8_LDB(B1, 1, 1); PG8_SCHED; PG8_LDA(At, 1, 0); PG8_STAGE(PG8_SA(0, 1), a2 + hstepA, voffA);
;             PG8_WAIT_V(8); PG8_WAIT_L(0); PG8_BAR; PG8_MMA(0, 0, At, B0); PG8_MMA(0, 1, At, B1); PG8_BAR; PG8_SCHED;
.Lpg8skip19:
	s_waitcnt lgkmcnt(0)
	s_barrier
	s_setprio 1
	s_waitcnt lgkmcnt(0)
	v_mfma_scale_f32_16x16x128_f8f6f4 v[96:99], v[28:35], v[186:193], v[96:99], v245, v245 op_sel_hi:[0,0,0]
	v_mfma_scale_f32_16x16x128_f8f6f4 v[92:95], v[20:27], v[186:193], v[92:95], v245, v245 op_sel_hi:[0,0,0]
	v_mfma_scale_f32_16x16x128_f8f6f4 v[80:83], v[28:35], v[208:215], v[80:83], v245, v245 op_sel_hi:[0,0,0]
	v_mfma_scale_f32_16x16x128_f8f6f4 v[76:79], v[20:27], v[208:215], v[76:79], v245, v245 op_sel_hi:[0,0,0]
	v_mfma_scale_f32_16x16x128_f8f6f4 v[64:67], v[28:35], v[216:223], v[64:67], v245, v245 op_sel_hi:[0,0,0]
	v_mfma_scale_f32_16x16x128_f8f6f4 v[60:63], v[20:27], v[216:223], v[60:63], v245, v245 op_sel_hi:[0,0,0]
	v_mfma_scale_f32_16x16x128_f8f6f4 v[48:51], v[28:35], v[228:235], v[48:51], v245, v245 op_sel_hi:[0,0,0]
	v_mfma_scale_f32_16x16x128_f8f6f4 v[44:47], v[20:27], v[228:235], v[44:47], v245, v245 op_sel_hi:[0,0,0]
	s_setprio 0
	s_setprio 1
	v_mfma_scale_f32_16x16x128_f8f6f4 v[88:91], v[12:19], v[186:193], v[88:91], v245, v245 op_sel_hi:[0,0,0]
	v_mfma_scale_f32_16x16x128_f8f6f4 v[84:87], v[4:11], v[186:193], v[84:87], v245, v245 op_sel_hi:[0,0,0]
	v_mfma_scale_f32_16x16x128_f8f6f4 v[72:75], v[12:19], v[208:215], v[72:75], v245, v245 op_sel_hi:[0,0,0]
	v_mfma_scale_f32_16x16x128_f8f6f4 v[68:71], v[4:11], v[208:215], v[68:71], v245, v245 op_sel_hi:[0,0,0]
	v_mfma_scale_f32_16x16x128_f8f6f4 v[56:59], v[12:19], v[216:223], v[56:59], v245, v245 op_sel_hi:[0,0,0]
	v_mfma_scale_f32_16x16x128_f8f6f4 v[52:55], v[4:11], v[216:223], v[52:55], v245, v245 op_sel_hi:[0,0,0]
	v_mfma_scale_f32_16x16x128_f8f6f4 v[40:43], v[12:19], v[228:235], v[40:43], v245, v245 op_sel_hi:[0,0,0]
	v_mfma_scale_f32_16x16x128_f8f6f4 v[36:39], v[4:11], v[228:235], v[36:39], v245, v245 op_sel_hi:[0,0,0]
	s_setprio 0
	s_barrier
	s_add_i32 s60, 0, 0x18000
	s_add_i32 s61, 0, 0x1c000
	v_add_u32_e32 v16, s60, v183
	v_add_u32_e32 v32, s61, v183
	ds_read_b128 v[4:7], v16
	ds_read_b128 v[8:11], v16 offset:1024
	ds_read_b128 v[12:15], v16 offset:2048
	ds_read_b128 v[16:19], v16 offset:3072
	ds_read_b128 v[20:23], v32
	ds_read_b128 v[24:27], v32 offset:1024
	ds_read_b128 v[28:31], v32 offset:2048
	ds_read_b128 v[32:35], v32 offset:3072
	s_mov_b32 m0, s20
	v_lshl_add_u64 v[194:195], v[194:195], 0, s[24:25]
	ds_read_b128 v[186:189], v184 offset:32768
	ds_read_b128 v[190:193], v184 offset:33792
	ds_read_b128 v[208:211], v184 offset:34816
	ds_read_b128 v[212:215], v184 offset:35840
	ds_read_b128 v[216:219], v184 offset:36864
	ds_read_b128 v[220:223], v184 offset:37888
	ds_read_b128 v[228:231], v184 offset:38912
	ds_read_b128 v[232:235], v184 offset:39936
	global_load_lds_dwordx4 v[194:195], off
	v_lshl_add_u64 v[194:195], v[204:205], 0, s[24:25]
	s_mov_b32 m0, s21
	s_nop 0
	global_load_lds_dwordx4 v[194:195], off
	s_waitcnt vmcnt(8)
	s_waitcnt lgkmcnt(0)
	s_barrier
	s_setprio 1
	s_waitcnt lgkmcnt(0)
	v_mfma_scale_f32_16x16x128_f8f6f4 v[160:163], v[4:11], v[186:193], v[160:163], v245, v245 op_sel_hi:[0,0,0]
	v_mfma_scale_f32_16x16x128_f8f6f4 v[156:159], v[12:19], v[186:193], v[156:159], v245, v245 op_sel_hi:[0,0,0]
	v_mfma_scale_f32_16x16x128_f8f6f4 v[144:147], v[4:11], v[208:215], v[144:147], v245, v245 op_sel_hi:[0,0,0]
	v_mfma_scale_f32_16x16x128_f8f6f4 v[140:143], v[12:19], v[208:215], v[140:143], v245, v245 op_sel_hi:[0,0,0]
	v_mfma_scale_f32_16x16x128_f8f6f4 v[128:131], v[4:11], v[216:223], v[128:131], v245, v245 op_sel_hi:[0,0,0]
	v_mfma_scale_f32_16x16x128_f8f6f4 v[124:127], v[12:19], v[216:223], v[124:127], v245, v245 op_sel_hi:[0,0,0]
	v_mfma_scale_f32_16x16x128_f8f6f4 v[112:115], v[4:11], v[228:235], v[112:115], v245, v245 op_sel_hi:[0,0,0]
	v_mfma_scale_f32_16x16x128_f8f6f4 v[108:111], v[12:19], v[228:235], v[108:111], v245, v245 op_sel_hi:[0,0,0]
	s_setprio 0
	s_setprio 1
	v_mfma_scale_f32_16x16x128_f8f6f4 v[152:155], v[20:27], v[186:193], v[152:155], v245, v245 op_sel_hi:[0,0,0]
	v_mfma_scale_f32_16x16x128_f8f6f4 v[148:151], v[28:35], v[186:193], v[148:151], v245, v245 op_sel_hi:[0,0,0]
	v_mfma_scale_f32_16x16x128_f8f6f4 v[136:139], v[20:27], v[208:215], v[136:139], v245, v245 op_sel_hi:[0,0,0]
	v_mfma_scale_f32_16x16x128_f8f6f4 v[132:135], v[28:35], v[208:215], v[132:135], v245, v245 op_sel_hi:[0,0,0]
	v_mfma_scale_f32_16x16x128_f8f6f4 v[120:123], v[20:27], v[216:223], v[120:123], v245, v245 op_sel_hi:[0,0,0]
	v_mfma_scale_f32_16x16x128_f8f6f4 v[116:119], v[28:35], v[216:223], v[116:119], v245, v245 op_sel_hi:[0,0,0]
	v_mfma_scale_f32_16x16x128_f8f6f4 v[104:107], v[20:27], v[228:235], v[104:107], v245, v245 op_sel_hi:[0,0,0]
	v_mfma_scale_f32_16x16x128_f8f6f4 v[100:103], v[28:35], v[228:235], v[100:103], v245, v245 op_sel_hi:[0,0,0]
	s_setprio 0
	s_barrier
; #define PG8_STAGE(bufoff, gbase, voff) do { _Pragma("unroll") for (int _i = 0; _i < 2; ++_i) \
;         __builtin_amdgcn_global_load_lds((const unsigned*)((const char*)(gbase) + (voff)[_i]), (PG8_LAS unsigned*)(lds + (bufoff) + ldsw + _i * 8192), 16, 0, 0); } while (0)
; #define PG8_WAIT_V(n) asm volatile("s_waitcnt vmcnt(" #n ")" ::: "memory")
; #define PG8_WAIT_L(n) asm volatile("s_waitcnt lgkmcnt(" #n ")" ::: "memory")
; #define PG8_BAR __builtin_amdgcn_s_barrier()
; template <class Epi, class Sched, bool ALIGN_EPI = false, bool SP2 = false, bool FP8 = false, bool ABLK = false>
; __device__ __forceinline__ void gemm_phase(PG8_LAS unsigned char* lds, const Gemm g, const Sched& S, const Epi& E) {
;     ...
;         for (int t = 0; t < nt; t += 2) {
;             const bool last = (t == nt - 2);
;             const char* a1 = cA + (size_t)(t + 1) * kstepA;
;             const char* a2 = last ? nA : cA + (size_t)(t + 2) * kstepA; const char* b2 = last ? nB : cB + (size_t)(t + 2) * kstep;
;             const char* a3 = a2 + kstepA; const char* b3 = b2 + kstep;
;             if (last && has_next) S.a_ready(nxt);
;             if constexpr (SP2) {
;             PG8_LDB(B0, 0, 0); PG8_LDB(B1, 0, 1); PG8_SCHED; PG8_LDA(At, 0, 0); PG8_STAGE(PG8_SA(1, 1), a1 + hstepA, voffA);
;             PG8_WAIT_V8_UNLESS_FIRST(t); PG8_WAIT_L(0); PG8_BAR; PG8_MMA(0, 0, At, B0); PG8_MMA(0, 1, At, B1); PG8_BAR; PG8_SCHED;
;             PG8_LDA(At, 0, 1); PG8_STAGE(PG8_SB(0, 0), b2, voffB); PG8_STAGE(PG8_SB(0, 1), b2 + hstep, voffB); PG8_STAGE(PG8_SA(0, 0), a2, voffA);
;             PG8_WAIT_V8_UNLESS_FIRST(t); PG8_WAIT_L(0); PG8_BAR; PG8_MMA(1, 0, At, B0); PG8_MMA(1, 1, At, B1); PG8_BAR; PG8_SCHED;
;             PG8_LDB(B0, 1, 0); PG8_LDB(B1, 1, 1); PG8_SCHED; PG8_LDA(At, 1, 0); PG8_STAGE(PG8_SA(0, 1), a2 + hstepA, voffA);
;             PG8_WAIT_V(8); PG8_WAIT_L(0); PG8_BAR; PG8_MMA(0, 0, At, B0); PG8_MMA(0, 1, At, B1); PG8_BAR; PG8_SCHED;
;             PG8_LDA(At, 1, 1); PG8_STAGE(PG8_SB(1, 0), b3, voffB); PG8_STAGE(PG8_SB(1, 1), b3 + hstep, voffB); PG8_STAGE(PG8_SA(1, 0), a3, voffA);
;             PG8_WAIT_V(8); PG8_WAIT_L(0); PG8_BAR; PG8_MMA(1, 0, At, B0); PG8_MMA(1, 1, At, B1); PG8_BAR; PG8_SCHED;
;     ...
;         if constexpr (SP2) PG8_WAIT_V(0);
;         if constexpr (FP8) asm volatile("s_nop 15\n\ts_nop 15" ::: "memory");
;         if constexpr (ALIGN_EPI) { if (wr == 0) PG8_BAR; }
	s_add_i32 s60, s60, s17
	v_lshl_add_u64 v[178:179], v[178:179], 0, s[34:35]
	s_mov_b32 m0, s60
	ds_read_b128 v[186:189], v184 offset:49152
	ds_read_b128 v[190:193], v184 offset:50176
	ds_read_b128 v[208:211], v184 offset:51200
	ds_read_b128 v[212:215], v184 offset:52224
	ds_read_b128 v[216:219], v184 offset:53248
	ds_read_b128 v[220:223], v184 offset:54272
	ds_read_b128 v[228:231], v184 offset:55296
	ds_read_b128 v[232:235], v184 offset:56320
	global_load_lds_dwordx4 v[178:179], off
	s_add_i32 m0, s60, 0x2000
	s_add_u32 s58, s58, 0x58080
	v_lshl_add_u64 v[178:179], v[180:181], 0, s[34:35]
	s_addc_u32 s59, s59, 0
	s_add_i32 s60, s61, s17
	global_load_lds_dwordx4 v[178:179], off
	s_mov_b32 m0, s60
	s_nop 0
	global_load_lds_dwordx4 v2, s[58:59]
	s_add_i32 m0, s60, 0x2000
	s_nop 0
	global_load_lds_dwordx4 v164, s[58:59]
	s_mov_b32 m0, s63
	s_nop 0
	global_load_lds_dwordx4 v168, s[56:57]
	s_mov_b32 m0, s64
	s_nop 0
	global_load_lds_dwordx4 v166, s[56:57]
	s_waitcnt vmcnt(8)
	s_waitcnt lgkmcnt(0)
	s_barrier
	s_setprio 1
	s_waitcnt lgkmcnt(0)
	v_mfma_scale_f32_16x16x128_f8f6f4 v[96:99], v[4:11], v[186:193], v[96:99], v245, v245 op_sel_hi:[0,0,0]
	v_mfma_scale_f32_16x16x128_f8f6f4 v[92:95], v[12:19], v[186:193], v[92:95], v245, v245 op_sel_hi:[0,0,0]
	v_mfma_scale_f32_16x16x128_f8f6f4 v[80:83], v[4:11], v[208:215], v[80:83], v245, v245 op_sel_hi:[0,0,0]
	v_mfma_scale_f32_16x16x128_f8f6f4 v[76:79], v[12:19], v[208:215], v[76:79], v245, v245 op_sel_hi:[0,0,0]
	v_mfma_scale_f32_16x16x128_f8f6f4 v[64:67], v[4:11], v[216:223], v[64:67], v245, v245 op_sel_hi:[0,0,0]
	v_mfma_scale_f32_16x16x128_f8f6f4 v[60:63], v[12:19], v[216:223], v[60:63], v245, v245 op_sel_hi:[0,0,0]
	v_mfma_scale_f32_16x16x128_f8f6f4 v[48:51], v[4:11], v[228:235], v[48:51], v245, v245 op_sel_hi:[0,0,0]
	v_mfma_scale_f32_16x16x128_f8f6f4 v[44:47], v[12:19], v[228:235], v[44:47], v245, v245 op_sel_hi:[0,0,0]
	s_setprio 0
	s_setprio 1
	v_mfma_scale_f32_16x16x128_f8f6f4 v[88:91], v[20:27], v[186:193], v[88:91], v245, v245 op_sel_hi:[0,0,0]
	v_mfma_scale_f32_16x16x128_f8f6f4 v[84:87], v[28:35], v[186:193], v[84:87], v245, v245 op_sel_hi:[0,0,0]
	v_mfma_scale_f32_16x16x128_f8f6f4 v[72:75], v[20:27], v[208:215], v[72:75], v245, v245 op_sel_hi:[0,0,0]
	v_mfma_scale_f32_16x16x128_f8f6f4 v[68:71], v[28:35], v[208:215], v[68:71], v245, v245 op_sel_hi:[0,0,0]
	v_mfma_scale_f32_16x16x128_f8f6f4 v[56:59], v[20:27], v[216:223], v[56:59], v245, v245 op_sel_hi:[0,0,0]
	v_mfma_scale_f32_16x16x128_f8f6f4 v[52:55], v[28:35], v[216:223], v[52:55], v245, v245 op_sel_hi:[0,0,0]
	v_mfma_scale_f32_16x16x128_f8f6f4 v[40:43], v[20:27], v[228:235], v[40:43], v245, v245 op_sel_hi:[0,0,0]
	v_mfma_scale_f32_16x16x128_f8f6f4 v[36:39], v[28:35], v[228:235], v[36:39], v245, v245 op_sel_hi:[0,0,0]
	s_setprio 0
	s_add_u32 s4, s4, 0x100
	s_addc_u32 s5, s5, 0
	s_add_u32 s54, s54, 0x10000
	s_addc_u32 s55, s55, 0
	s_cmp_gt_u32 s70, 19
	s_cbranch_scc1 .Lrot9_exit
	s_add_i32 s70, s70, 2
	s_add_u32 s56, s52, s54
	s_addc_u32 s57, s53, s55
	s_add_u32 s56, s56, 0x10000
	s_addc_u32 s57, s57, 0
	s_cmp_eq_u32 s54, 0xa0000
	s_cselect_b32 s60, s40, s56
	s_cselect_b32 s61, s41, s57
	s_cselect_b32 s58, s50, s4
	s_cselect_b32 s59, s51, s5
	s_add_u32 s56, s60, 0x8000
	s_addc_u32 s57, s61, 0
	s_add_i32 s72, 0, 0x10000
	s_add_i32 s71, 0, 0x14000
	v_add_u32_e32 v4, s72, v183
	v_add_u32_e32 v8, s71, v183
	s_barrier
	s_branch .Lrot9_body
.Lrot9_exit:
	s_barrier
	s_waitcnt vmcnt(0)
	s_nop 15
	s_nop 15
	s_and_b64 vcc, exec, s[48:49]
	s_cbranch_vccz .LBB0_1834
	s_barrier
